# speedup vs baseline: 1.0109x; 1.0046x over previous
.LBB6_11:
	v_lshlrev_b32_e32 v2, 12, v2
	s_lshl_b32 s48, s65, 6
	v_lshlrev_b32_e32 v6, 12, v6
	v_and_b32_e32 v2, 0xffffe000, v2
	s_lshl_b32 s17, s66, 13
	s_and_b32 s48, s48, 0x3000
	v_and_b32_e32 v6, 0xffffe000, v6
	v_lshl_add_u32 v2, v3, 9, v2
	v_and_b32_e32 v10, 48, v210
	v_lshlrev_b32_e32 v11, 6, v210
	v_lshl_add_u32 v6, v7, 9, v6
	s_add_u32 s46, s26, s46
	v_or_b32_e32 v2, v2, v4
	v_and_or_b32 v10, v11, s58, v10
	v_lshlrev_b32_e32 v11, 2, v210
	v_or_b32_e32 v6, v6, v8
	s_addc_u32 s47, s27, s47
	v_add_u32_sdwa v2, v2, sext(v5) dst_sel:DWORD dst_unused:UNUSED_PAD src0_sel:DWORD src1_sel:WORD_0
	v_and_b32_e32 v11, 32, v11
	v_add_u32_sdwa v6, v6, sext(v9) dst_sel:DWORD dst_unused:UNUSED_PAD src0_sel:DWORD src1_sel:WORD_0
	v_ashrrev_i32_e32 v3, 31, v2
	s_add_u32 s44, s24, s44
	v_xad_u32 v168, v10, v11, 0
	s_waitcnt vmcnt(6)
	v_ashrrev_i32_e32 v7, 31, v6
	v_lshlrev_b64 v[2:3], 1, v[2:3]
	s_addc_u32 s45, s25, s45
	v_add_u32_e32 v10, s48, v168
	v_lshlrev_b64 v[6:7], 1, v[6:7]
	v_lshl_add_u64 v[136:137], s[46:47], 0, v[2:3]
	v_lshl_add_u64 v[140:141], s[44:45], 0, v[2:3]
	v_mov_b32_e32 v2, 0
	v_add_u32_e32 v169, 0x10000, v10
	v_add_u32_e32 v170, 0x10400, v10
	v_add_u32_e32 v171, 0x10800, v10
	v_add_u32_e32 v172, 0x10c00, v10
	v_add_u32_e32 v161, 0x14000, v10
	v_add_u32_e32 v162, 0x14400, v10
	v_add_u32_e32 v163, 0x14800, v10
	v_add_u32_e32 v164, 0x14c00, v10
	v_add_u32_e32 v148, 0x18000, v10
	v_add_u32_e32 v149, 0x18400, v10
	v_add_u32_e32 v150, 0x18800, v10
	v_add_u32_e32 v151, 0x18c00, v10
	v_add_u32_e32 v142, 0x1c000, v10
	v_add_u32_e32 v143, 0x1c400, v10
	v_add_u32_e32 v144, 0x1c800, v10
	v_add_u32_e32 v145, 0x1cc00, v10
	v_lshl_add_u64 v[134:135], s[46:47], 0, v[6:7]
	v_lshl_add_u64 v[138:139], s[44:45], 0, v[6:7]
	s_mov_b32 s46, -2
	s_mov_b64 s[44:45], 0
	v_mov_b32_e32 v3, v2
	v_mov_b32_e32 v4, v2
	v_mov_b32_e32 v5, v2
	v_mov_b32_e32 v6, v2
	v_mov_b32_e32 v7, v2
	v_mov_b32_e32 v8, v2
	v_mov_b32_e32 v9, v2
	v_mov_b32_e32 v10, v2
	v_mov_b32_e32 v11, v2
	v_mov_b32_e32 v12, v2
	v_mov_b32_e32 v13, v2
	v_mov_b32_e32 v18, v2
	v_mov_b32_e32 v19, v2
	v_mov_b32_e32 v20, v2
	v_mov_b32_e32 v21, v2
	v_mov_b32_e32 v30, v2
	v_mov_b32_e32 v31, v2
	v_mov_b32_e32 v32, v2
	v_mov_b32_e32 v33, v2
	v_mov_b32_e32 v42, v2
	v_mov_b32_e32 v43, v2
	v_mov_b32_e32 v44, v2
	v_mov_b32_e32 v45, v2
	v_mov_b32_e32 v54, v2
	v_mov_b32_e32 v55, v2
	v_mov_b32_e32 v56, v2
	v_mov_b32_e32 v57, v2
	v_mov_b32_e32 v66, v2
	v_mov_b32_e32 v67, v2
	v_mov_b32_e32 v68, v2
	v_mov_b32_e32 v69, v2
	v_mov_b32_e32 v14, v2
	v_mov_b32_e32 v15, v2
	v_mov_b32_e32 v16, v2
	v_mov_b32_e32 v17, v2
	v_mov_b32_e32 v22, v2
	v_mov_b32_e32 v23, v2
	v_mov_b32_e32 v24, v2
	v_mov_b32_e32 v25, v2
	v_mov_b32_e32 v34, v2
	v_mov_b32_e32 v35, v2
	v_mov_b32_e32 v36, v2
	v_mov_b32_e32 v37, v2
	v_mov_b32_e32 v46, v2
	v_mov_b32_e32 v47, v2
	v_mov_b32_e32 v48, v2
	v_mov_b32_e32 v49, v2
	v_mov_b32_e32 v58, v2
	v_mov_b32_e32 v59, v2
	v_mov_b32_e32 v60, v2
	v_mov_b32_e32 v61, v2
	v_mov_b32_e32 v70, v2
	v_mov_b32_e32 v71, v2
	v_mov_b32_e32 v72, v2
	v_mov_b32_e32 v73, v2
	v_mov_b32_e32 v78, v2
	v_mov_b32_e32 v79, v2
	v_mov_b32_e32 v80, v2
	v_mov_b32_e32 v81, v2
	v_mov_b32_e32 v86, v2
	v_mov_b32_e32 v87, v2
	v_mov_b32_e32 v88, v2
	v_mov_b32_e32 v89, v2
	v_mov_b32_e32 v26, v2
	v_mov_b32_e32 v27, v2
	v_mov_b32_e32 v28, v2
	v_mov_b32_e32 v29, v2
	v_mov_b32_e32 v38, v2
	v_mov_b32_e32 v39, v2
	v_mov_b32_e32 v40, v2
	v_mov_b32_e32 v41, v2
	v_mov_b32_e32 v50, v2
	v_mov_b32_e32 v51, v2
	v_mov_b32_e32 v52, v2
	v_mov_b32_e32 v53, v2
	v_mov_b32_e32 v62, v2
	v_mov_b32_e32 v63, v2
	v_mov_b32_e32 v64, v2
	v_mov_b32_e32 v65, v2
	v_mov_b32_e32 v74, v2
	v_mov_b32_e32 v75, v2
	v_mov_b32_e32 v76, v2
	v_mov_b32_e32 v77, v2
	v_mov_b32_e32 v82, v2
	v_mov_b32_e32 v83, v2
	v_mov_b32_e32 v84, v2
	v_mov_b32_e32 v85, v2
	v_mov_b32_e32 v90, v2
	v_mov_b32_e32 v91, v2
	v_mov_b32_e32 v92, v2
	v_mov_b32_e32 v93, v2
	v_mov_b32_e32 v94, v2
	v_mov_b32_e32 v95, v2
	v_mov_b32_e32 v96, v2
	v_mov_b32_e32 v97, v2
	v_mov_b32_e32 v98, v2
	v_mov_b32_e32 v99, v2
	v_mov_b32_e32 v100, v2
	v_mov_b32_e32 v101, v2
	v_mov_b32_e32 v102, v2
	v_mov_b32_e32 v103, v2
	v_mov_b32_e32 v104, v2
	v_mov_b32_e32 v105, v2
	v_mov_b32_e32 v106, v2
	v_mov_b32_e32 v107, v2
	v_mov_b32_e32 v108, v2
	v_mov_b32_e32 v109, v2
	v_mov_b32_e32 v110, v2
	v_mov_b32_e32 v111, v2
	v_mov_b32_e32 v112, v2
	v_mov_b32_e32 v113, v2
	v_mov_b32_e32 v114, v2
	v_mov_b32_e32 v115, v2
	v_mov_b32_e32 v116, v2
	v_mov_b32_e32 v117, v2
	v_mov_b32_e32 v118, v2
	v_mov_b32_e32 v119, v2
	v_mov_b32_e32 v120, v2
	v_mov_b32_e32 v121, v2
	v_mov_b32_e32 v122, v2
	v_mov_b32_e32 v123, v2
	v_mov_b32_e32 v124, v2
	v_mov_b32_e32 v125, v2
	v_mov_b32_e32 v126, v2
	v_mov_b32_e32 v127, v2
	v_mov_b32_e32 v128, v2
	v_mov_b32_e32 v129, v2
	v_add_u32_e32 v174, 0xc000, v152
	v_add_u32_e32 v175, 0xe000, v152
	s_nop 0
	v_readfirstlane_b32 s72, v174
	v_readfirstlane_b32 s73, v175
	v_readfirstlane_b32 s74, v146
	v_readfirstlane_b32 s75, v147
	v_readfirstlane_b32 s76, v152
	v_readfirstlane_b32 s77, v153
	v_readfirstlane_b32 s78, v154
	v_readfirstlane_b32 s79, v155
	v_readfirstlane_b32 s80, v156
	v_readfirstlane_b32 s81, v157
	v_readfirstlane_b32 s82, v158
	v_readfirstlane_b32 s83, v159
	v_readfirstlane_b32 s84, v160
	v_readfirstlane_b32 s85, v165
	v_readfirstlane_b32 s86, v166
	v_readfirstlane_b32 s87, v167
	s_barrier
	s_barrier
.LBB6_12:
	ds_read_b128 v[176:179], v169
	ds_read_b128 v[180:183], v170
	ds_read_b128 v[184:187], v171
	ds_read_b128 v[188:191], v172
	v_add_u32_e32 v174, 0xc000, v152
	v_lshl_add_u64 v[192:193], v[136:137], 0, s[44:45]
	v_add_u32_e32 v175, 0xe000, v152
	v_add_u32_e32 v173, s17, v168
	v_lshl_add_u64 v[232:233], v[192:193], 0, s[30:31]
	s_mov_b32 m0, s72
	v_lshl_add_u64 v[248:249], v[134:135], 0, s[44:45]
	ds_read_b128 v[196:199], v173
	ds_read_b128 v[200:203], v173 offset:1024
	ds_read_b128 v[204:207], v173 offset:2048
	ds_read_b128 v[212:215], v173 offset:3072
	ds_read_b128 v[216:219], v173 offset:4096
	ds_read_b128 v[220:223], v173 offset:5120
	ds_read_b128 v[224:227], v173 offset:6144
	ds_read_b128 v[228:231], v173 offset:7168
	global_load_lds_dwordx4 v[232:233], off
	v_lshl_add_u64 v[232:233], v[248:249], 0, s[30:31]
	s_mov_b32 m0, s73
	s_nop 0
	global_load_lds_dwordx4 v[232:233], off
	s_waitcnt lgkmcnt(8)
	s_barrier
	s_waitcnt lgkmcnt(0)
	v_mfma_f32_16x16x32_f16 v[2:5], v[196:199], v[176:179], v[2:5]
	v_mfma_f32_16x16x32_f16 v[6:9], v[196:199], v[184:187], v[6:9]
	v_mfma_f32_16x16x32_f16 v[10:13], v[204:207], v[176:179], v[10:13]
	v_mfma_f32_16x16x32_f16 v[18:21], v[204:207], v[184:187], v[18:21]
	v_mfma_f32_16x16x32_f16 v[30:33], v[216:219], v[176:179], v[30:33]
	v_mfma_f32_16x16x32_f16 v[42:45], v[216:219], v[184:187], v[42:45]
	v_mfma_f32_16x16x32_f16 v[54:57], v[224:227], v[176:179], v[54:57]
	v_mfma_f32_16x16x32_f16 v[66:69], v[224:227], v[184:187], v[66:69]
	v_mfma_f32_16x16x32_f16 v[2:5], v[200:203], v[180:183], v[2:5]
	v_mfma_f32_16x16x32_f16 v[6:9], v[200:203], v[188:191], v[6:9]
	v_mfma_f32_16x16x32_f16 v[10:13], v[212:215], v[180:183], v[10:13]
	v_mfma_f32_16x16x32_f16 v[18:21], v[212:215], v[188:191], v[18:21]
	v_mfma_f32_16x16x32_f16 v[30:33], v[220:223], v[180:183], v[30:33]
	v_mfma_f32_16x16x32_f16 v[42:45], v[220:223], v[188:191], v[42:45]
	v_mfma_f32_16x16x32_f16 v[54:57], v[228:231], v[180:183], v[54:57]
	v_mfma_f32_16x16x32_f16 v[66:69], v[228:231], v[188:191], v[66:69]
	s_barrier
	v_lshl_add_u64 v[250:251], v[140:141], 0, s[44:45]
	v_lshl_add_u64 v[252:253], v[250:251], 0, s[34:35]
	s_mov_b32 m0, s74
	ds_read_b128 v[232:235], v161
	ds_read_b128 v[236:239], v162
	ds_read_b128 v[240:243], v163
	ds_read_b128 v[244:247], v164
	global_load_lds_dwordx4 v[252:253], off
	v_lshl_add_u64 v[252:253], v[138:139], 0, s[44:45]
	v_lshl_add_u64 v[254:255], v[252:253], 0, s[34:35]
	s_mov_b32 m0, s75
	s_nop 0
	global_load_lds_dwordx4 v[254:255], off
	s_barrier
	s_waitcnt lgkmcnt(0)
	v_mfma_f32_16x16x32_f16 v[14:17], v[196:199], v[232:235], v[14:17]
	v_mfma_f32_16x16x32_f16 v[22:25], v[196:199], v[240:243], v[22:25]
	v_mfma_f32_16x16x32_f16 v[34:37], v[204:207], v[232:235], v[34:37]
	v_mfma_f32_16x16x32_f16 v[46:49], v[204:207], v[240:243], v[46:49]
	v_mfma_f32_16x16x32_f16 v[58:61], v[216:219], v[232:235], v[58:61]
	v_mfma_f32_16x16x32_f16 v[70:73], v[216:219], v[240:243], v[70:73]
	v_mfma_f32_16x16x32_f16 v[78:81], v[224:227], v[232:235], v[78:81]
	v_mfma_f32_16x16x32_f16 v[86:89], v[224:227], v[240:243], v[86:89]
	v_mfma_f32_16x16x32_f16 v[14:17], v[200:203], v[236:239], v[14:17]
	v_mfma_f32_16x16x32_f16 v[22:25], v[200:203], v[244:247], v[22:25]
	v_mfma_f32_16x16x32_f16 v[34:37], v[212:215], v[236:239], v[34:37]
	v_mfma_f32_16x16x32_f16 v[46:49], v[212:215], v[244:247], v[46:49]
	v_mfma_f32_16x16x32_f16 v[58:61], v[220:223], v[236:239], v[58:61]
	v_mfma_f32_16x16x32_f16 v[70:73], v[220:223], v[244:247], v[70:73]
	v_mfma_f32_16x16x32_f16 v[78:81], v[228:231], v[236:239], v[78:81]
	v_mfma_f32_16x16x32_f16 v[86:89], v[228:231], v[244:247], v[86:89]
	v_lshl_add_u64 v[254:255], v[192:193], 0, s[34:35]
	s_mov_b32 m0, s76
	s_barrier
	ds_read_b128 v[196:199], v173 offset:16384
	ds_read_b128 v[200:203], v173 offset:17408
	ds_read_b128 v[204:207], v173 offset:18432
	ds_read_b128 v[212:215], v173 offset:19456
	ds_read_b128 v[216:219], v173 offset:20480
	ds_read_b128 v[220:223], v173 offset:21504
	ds_read_b128 v[224:227], v173 offset:22528
	ds_read_b128 v[228:231], v173 offset:23552
	global_load_lds_dwordx4 v[254:255], off
	v_lshl_add_u64 v[254:255], v[248:249], 0, s[34:35]
	s_mov_b32 m0, s77
	s_nop 0
	global_load_lds_dwordx4 v[254:255], off
	s_barrier
	s_waitcnt lgkmcnt(0)
	v_mfma_f32_16x16x32_f16 v[26:29], v[196:199], v[176:179], v[26:29]
	v_mfma_f32_16x16x32_f16 v[38:41], v[196:199], v[184:187], v[38:41]
	v_mfma_f32_16x16x32_f16 v[50:53], v[204:207], v[176:179], v[50:53]
	v_mfma_f32_16x16x32_f16 v[62:65], v[204:207], v[184:187], v[62:65]
	v_mfma_f32_16x16x32_f16 v[74:77], v[216:219], v[176:179], v[74:77]
	v_mfma_f32_16x16x32_f16 v[82:85], v[216:219], v[184:187], v[82:85]
	v_mfma_f32_16x16x32_f16 v[90:93], v[224:227], v[176:179], v[90:93]
	v_mfma_f32_16x16x32_f16 v[94:97], v[224:227], v[184:187], v[94:97]
	v_mfma_f32_16x16x32_f16 v[26:29], v[200:203], v[180:183], v[26:29]
	v_mfma_f32_16x16x32_f16 v[38:41], v[200:203], v[188:191], v[38:41]
	v_mfma_f32_16x16x32_f16 v[50:53], v[212:215], v[180:183], v[50:53]
	v_mfma_f32_16x16x32_f16 v[62:65], v[212:215], v[188:191], v[62:65]
	v_mfma_f32_16x16x32_f16 v[74:77], v[220:223], v[180:183], v[74:77]
	v_mfma_f32_16x16x32_f16 v[82:85], v[220:223], v[188:191], v[82:85]
	v_mfma_f32_16x16x32_f16 v[90:93], v[228:231], v[180:183], v[90:93]
	v_mfma_f32_16x16x32_f16 v[94:97], v[228:231], v[188:191], v[94:97]
	s_barrier
	v_lshl_add_u64 v[176:177], v[250:251], 0, s[36:37]
	s_mov_b32 m0, s78
	global_load_lds_dwordx4 v[176:177], off
	v_lshl_add_u64 v[176:177], v[252:253], 0, s[36:37]
	s_mov_b32 m0, s79
	s_nop 0
	global_load_lds_dwordx4 v[176:177], off
	s_waitcnt vmcnt(6)
	s_barrier
	v_mfma_f32_16x16x32_f16 v[98:101], v[196:199], v[232:235], v[98:101]
	v_mfma_f32_16x16x32_f16 v[102:105], v[196:199], v[240:243], v[102:105]
	v_mfma_f32_16x16x32_f16 v[106:109], v[204:207], v[232:235], v[106:109]
	v_mfma_f32_16x16x32_f16 v[110:113], v[204:207], v[240:243], v[110:113]
	v_mfma_f32_16x16x32_f16 v[114:117], v[216:219], v[232:235], v[114:117]
	v_mfma_f32_16x16x32_f16 v[118:121], v[216:219], v[240:243], v[118:121]
	v_mfma_f32_16x16x32_f16 v[122:125], v[224:227], v[232:235], v[122:125]
	v_mfma_f32_16x16x32_f16 v[126:129], v[224:227], v[240:243], v[126:129]
	v_mfma_f32_16x16x32_f16 v[98:101], v[200:203], v[236:239], v[98:101]
	v_mfma_f32_16x16x32_f16 v[102:105], v[200:203], v[244:247], v[102:105]
	v_mfma_f32_16x16x32_f16 v[106:109], v[212:215], v[236:239], v[106:109]
	v_mfma_f32_16x16x32_f16 v[110:113], v[212:215], v[244:247], v[110:113]
	v_mfma_f32_16x16x32_f16 v[114:117], v[220:223], v[236:239], v[114:117]
	v_mfma_f32_16x16x32_f16 v[118:121], v[220:223], v[244:247], v[118:121]
	v_mfma_f32_16x16x32_f16 v[122:125], v[228:231], v[236:239], v[122:125]
	v_mfma_f32_16x16x32_f16 v[126:129], v[228:231], v[244:247], v[126:129]
	s_barrier
	ds_read_b128 v[176:179], v148
	ds_read_b128 v[180:183], v149
	ds_read_b128 v[184:187], v150
	ds_read_b128 v[188:191], v151
	v_lshl_add_u64 v[232:233], v[192:193], 0, s[36:37]
	s_mov_b32 m0, s80
	ds_read_b128 v[196:199], v173 offset:32768
	ds_read_b128 v[200:203], v173 offset:33792
	ds_read_b128 v[204:207], v173 offset:34816
	ds_read_b128 v[212:215], v173 offset:35840
	ds_read_b128 v[216:219], v173 offset:36864
	ds_read_b128 v[220:223], v173 offset:37888
	ds_read_b128 v[224:227], v173 offset:38912
	ds_read_b128 v[228:231], v173 offset:39936
	global_load_lds_dwordx4 v[232:233], off
	v_lshl_add_u64 v[232:233], v[248:249], 0, s[36:37]
	s_mov_b32 m0, s81
	s_nop 0
	global_load_lds_dwordx4 v[232:233], off
	s_waitcnt lgkmcnt(8)
	s_barrier
	s_waitcnt lgkmcnt(0)
	v_mfma_f32_16x16x32_f16 v[2:5], v[196:199], v[176:179], v[2:5]
	v_mfma_f32_16x16x32_f16 v[6:9], v[196:199], v[184:187], v[6:9]
	v_mfma_f32_16x16x32_f16 v[10:13], v[204:207], v[176:179], v[10:13]
	v_mfma_f32_16x16x32_f16 v[18:21], v[204:207], v[184:187], v[18:21]
	v_mfma_f32_16x16x32_f16 v[30:33], v[216:219], v[176:179], v[30:33]
	v_mfma_f32_16x16x32_f16 v[42:45], v[216:219], v[184:187], v[42:45]
	v_mfma_f32_16x16x32_f16 v[54:57], v[224:227], v[176:179], v[54:57]
	v_mfma_f32_16x16x32_f16 v[66:69], v[224:227], v[184:187], v[66:69]
	v_mfma_f32_16x16x32_f16 v[2:5], v[200:203], v[180:183], v[2:5]
	v_mfma_f32_16x16x32_f16 v[6:9], v[200:203], v[188:191], v[6:9]
	v_mfma_f32_16x16x32_f16 v[10:13], v[212:215], v[180:183], v[10:13]
	v_mfma_f32_16x16x32_f16 v[18:21], v[212:215], v[188:191], v[18:21]
	v_mfma_f32_16x16x32_f16 v[30:33], v[220:223], v[180:183], v[30:33]
	v_mfma_f32_16x16x32_f16 v[42:45], v[220:223], v[188:191], v[42:45]
	v_mfma_f32_16x16x32_f16 v[54:57], v[228:231], v[180:183], v[54:57]
	v_mfma_f32_16x16x32_f16 v[66:69], v[228:231], v[188:191], v[66:69]
	s_barrier
	v_lshl_add_u64 v[254:255], v[250:251], 0, s[38:39]
	s_mov_b32 m0, s82
	ds_read_b128 v[232:235], v142
	ds_read_b128 v[236:239], v143
	ds_read_b128 v[240:243], v144
	ds_read_b128 v[244:247], v145
	global_load_lds_dwordx4 v[254:255], off
	v_lshl_add_u64 v[254:255], v[252:253], 0, s[38:39]
	s_mov_b32 m0, s83
	s_nop 0
	global_load_lds_dwordx4 v[254:255], off
	s_barrier
	s_waitcnt lgkmcnt(0)
	v_mfma_f32_16x16x32_f16 v[14:17], v[196:199], v[232:235], v[14:17]
	v_mfma_f32_16x16x32_f16 v[22:25], v[196:199], v[240:243], v[22:25]
	v_mfma_f32_16x16x32_f16 v[34:37], v[204:207], v[232:235], v[34:37]
	v_mfma_f32_16x16x32_f16 v[46:49], v[204:207], v[240:243], v[46:49]
	v_mfma_f32_16x16x32_f16 v[58:61], v[216:219], v[232:235], v[58:61]
	v_mfma_f32_16x16x32_f16 v[70:73], v[216:219], v[240:243], v[70:73]
	v_mfma_f32_16x16x32_f16 v[78:81], v[224:227], v[232:235], v[78:81]
	v_mfma_f32_16x16x32_f16 v[86:89], v[224:227], v[240:243], v[86:89]
	v_mfma_f32_16x16x32_f16 v[14:17], v[200:203], v[236:239], v[14:17]
	v_mfma_f32_16x16x32_f16 v[22:25], v[200:203], v[244:247], v[22:25]
	v_mfma_f32_16x16x32_f16 v[34:37], v[212:215], v[236:239], v[34:37]
	v_mfma_f32_16x16x32_f16 v[46:49], v[212:215], v[244:247], v[46:49]
	v_mfma_f32_16x16x32_f16 v[58:61], v[220:223], v[236:239], v[58:61]
	v_mfma_f32_16x16x32_f16 v[70:73], v[220:223], v[244:247], v[70:73]
	v_mfma_f32_16x16x32_f16 v[78:81], v[228:231], v[236:239], v[78:81]
	v_mfma_f32_16x16x32_f16 v[86:89], v[228:231], v[244:247], v[86:89]
	v_lshl_add_u64 v[192:193], v[192:193], 0, s[38:39]
	s_mov_b32 m0, s84
	s_barrier
	ds_read_b128 v[196:199], v173 offset:49152
	ds_read_b128 v[200:203], v173 offset:50176
	ds_read_b128 v[204:207], v173 offset:51200
	ds_read_b128 v[212:215], v173 offset:52224
	ds_read_b128 v[216:219], v173 offset:53248
	ds_read_b128 v[220:223], v173 offset:54272
	ds_read_b128 v[224:227], v173 offset:55296
	ds_read_b128 v[228:231], v173 offset:56320
	global_load_lds_dwordx4 v[192:193], off
	v_lshl_add_u64 v[192:193], v[248:249], 0, s[38:39]
	s_mov_b32 m0, s85
	s_nop 0
	global_load_lds_dwordx4 v[192:193], off
	s_barrier
	s_waitcnt lgkmcnt(0)
	v_mfma_f32_16x16x32_f16 v[26:29], v[196:199], v[176:179], v[26:29]
	v_mfma_f32_16x16x32_f16 v[38:41], v[196:199], v[184:187], v[38:41]
	v_mfma_f32_16x16x32_f16 v[50:53], v[204:207], v[176:179], v[50:53]
	v_mfma_f32_16x16x32_f16 v[62:65], v[204:207], v[184:187], v[62:65]
	v_mfma_f32_16x16x32_f16 v[74:77], v[216:219], v[176:179], v[74:77]
	v_mfma_f32_16x16x32_f16 v[82:85], v[216:219], v[184:187], v[82:85]
	v_mfma_f32_16x16x32_f16 v[90:93], v[224:227], v[176:179], v[90:93]
	v_mfma_f32_16x16x32_f16 v[94:97], v[224:227], v[184:187], v[94:97]
	v_mfma_f32_16x16x32_f16 v[26:29], v[200:203], v[180:183], v[26:29]
	v_mfma_f32_16x16x32_f16 v[38:41], v[200:203], v[188:191], v[38:41]
	v_mfma_f32_16x16x32_f16 v[50:53], v[212:215], v[180:183], v[50:53]
	v_mfma_f32_16x16x32_f16 v[62:65], v[212:215], v[188:191], v[62:65]
	v_mfma_f32_16x16x32_f16 v[74:77], v[220:223], v[180:183], v[74:77]
	v_mfma_f32_16x16x32_f16 v[82:85], v[220:223], v[188:191], v[82:85]
	v_mfma_f32_16x16x32_f16 v[90:93], v[228:231], v[180:183], v[90:93]
	v_mfma_f32_16x16x32_f16 v[94:97], v[228:231], v[188:191], v[94:97]
	s_barrier
	v_lshl_add_u64 v[176:177], v[250:251], 0, s[40:41]
	s_mov_b32 m0, s86
	global_load_lds_dwordx4 v[176:177], off
	v_lshl_add_u64 v[176:177], v[252:253], 0, s[40:41]
	s_mov_b32 m0, s87
	s_nop 0
	global_load_lds_dwordx4 v[176:177], off
	s_waitcnt vmcnt(6)
	s_barrier
	v_mfma_f32_16x16x32_f16 v[98:101], v[196:199], v[232:235], v[98:101]
	v_mfma_f32_16x16x32_f16 v[102:105], v[196:199], v[240:243], v[102:105]
	v_mfma_f32_16x16x32_f16 v[106:109], v[204:207], v[232:235], v[106:109]
	v_mfma_f32_16x16x32_f16 v[110:113], v[204:207], v[240:243], v[110:113]
	v_mfma_f32_16x16x32_f16 v[114:117], v[216:219], v[232:235], v[114:117]
	v_mfma_f32_16x16x32_f16 v[118:121], v[216:219], v[240:243], v[118:121]
	v_mfma_f32_16x16x32_f16 v[122:125], v[224:227], v[232:235], v[122:125]
	v_mfma_f32_16x16x32_f16 v[126:129], v[224:227], v[240:243], v[126:129]
	v_mfma_f32_16x16x32_f16 v[98:101], v[200:203], v[236:239], v[98:101]
	v_mfma_f32_16x16x32_f16 v[102:105], v[200:203], v[244:247], v[102:105]
	v_mfma_f32_16x16x32_f16 v[106:109], v[212:215], v[236:239], v[106:109]
	v_mfma_f32_16x16x32_f16 v[110:113], v[212:215], v[244:247], v[110:113]
	v_mfma_f32_16x16x32_f16 v[114:117], v[220:223], v[236:239], v[114:117]
	v_mfma_f32_16x16x32_f16 v[118:121], v[220:223], v[244:247], v[118:121]
	v_mfma_f32_16x16x32_f16 v[122:125], v[228:231], v[236:239], v[122:125]
	v_mfma_f32_16x16x32_f16 v[126:129], v[228:231], v[244:247], v[126:129]
	s_add_i32 s46, s46, 2
	s_add_u32 s44, s44, 0x100
	s_addc_u32 s45, s45, 0
	s_cmp_lt_u32 s46, 4
	s_barrier
	s_cbranch_scc1 .LBB6_12
	s_add_u32 s0, s0, 0x20380
	s_addc_u32 s1, s1, 0
	v_readfirstlane_b32 s17, v174
	v_lshl_add_u64 v[130:131], v[130:131], 1, s[0:1]
	s_mov_b32 m0, s17
	ds_read_b128 v[134:137], v169
	ds_read_b128 v[138:141], v170
	ds_read_b128 v[152:155], v171
	ds_read_b128 v[156:159], v172
	ds_read_b128 v[166:169], v173
	ds_read_b128 v[176:179], v173 offset:1024
	ds_read_b128 v[180:183], v173 offset:2048
	ds_read_b128 v[184:187], v173 offset:3072
	ds_read_b128 v[188:191], v173 offset:4096
	ds_read_b128 v[196:199], v173 offset:5120
	ds_read_b128 v[200:203], v173 offset:6144
	ds_read_b128 v[204:207], v173 offset:7168
	global_load_lds_dwordx4 v[130:131], off
	v_lshl_add_u64 v[130:131], v[132:133], 1, s[0:1]
	v_readfirstlane_b32 s0, v175
	s_mov_b32 m0, s0
	s_nop 0
	global_load_lds_dwordx4 v[130:131], off
	s_barrier
	s_waitcnt lgkmcnt(0)
	v_mfma_f32_16x16x32_f16 v[2:5], v[166:169], v[134:137], v[2:5]
	v_mfma_f32_16x16x32_f16 v[42:45], v[188:191], v[152:155], v[42:45]
	v_mfma_f32_16x16x32_f16 v[54:57], v[200:203], v[134:137], v[54:57]
	v_mfma_f32_16x16x32_f16 v[66:69], v[200:203], v[152:155], v[66:69]
	v_mfma_f32_16x16x32_f16 v[2:5], v[176:179], v[138:141], v[2:5]
	v_mfma_f32_16x16x32_f16 v[6:9], v[166:169], v[152:155], v[6:9]
	v_mfma_f32_16x16x32_f16 v[10:13], v[180:183], v[134:137], v[10:13]
	v_mfma_f32_16x16x32_f16 v[18:21], v[180:183], v[152:155], v[18:21]
	v_mfma_f32_16x16x32_f16 v[30:33], v[188:191], v[134:137], v[30:33]
	v_mfma_f32_16x16x32_f16 v[42:45], v[196:199], v[156:159], v[42:45]
	v_mfma_f32_16x16x32_f16 v[54:57], v[204:207], v[138:141], v[54:57]
	v_mfma_f32_16x16x32_f16 v[66:69], v[204:207], v[156:159], v[66:69]
	v_mfma_f32_16x16x32_f16 v[6:9], v[176:179], v[156:159], v[6:9]
	v_mfma_f32_16x16x32_f16 v[10:13], v[184:187], v[138:141], v[10:13]
	v_mfma_f32_16x16x32_f16 v[18:21], v[184:187], v[156:159], v[18:21]
	v_mfma_f32_16x16x32_f16 v[30:33], v[196:199], v[138:141], v[30:33]
	s_barrier
	ds_read_b128 v[130:133], v161
	ds_read_b128 v[212:215], v162
	ds_read_b128 v[160:163], v163
	ds_read_b128 v[216:219], v164
	s_barrier
	s_waitcnt lgkmcnt(0)
	v_mfma_f32_16x16x32_f16 v[14:17], v[166:169], v[130:133], v[14:17]
	v_mfma_f32_16x16x32_f16 v[78:81], v[200:203], v[130:133], v[78:81]
	v_mfma_f32_16x16x32_f16 v[14:17], v[176:179], v[212:215], v[14:17]
	v_mfma_f32_16x16x32_f16 v[22:25], v[166:169], v[160:163], v[22:25]
	v_mfma_f32_16x16x32_f16 v[34:37], v[180:183], v[130:133], v[34:37]
	v_mfma_f32_16x16x32_f16 v[46:49], v[180:183], v[160:163], v[46:49]
	v_mfma_f32_16x16x32_f16 v[58:61], v[188:191], v[130:133], v[58:61]
	v_mfma_f32_16x16x32_f16 v[70:73], v[188:191], v[160:163], v[70:73]
	v_mfma_f32_16x16x32_f16 v[164:167], v[204:207], v[212:215], v[78:81]
	v_mfma_f32_16x16x32_f16 v[78:81], v[200:203], v[160:163], v[86:89]
	v_mfma_f32_16x16x32_f16 v[22:25], v[176:179], v[216:219], v[22:25]
	v_mfma_f32_16x16x32_f16 v[34:37], v[184:187], v[212:215], v[34:37]
	v_mfma_f32_16x16x32_f16 v[46:49], v[184:187], v[216:219], v[46:49]
	v_mfma_f32_16x16x32_f16 v[58:61], v[196:199], v[212:215], v[58:61]
	v_mfma_f32_16x16x32_f16 v[70:73], v[196:199], v[216:219], v[70:73]
	v_mfma_f32_16x16x32_f16 v[86:89], v[204:207], v[216:219], v[78:81]
	s_barrier
	s_nop 0
	ds_read_b128 v[78:81], v173 offset:16384
	ds_read_b128 v[168:171], v173 offset:17408
	ds_read_b128 v[174:177], v173 offset:18432
	ds_read_b128 v[178:181], v173 offset:19456
	ds_read_b128 v[182:185], v173 offset:20480
	ds_read_b128 v[186:189], v173 offset:21504
	ds_read_b128 v[190:193], v173 offset:22528
	ds_read_b128 v[196:199], v173 offset:23552
	s_waitcnt vmcnt(4)
	s_barrier
	s_waitcnt lgkmcnt(0)
	v_mfma_f32_16x16x32_f16 v[26:29], v[78:81], v[134:137], v[26:29]
	v_mfma_f32_16x16x32_f16 v[38:41], v[78:81], v[152:155], v[38:41]
	v_mfma_f32_16x16x32_f16 v[26:29], v[168:171], v[138:141], v[26:29]
	v_mfma_f32_16x16x32_f16 v[38:41], v[168:171], v[156:159], v[38:41]
	v_mfma_f32_16x16x32_f16 v[50:53], v[174:177], v[134:137], v[50:53]
	v_mfma_f32_16x16x32_f16 v[62:65], v[174:177], v[152:155], v[62:65]
	v_mfma_f32_16x16x32_f16 v[74:77], v[182:185], v[134:137], v[74:77]
	v_mfma_f32_16x16x32_f16 v[82:85], v[182:185], v[152:155], v[82:85]
	v_mfma_f32_16x16x32_f16 v[90:93], v[190:193], v[134:137], v[90:93]
	v_mfma_f32_16x16x32_f16 v[94:97], v[190:193], v[152:155], v[94:97]
	v_mfma_f32_16x16x32_f16 v[50:53], v[178:181], v[138:141], v[50:53]
	v_mfma_f32_16x16x32_f16 v[62:65], v[178:181], v[156:159], v[62:65]
	v_mfma_f32_16x16x32_f16 v[74:77], v[186:189], v[138:141], v[74:77]
	v_mfma_f32_16x16x32_f16 v[82:85], v[186:189], v[156:159], v[82:85]
	v_mfma_f32_16x16x32_f16 v[90:93], v[196:199], v[138:141], v[90:93]
	v_mfma_f32_16x16x32_f16 v[94:97], v[196:199], v[156:159], v[94:97]
	v_mfma_f32_16x16x32_f16 v[98:101], v[78:81], v[130:133], v[98:101]
	v_mfma_f32_16x16x32_f16 v[78:81], v[78:81], v[160:163], v[102:105]
	v_mfma_f32_16x16x32_f16 v[102:105], v[168:171], v[216:219], v[78:81]
	v_mfma_f32_16x16x32_f16 v[78:81], v[174:177], v[130:133], v[106:109]
	v_mfma_f32_16x16x32_f16 v[106:109], v[178:181], v[212:215], v[78:81]
	v_mfma_f32_16x16x32_f16 v[78:81], v[174:177], v[160:163], v[110:113]
	v_mfma_f32_16x16x32_f16 v[200:203], v[178:181], v[216:219], v[78:81]
	v_mfma_f32_16x16x32_f16 v[78:81], v[182:185], v[130:133], v[114:117]
	v_mfma_f32_16x16x32_f16 v[204:207], v[186:189], v[212:215], v[78:81]
	v_mfma_f32_16x16x32_f16 v[78:81], v[182:185], v[160:163], v[118:121]
	v_mfma_f32_16x16x32_f16 v[220:223], v[186:189], v[216:219], v[78:81]
	v_mfma_f32_16x16x32_f16 v[78:81], v[190:193], v[130:133], v[122:125]
	v_mfma_f32_16x16x32_f16 v[98:101], v[168:171], v[212:215], v[98:101]
	v_mfma_f32_16x16x32_f16 v[212:215], v[196:199], v[212:215], v[78:81]
	v_mfma_f32_16x16x32_f16 v[78:81], v[190:193], v[160:163], v[126:129]
	v_mfma_f32_16x16x32_f16 v[196:199], v[196:199], v[216:219], v[78:81]
	s_barrier
	ds_read_b128 v[110:113], v148
	ds_read_b128 v[130:133], v149
	ds_read_b128 v[216:219], v150
	ds_read_b128 v[224:227], v151
	s_nop 0
	ds_read_b128 v[78:81], v173 offset:32768
	ds_read_b128 v[114:117], v173 offset:33792
	ds_read_b128 v[118:121], v173 offset:34816
	ds_read_b128 v[134:137], v173 offset:35840
	ds_read_b128 v[138:141], v173 offset:36864
	ds_read_b128 v[168:171], v173 offset:37888
	ds_read_b128 v[174:177], v173 offset:38912
	ds_read_b128 v[228:231], v173 offset:39936
	s_waitcnt vmcnt(2)
	s_barrier
	s_waitcnt lgkmcnt(0)
	v_mfma_f32_16x16x32_f16 v[2:5], v[78:81], v[110:113], v[2:5]
	v_mfma_f32_16x16x32_f16 v[190:193], v[114:117], v[130:133], v[2:5]
	v_mfma_f32_16x16x32_f16 v[2:5], v[78:81], v[216:219], v[6:9]
	v_mfma_f32_16x16x32_f16 v[158:161], v[114:117], v[224:227], v[2:5]
	v_mfma_f32_16x16x32_f16 v[2:5], v[118:121], v[110:113], v[10:13]
	v_mfma_f32_16x16x32_f16 v[186:189], v[134:137], v[130:133], v[2:5]
	v_mfma_f32_16x16x32_f16 v[2:5], v[118:121], v[216:219], v[18:21]
	v_mfma_f32_16x16x32_f16 v[154:157], v[134:137], v[224:227], v[2:5]
	v_mfma_f32_16x16x32_f16 v[2:5], v[138:141], v[110:113], v[30:33]
	v_mfma_f32_16x16x32_f16 v[182:185], v[168:171], v[130:133], v[2:5]
	v_mfma_f32_16x16x32_f16 v[2:5], v[138:141], v[216:219], v[42:45]
	v_mfma_f32_16x16x32_f16 v[150:153], v[168:171], v[224:227], v[2:5]
	v_mfma_f32_16x16x32_f16 v[2:5], v[174:177], v[110:113], v[54:57]
	v_mfma_f32_16x16x32_f16 v[178:181], v[228:231], v[130:133], v[2:5]
	v_mfma_f32_16x16x32_f16 v[2:5], v[174:177], v[216:219], v[66:69]
	v_mfma_f32_16x16x32_f16 v[146:149], v[228:231], v[224:227], v[2:5]
	s_barrier
	s_nop 4
	ds_read_b128 v[2:5], v142
	ds_read_b128 v[6:9], v143
	ds_read_b128 v[10:13], v144
	ds_read_b128 v[18:21], v145
	s_waitcnt vmcnt(0)
	s_barrier
	s_waitcnt lgkmcnt(0)
	v_mfma_f32_16x16x32_f16 v[14:17], v[78:81], v[2:5], v[14:17]
	v_mfma_f32_16x16x32_f16 v[126:129], v[114:117], v[6:9], v[14:17]
	v_mfma_f32_16x16x32_f16 v[14:17], v[78:81], v[10:13], v[22:25]
	v_mfma_f32_16x16x32_f16 v[78:81], v[114:117], v[18:21], v[14:17]
	v_mfma_f32_16x16x32_f16 v[14:17], v[118:121], v[2:5], v[34:37]
	v_mfma_f32_16x16x32_f16 v[122:125], v[134:137], v[6:9], v[14:17]
	v_mfma_f32_16x16x32_f16 v[14:17], v[118:121], v[10:13], v[46:49]
	v_mfma_f32_16x16x32_f16 v[66:69], v[134:137], v[18:21], v[14:17]
	v_mfma_f32_16x16x32_f16 v[14:17], v[138:141], v[2:5], v[58:61]
	v_mfma_f32_16x16x32_f16 v[118:121], v[168:171], v[6:9], v[14:17]
	v_mfma_f32_16x16x32_f16 v[14:17], v[138:141], v[10:13], v[70:73]
	v_mfma_f32_16x16x32_f16 v[54:57], v[168:171], v[18:21], v[14:17]
	v_mfma_f32_16x16x32_f16 v[14:17], v[174:177], v[2:5], v[164:167]
	v_mfma_f32_16x16x32_f16 v[114:117], v[228:231], v[6:9], v[14:17]
	v_mfma_f32_16x16x32_f16 v[14:17], v[174:177], v[10:13], v[86:89]
	v_mfma_f32_16x16x32_f16 v[42:45], v[228:231], v[18:21], v[14:17]
	s_barrier
	s_nop 4
	ds_read_b128 v[14:17], v173 offset:49152
	ds_read_b128 v[22:25], v173 offset:50176
	ds_read_b128 v[30:33], v173 offset:51200
	ds_read_b128 v[34:37], v173 offset:52224
	ds_read_b128 v[46:49], v173 offset:53248
	ds_read_b128 v[58:61], v173 offset:54272
	ds_read_b128 v[70:73], v173 offset:55296
	ds_read_b128 v[86:89], v173 offset:56320
	s_barrier
	s_waitcnt lgkmcnt(0)
	v_mfma_f32_16x16x32_f16 v[26:29], v[14:17], v[110:113], v[26:29]
	v_mfma_f32_16x16x32_f16 v[174:177], v[22:25], v[130:133], v[26:29]
	v_mfma_f32_16x16x32_f16 v[26:29], v[14:17], v[216:219], v[38:41]
	v_mfma_f32_16x16x32_f16 v[142:145], v[22:25], v[224:227], v[26:29]
	v_mfma_f32_16x16x32_f16 v[26:29], v[30:33], v[110:113], v[50:53]
	v_mfma_f32_16x16x32_f16 v[170:173], v[34:37], v[130:133], v[26:29]
	v_mfma_f32_16x16x32_f16 v[26:29], v[30:33], v[216:219], v[62:65]
	v_mfma_f32_16x16x32_f16 v[138:141], v[34:37], v[224:227], v[26:29]
	v_mfma_f32_16x16x32_f16 v[26:29], v[46:49], v[110:113], v[74:77]
	v_mfma_f32_16x16x32_f16 v[166:169], v[58:61], v[130:133], v[26:29]
	v_mfma_f32_16x16x32_f16 v[26:29], v[46:49], v[216:219], v[82:85]
	v_mfma_f32_16x16x32_f16 v[134:137], v[58:61], v[224:227], v[26:29]
	v_mfma_f32_16x16x32_f16 v[26:29], v[70:73], v[110:113], v[90:93]
	v_mfma_f32_16x16x32_f16 v[162:165], v[86:89], v[130:133], v[26:29]
	v_mfma_f32_16x16x32_f16 v[26:29], v[70:73], v[216:219], v[94:97]
	v_mfma_f32_16x16x32_f16 v[130:133], v[86:89], v[224:227], v[26:29]
	v_mfma_f32_16x16x32_f16 v[26:29], v[14:17], v[2:5], v[98:101]
	v_mfma_f32_16x16x32_f16 v[14:17], v[14:17], v[10:13], v[102:105]
	v_mfma_f32_16x16x32_f16 v[38:41], v[22:25], v[18:21], v[14:17]
	v_mfma_f32_16x16x32_f16 v[14:17], v[30:33], v[2:5], v[106:109]
	v_mfma_f32_16x16x32_f16 v[106:109], v[34:37], v[6:9], v[14:17]
	v_mfma_f32_16x16x32_f16 v[14:17], v[30:33], v[10:13], v[200:203]
	v_mfma_f32_16x16x32_f16 v[110:113], v[22:25], v[6:9], v[26:29]
	v_mfma_f32_16x16x32_f16 v[26:29], v[34:37], v[18:21], v[14:17]
	v_mfma_f32_16x16x32_f16 v[14:17], v[46:49], v[2:5], v[204:207]
	v_mfma_f32_16x16x32_f16 v[2:5], v[70:73], v[2:5], v[212:215]
	v_mfma_f32_16x16x32_f16 v[102:105], v[58:61], v[6:9], v[14:17]
	v_mfma_f32_16x16x32_f16 v[14:17], v[46:49], v[10:13], v[220:223]
	v_mfma_f32_16x16x32_f16 v[98:101], v[86:89], v[6:9], v[2:5]
	v_mfma_f32_16x16x32_f16 v[2:5], v[70:73], v[10:13], v[196:199]
	v_mfma_f32_16x16x32_f16 v[14:17], v[58:61], v[18:21], v[14:17]
	v_mfma_f32_16x16x32_f16 v[2:5], v[86:89], v[18:21], v[2:5]
	s_cmpk_gt_u32 s65, 0xff
	s_barrier
	s_cbranch_scc1 .LBB6_15
	s_barrier

	.amdhsa_kernel _Z14gemm256_kernelILi0ELi512ELi1536EEv8GemmArgs
		.amdhsa_group_segment_fixed_size 0
		.amdhsa_private_segment_fixed_size 0
		.amdhsa_kernarg_size 592
		.amdhsa_user_sgpr_count 2
		.amdhsa_user_sgpr_dispatch_ptr 0
		.amdhsa_user_sgpr_queue_ptr 0
		.amdhsa_user_sgpr_kernarg_segment_ptr 1
		.amdhsa_user_sgpr_dispatch_id 0
		.amdhsa_user_sgpr_kernarg_preload_length 0
		.amdhsa_user_sgpr_kernarg_preload_offset 0
		.amdhsa_user_sgpr_private_segment_size 0
		.amdhsa_uses_dynamic_stack 0
		.amdhsa_enable_private_segment 0
		.amdhsa_system_sgpr_workgroup_id_x 1
		.amdhsa_system_sgpr_workgroup_id_y 0
		.amdhsa_system_sgpr_workgroup_id_z 0
		.amdhsa_system_sgpr_workgroup_info 0
		.amdhsa_system_vgpr_workitem_id 0
		.amdhsa_next_free_vgpr 256
		.amdhsa_next_free_sgpr 88
		.amdhsa_accum_offset 256
		.amdhsa_reserve_vcc 1
		.amdhsa_float_round_mode_32 0
		.amdhsa_float_round_mode_16_64 0
		.amdhsa_float_denorm_mode_32 3
		.amdhsa_float_denorm_mode_16_64 3
		.amdhsa_dx10_clamp 1
		.amdhsa_ieee_mode 1
		.amdhsa_fp16_overflow 0
		.amdhsa_tg_split 0
		.amdhsa_exception_fp_ieee_invalid_op 0
		.amdhsa_exception_fp_denorm_src 0
		.amdhsa_exception_fp_ieee_div_zero 0
		.amdhsa_exception_fp_ieee_overflow 0
		.amdhsa_exception_fp_ieee_underflow 0
		.amdhsa_exception_fp_ieee_inexact 0
		.amdhsa_exception_int_div_zero 0
	.end_amdhsa_kernel

.LBB7_238:
	v_lshlrev_b32_e32 v2, 12, v2
	s_lshl_b32 s50, s65, 6
	v_lshlrev_b32_e32 v6, 12, v6
	v_and_b32_e32 v2, 0xffffe000, v2
	s_lshl_b32 s5, s66, 13
	s_and_b32 s50, s50, 0x3000
	v_and_b32_e32 v6, 0xffffe000, v6
	v_lshl_add_u32 v2, v3, 9, v2
	v_and_b32_e32 v10, 48, v210
	v_lshlrev_b32_e32 v11, 6, v210
	v_lshl_add_u32 v6, v7, 9, v6
	s_add_u32 s48, s8, s48
	v_or_b32_e32 v2, v2, v4
	v_and_or_b32 v10, v11, s58, v10
	v_lshlrev_b32_e32 v11, 2, v210
	v_or_b32_e32 v6, v6, v8
	s_addc_u32 s49, s9, s49
	v_add_u32_sdwa v2, v2, sext(v5) dst_sel:DWORD dst_unused:UNUSED_PAD src0_sel:DWORD src1_sel:WORD_0
	v_and_b32_e32 v11, 32, v11
	v_add_u32_sdwa v6, v6, sext(v9) dst_sel:DWORD dst_unused:UNUSED_PAD src0_sel:DWORD src1_sel:WORD_0
	v_ashrrev_i32_e32 v3, 31, v2
	s_add_u32 s46, s10, s46
	v_xad_u32 v168, v10, v11, 0
	s_waitcnt vmcnt(6)
	v_ashrrev_i32_e32 v7, 31, v6
	v_lshlrev_b64 v[2:3], 1, v[2:3]
	s_addc_u32 s47, s11, s47
	v_add_u32_e32 v10, s50, v168
	v_lshlrev_b64 v[6:7], 1, v[6:7]
	v_lshl_add_u64 v[136:137], s[48:49], 0, v[2:3]
	v_lshl_add_u64 v[140:141], s[46:47], 0, v[2:3]
	v_mov_b32_e32 v2, 0
	v_add_u32_e32 v169, 0x10000, v10
	v_add_u32_e32 v170, 0x10400, v10
	v_add_u32_e32 v171, 0x10800, v10
	v_add_u32_e32 v172, 0x10c00, v10
	v_add_u32_e32 v161, 0x14000, v10
	v_add_u32_e32 v162, 0x14400, v10
	v_add_u32_e32 v163, 0x14800, v10
	v_add_u32_e32 v164, 0x14c00, v10
	v_add_u32_e32 v148, 0x18000, v10
	v_add_u32_e32 v149, 0x18400, v10
	v_add_u32_e32 v150, 0x18800, v10
	v_add_u32_e32 v151, 0x18c00, v10
	v_add_u32_e32 v142, 0x1c000, v10
	v_add_u32_e32 v143, 0x1c400, v10
	v_add_u32_e32 v144, 0x1c800, v10
	v_add_u32_e32 v145, 0x1cc00, v10
	v_lshl_add_u64 v[134:135], s[48:49], 0, v[6:7]
	v_lshl_add_u64 v[138:139], s[46:47], 0, v[6:7]
	s_mov_b32 s48, -2
	s_mov_b64 s[46:47], 0
	v_mov_b32_e32 v3, v2
	v_mov_b32_e32 v4, v2
	v_mov_b32_e32 v5, v2
	v_mov_b32_e32 v6, v2
	v_mov_b32_e32 v7, v2
	v_mov_b32_e32 v8, v2
	v_mov_b32_e32 v9, v2
	v_mov_b32_e32 v10, v2
	v_mov_b32_e32 v11, v2
	v_mov_b32_e32 v12, v2
	v_mov_b32_e32 v13, v2
	v_mov_b32_e32 v18, v2
	v_mov_b32_e32 v19, v2
	v_mov_b32_e32 v20, v2
	v_mov_b32_e32 v21, v2
	v_mov_b32_e32 v30, v2
	v_mov_b32_e32 v31, v2
	v_mov_b32_e32 v32, v2
	v_mov_b32_e32 v33, v2
	v_mov_b32_e32 v42, v2
	v_mov_b32_e32 v43, v2
	v_mov_b32_e32 v44, v2
	v_mov_b32_e32 v45, v2
	v_mov_b32_e32 v54, v2
	v_mov_b32_e32 v55, v2
	v_mov_b32_e32 v56, v2
	v_mov_b32_e32 v57, v2
	v_mov_b32_e32 v66, v2
	v_mov_b32_e32 v67, v2
	v_mov_b32_e32 v68, v2
	v_mov_b32_e32 v69, v2
	v_mov_b32_e32 v14, v2
	v_mov_b32_e32 v15, v2
	v_mov_b32_e32 v16, v2
	v_mov_b32_e32 v17, v2
	v_mov_b32_e32 v22, v2
	v_mov_b32_e32 v23, v2
	v_mov_b32_e32 v24, v2
	v_mov_b32_e32 v25, v2
	v_mov_b32_e32 v34, v2
	v_mov_b32_e32 v35, v2
	v_mov_b32_e32 v36, v2
	v_mov_b32_e32 v37, v2
	v_mov_b32_e32 v46, v2
	v_mov_b32_e32 v47, v2
	v_mov_b32_e32 v48, v2
	v_mov_b32_e32 v49, v2
	v_mov_b32_e32 v58, v2
	v_mov_b32_e32 v59, v2
	v_mov_b32_e32 v60, v2
	v_mov_b32_e32 v61, v2
	v_mov_b32_e32 v70, v2
	v_mov_b32_e32 v71, v2
	v_mov_b32_e32 v72, v2
	v_mov_b32_e32 v73, v2
	v_mov_b32_e32 v78, v2
	v_mov_b32_e32 v79, v2
	v_mov_b32_e32 v80, v2
	v_mov_b32_e32 v81, v2
	v_mov_b32_e32 v86, v2
	v_mov_b32_e32 v87, v2
	v_mov_b32_e32 v88, v2
	v_mov_b32_e32 v89, v2
	v_mov_b32_e32 v26, v2
	v_mov_b32_e32 v27, v2
	v_mov_b32_e32 v28, v2
	v_mov_b32_e32 v29, v2
	v_mov_b32_e32 v38, v2
	v_mov_b32_e32 v39, v2
	v_mov_b32_e32 v40, v2
	v_mov_b32_e32 v41, v2
	v_mov_b32_e32 v50, v2
	v_mov_b32_e32 v51, v2
	v_mov_b32_e32 v52, v2
	v_mov_b32_e32 v53, v2
	v_mov_b32_e32 v62, v2
	v_mov_b32_e32 v63, v2
	v_mov_b32_e32 v64, v2
	v_mov_b32_e32 v65, v2
	v_mov_b32_e32 v74, v2
	v_mov_b32_e32 v75, v2
	v_mov_b32_e32 v76, v2
	v_mov_b32_e32 v77, v2
	v_mov_b32_e32 v82, v2
	v_mov_b32_e32 v83, v2
	v_mov_b32_e32 v84, v2
	v_mov_b32_e32 v85, v2
	v_mov_b32_e32 v90, v2
	v_mov_b32_e32 v91, v2
	v_mov_b32_e32 v92, v2
	v_mov_b32_e32 v93, v2
	v_mov_b32_e32 v94, v2
	v_mov_b32_e32 v95, v2
	v_mov_b32_e32 v96, v2
	v_mov_b32_e32 v97, v2
	v_mov_b32_e32 v98, v2
	v_mov_b32_e32 v99, v2
	v_mov_b32_e32 v100, v2
	v_mov_b32_e32 v101, v2
	v_mov_b32_e32 v102, v2
	v_mov_b32_e32 v103, v2
	v_mov_b32_e32 v104, v2
	v_mov_b32_e32 v105, v2
	v_mov_b32_e32 v106, v2
	v_mov_b32_e32 v107, v2
	v_mov_b32_e32 v108, v2
	v_mov_b32_e32 v109, v2
	v_mov_b32_e32 v110, v2
	v_mov_b32_e32 v111, v2
	v_mov_b32_e32 v112, v2
	v_mov_b32_e32 v113, v2
	v_mov_b32_e32 v114, v2
	v_mov_b32_e32 v115, v2
	v_mov_b32_e32 v116, v2
	v_mov_b32_e32 v117, v2
	v_mov_b32_e32 v118, v2
	v_mov_b32_e32 v119, v2
	v_mov_b32_e32 v120, v2
	v_mov_b32_e32 v121, v2
	v_mov_b32_e32 v122, v2
	v_mov_b32_e32 v123, v2
	v_mov_b32_e32 v124, v2
	v_mov_b32_e32 v125, v2
	v_mov_b32_e32 v126, v2
	v_mov_b32_e32 v127, v2
	v_mov_b32_e32 v128, v2
	v_mov_b32_e32 v129, v2
	v_add_u32_e32 v174, 0xc000, v152
	v_add_u32_e32 v175, 0xe000, v152
	s_nop 0
	v_readfirstlane_b32 s72, v174
	v_readfirstlane_b32 s73, v175
	v_readfirstlane_b32 s74, v146
	v_readfirstlane_b32 s75, v147
	v_readfirstlane_b32 s76, v152
	v_readfirstlane_b32 s77, v153
	v_readfirstlane_b32 s78, v154
	v_readfirstlane_b32 s79, v155
	v_readfirstlane_b32 s80, v156
	v_readfirstlane_b32 s81, v157
	v_readfirstlane_b32 s82, v158
	v_readfirstlane_b32 s83, v159
	v_readfirstlane_b32 s84, v160
	v_readfirstlane_b32 s85, v165
	v_readfirstlane_b32 s86, v166
	v_readfirstlane_b32 s87, v167
	s_barrier
	s_barrier
.LBB7_239:
	ds_read_b128 v[176:179], v169
	ds_read_b128 v[180:183], v170
	ds_read_b128 v[184:187], v171
	ds_read_b128 v[188:191], v172
	v_add_u32_e32 v174, 0xc000, v152
	v_lshl_add_u64 v[192:193], v[136:137], 0, s[46:47]
	v_add_u32_e32 v175, 0xe000, v152
	v_add_u32_e32 v173, s5, v168
	v_lshl_add_u64 v[232:233], v[192:193], 0, s[34:35]
	s_mov_b32 m0, s72
	v_lshl_add_u64 v[248:249], v[134:135], 0, s[46:47]
	ds_read_b128 v[196:199], v173
	ds_read_b128 v[200:203], v173 offset:1024
	ds_read_b128 v[204:207], v173 offset:2048
	ds_read_b128 v[212:215], v173 offset:3072
	ds_read_b128 v[216:219], v173 offset:4096
	ds_read_b128 v[220:223], v173 offset:5120
	ds_read_b128 v[224:227], v173 offset:6144
	ds_read_b128 v[228:231], v173 offset:7168
	global_load_lds_dwordx4 v[232:233], off
	v_lshl_add_u64 v[232:233], v[248:249], 0, s[34:35]
	s_mov_b32 m0, s73
	s_nop 0
	global_load_lds_dwordx4 v[232:233], off
	s_waitcnt lgkmcnt(8)
	s_barrier
	s_waitcnt lgkmcnt(0)
	v_mfma_f32_16x16x32_f16 v[2:5], v[196:199], v[176:179], v[2:5]
	v_mfma_f32_16x16x32_f16 v[6:9], v[196:199], v[184:187], v[6:9]
	v_mfma_f32_16x16x32_f16 v[10:13], v[204:207], v[176:179], v[10:13]
	v_mfma_f32_16x16x32_f16 v[18:21], v[204:207], v[184:187], v[18:21]
	v_mfma_f32_16x16x32_f16 v[30:33], v[216:219], v[176:179], v[30:33]
	v_mfma_f32_16x16x32_f16 v[42:45], v[216:219], v[184:187], v[42:45]
	v_mfma_f32_16x16x32_f16 v[54:57], v[224:227], v[176:179], v[54:57]
	v_mfma_f32_16x16x32_f16 v[66:69], v[224:227], v[184:187], v[66:69]
	v_mfma_f32_16x16x32_f16 v[2:5], v[200:203], v[180:183], v[2:5]
	v_mfma_f32_16x16x32_f16 v[6:9], v[200:203], v[188:191], v[6:9]
	v_mfma_f32_16x16x32_f16 v[10:13], v[212:215], v[180:183], v[10:13]
	v_mfma_f32_16x16x32_f16 v[18:21], v[212:215], v[188:191], v[18:21]
	v_mfma_f32_16x16x32_f16 v[30:33], v[220:223], v[180:183], v[30:33]
	v_mfma_f32_16x16x32_f16 v[42:45], v[220:223], v[188:191], v[42:45]
	v_mfma_f32_16x16x32_f16 v[54:57], v[228:231], v[180:183], v[54:57]
	v_mfma_f32_16x16x32_f16 v[66:69], v[228:231], v[188:191], v[66:69]
	s_barrier
	v_lshl_add_u64 v[250:251], v[140:141], 0, s[46:47]
	v_lshl_add_u64 v[252:253], v[250:251], 0, s[36:37]
	s_mov_b32 m0, s74
	ds_read_b128 v[232:235], v161
	ds_read_b128 v[236:239], v162
	ds_read_b128 v[240:243], v163
	ds_read_b128 v[244:247], v164
	global_load_lds_dwordx4 v[252:253], off
	v_lshl_add_u64 v[252:253], v[138:139], 0, s[46:47]
	v_lshl_add_u64 v[254:255], v[252:253], 0, s[36:37]
	s_mov_b32 m0, s75
	s_nop 0
	global_load_lds_dwordx4 v[254:255], off
	s_barrier
	s_waitcnt lgkmcnt(0)
	v_mfma_f32_16x16x32_f16 v[14:17], v[196:199], v[232:235], v[14:17]
	v_mfma_f32_16x16x32_f16 v[22:25], v[196:199], v[240:243], v[22:25]
	v_mfma_f32_16x16x32_f16 v[34:37], v[204:207], v[232:235], v[34:37]
	v_mfma_f32_16x16x32_f16 v[46:49], v[204:207], v[240:243], v[46:49]
	v_mfma_f32_16x16x32_f16 v[58:61], v[216:219], v[232:235], v[58:61]
	v_mfma_f32_16x16x32_f16 v[70:73], v[216:219], v[240:243], v[70:73]
	v_mfma_f32_16x16x32_f16 v[78:81], v[224:227], v[232:235], v[78:81]
	v_mfma_f32_16x16x32_f16 v[86:89], v[224:227], v[240:243], v[86:89]
	v_mfma_f32_16x16x32_f16 v[14:17], v[200:203], v[236:239], v[14:17]
	v_mfma_f32_16x16x32_f16 v[22:25], v[200:203], v[244:247], v[22:25]
	v_mfma_f32_16x16x32_f16 v[34:37], v[212:215], v[236:239], v[34:37]
	v_mfma_f32_16x16x32_f16 v[46:49], v[212:215], v[244:247], v[46:49]
	v_mfma_f32_16x16x32_f16 v[58:61], v[220:223], v[236:239], v[58:61]
	v_mfma_f32_16x16x32_f16 v[70:73], v[220:223], v[244:247], v[70:73]
	v_mfma_f32_16x16x32_f16 v[78:81], v[228:231], v[236:239], v[78:81]
	v_mfma_f32_16x16x32_f16 v[86:89], v[228:231], v[244:247], v[86:89]
	v_lshl_add_u64 v[254:255], v[192:193], 0, s[36:37]
	s_mov_b32 m0, s76
	s_barrier
	ds_read_b128 v[196:199], v173 offset:16384
	ds_read_b128 v[200:203], v173 offset:17408
	ds_read_b128 v[204:207], v173 offset:18432
	ds_read_b128 v[212:215], v173 offset:19456
	ds_read_b128 v[216:219], v173 offset:20480
	ds_read_b128 v[220:223], v173 offset:21504
	ds_read_b128 v[224:227], v173 offset:22528
	ds_read_b128 v[228:231], v173 offset:23552
	global_load_lds_dwordx4 v[254:255], off
	v_lshl_add_u64 v[254:255], v[248:249], 0, s[36:37]
	s_mov_b32 m0, s77
	s_nop 0
	global_load_lds_dwordx4 v[254:255], off
	s_barrier
	s_waitcnt lgkmcnt(0)
	v_mfma_f32_16x16x32_f16 v[26:29], v[196:199], v[176:179], v[26:29]
	v_mfma_f32_16x16x32_f16 v[38:41], v[196:199], v[184:187], v[38:41]
	v_mfma_f32_16x16x32_f16 v[50:53], v[204:207], v[176:179], v[50:53]
	v_mfma_f32_16x16x32_f16 v[62:65], v[204:207], v[184:187], v[62:65]
	v_mfma_f32_16x16x32_f16 v[74:77], v[216:219], v[176:179], v[74:77]
	v_mfma_f32_16x16x32_f16 v[82:85], v[216:219], v[184:187], v[82:85]
	v_mfma_f32_16x16x32_f16 v[90:93], v[224:227], v[176:179], v[90:93]
	v_mfma_f32_16x16x32_f16 v[94:97], v[224:227], v[184:187], v[94:97]
	v_mfma_f32_16x16x32_f16 v[26:29], v[200:203], v[180:183], v[26:29]
	v_mfma_f32_16x16x32_f16 v[38:41], v[200:203], v[188:191], v[38:41]
	v_mfma_f32_16x16x32_f16 v[50:53], v[212:215], v[180:183], v[50:53]
	v_mfma_f32_16x16x32_f16 v[62:65], v[212:215], v[188:191], v[62:65]
	v_mfma_f32_16x16x32_f16 v[74:77], v[220:223], v[180:183], v[74:77]
	v_mfma_f32_16x16x32_f16 v[82:85], v[220:223], v[188:191], v[82:85]
	v_mfma_f32_16x16x32_f16 v[90:93], v[228:231], v[180:183], v[90:93]
	v_mfma_f32_16x16x32_f16 v[94:97], v[228:231], v[188:191], v[94:97]
	s_barrier
	v_lshl_add_u64 v[176:177], v[250:251], 0, s[38:39]
	s_mov_b32 m0, s78
	global_load_lds_dwordx4 v[176:177], off
	v_lshl_add_u64 v[176:177], v[252:253], 0, s[38:39]
	s_mov_b32 m0, s79
	s_nop 0
	global_load_lds_dwordx4 v[176:177], off
	s_waitcnt vmcnt(6)
	s_barrier
	v_mfma_f32_16x16x32_f16 v[98:101], v[196:199], v[232:235], v[98:101]
	v_mfma_f32_16x16x32_f16 v[102:105], v[196:199], v[240:243], v[102:105]
	v_mfma_f32_16x16x32_f16 v[106:109], v[204:207], v[232:235], v[106:109]
	v_mfma_f32_16x16x32_f16 v[110:113], v[204:207], v[240:243], v[110:113]
	v_mfma_f32_16x16x32_f16 v[114:117], v[216:219], v[232:235], v[114:117]
	v_mfma_f32_16x16x32_f16 v[118:121], v[216:219], v[240:243], v[118:121]
	v_mfma_f32_16x16x32_f16 v[122:125], v[224:227], v[232:235], v[122:125]
	v_mfma_f32_16x16x32_f16 v[126:129], v[224:227], v[240:243], v[126:129]
	v_mfma_f32_16x16x32_f16 v[98:101], v[200:203], v[236:239], v[98:101]
	v_mfma_f32_16x16x32_f16 v[102:105], v[200:203], v[244:247], v[102:105]
	v_mfma_f32_16x16x32_f16 v[106:109], v[212:215], v[236:239], v[106:109]
	v_mfma_f32_16x16x32_f16 v[110:113], v[212:215], v[244:247], v[110:113]
	v_mfma_f32_16x16x32_f16 v[114:117], v[220:223], v[236:239], v[114:117]
	v_mfma_f32_16x16x32_f16 v[118:121], v[220:223], v[244:247], v[118:121]
	v_mfma_f32_16x16x32_f16 v[122:125], v[228:231], v[236:239], v[122:125]
	v_mfma_f32_16x16x32_f16 v[126:129], v[228:231], v[244:247], v[126:129]
	s_barrier
	ds_read_b128 v[176:179], v148
	ds_read_b128 v[180:183], v149
	ds_read_b128 v[184:187], v150
	ds_read_b128 v[188:191], v151
	v_lshl_add_u64 v[232:233], v[192:193], 0, s[38:39]
	s_mov_b32 m0, s80
	ds_read_b128 v[196:199], v173 offset:32768
	ds_read_b128 v[200:203], v173 offset:33792
	ds_read_b128 v[204:207], v173 offset:34816
	ds_read_b128 v[212:215], v173 offset:35840
	ds_read_b128 v[216:219], v173 offset:36864
	ds_read_b128 v[220:223], v173 offset:37888
	ds_read_b128 v[224:227], v173 offset:38912
	ds_read_b128 v[228:231], v173 offset:39936
	global_load_lds_dwordx4 v[232:233], off
	v_lshl_add_u64 v[232:233], v[248:249], 0, s[38:39]
	s_mov_b32 m0, s81
	s_nop 0
	global_load_lds_dwordx4 v[232:233], off
	s_waitcnt lgkmcnt(8)
	s_barrier
	s_waitcnt lgkmcnt(0)
	v_mfma_f32_16x16x32_f16 v[2:5], v[196:199], v[176:179], v[2:5]
	v_mfma_f32_16x16x32_f16 v[6:9], v[196:199], v[184:187], v[6:9]
	v_mfma_f32_16x16x32_f16 v[10:13], v[204:207], v[176:179], v[10:13]
	v_mfma_f32_16x16x32_f16 v[18:21], v[204:207], v[184:187], v[18:21]
	v_mfma_f32_16x16x32_f16 v[30:33], v[216:219], v[176:179], v[30:33]
	v_mfma_f32_16x16x32_f16 v[42:45], v[216:219], v[184:187], v[42:45]
	v_mfma_f32_16x16x32_f16 v[54:57], v[224:227], v[176:179], v[54:57]
	v_mfma_f32_16x16x32_f16 v[66:69], v[224:227], v[184:187], v[66:69]
	v_mfma_f32_16x16x32_f16 v[2:5], v[200:203], v[180:183], v[2:5]
	v_mfma_f32_16x16x32_f16 v[6:9], v[200:203], v[188:191], v[6:9]
	v_mfma_f32_16x16x32_f16 v[10:13], v[212:215], v[180:183], v[10:13]
	v_mfma_f32_16x16x32_f16 v[18:21], v[212:215], v[188:191], v[18:21]
	v_mfma_f32_16x16x32_f16 v[30:33], v[220:223], v[180:183], v[30:33]
	v_mfma_f32_16x16x32_f16 v[42:45], v[220:223], v[188:191], v[42:45]
	v_mfma_f32_16x16x32_f16 v[54:57], v[228:231], v[180:183], v[54:57]
	v_mfma_f32_16x16x32_f16 v[66:69], v[228:231], v[188:191], v[66:69]
	s_barrier
	v_lshl_add_u64 v[254:255], v[250:251], 0, s[40:41]
	s_mov_b32 m0, s82
	ds_read_b128 v[232:235], v142
	ds_read_b128 v[236:239], v143
	ds_read_b128 v[240:243], v144
	ds_read_b128 v[244:247], v145
	global_load_lds_dwordx4 v[254:255], off
	v_lshl_add_u64 v[254:255], v[252:253], 0, s[40:41]
	s_mov_b32 m0, s83
	s_nop 0
	global_load_lds_dwordx4 v[254:255], off
	s_barrier
	s_waitcnt lgkmcnt(0)
	v_mfma_f32_16x16x32_f16 v[14:17], v[196:199], v[232:235], v[14:17]
	v_mfma_f32_16x16x32_f16 v[22:25], v[196:199], v[240:243], v[22:25]
	v_mfma_f32_16x16x32_f16 v[34:37], v[204:207], v[232:235], v[34:37]
	v_mfma_f32_16x16x32_f16 v[46:49], v[204:207], v[240:243], v[46:49]
	v_mfma_f32_16x16x32_f16 v[58:61], v[216:219], v[232:235], v[58:61]
	v_mfma_f32_16x16x32_f16 v[70:73], v[216:219], v[240:243], v[70:73]
	v_mfma_f32_16x16x32_f16 v[78:81], v[224:227], v[232:235], v[78:81]
	v_mfma_f32_16x16x32_f16 v[86:89], v[224:227], v[240:243], v[86:89]
	v_mfma_f32_16x16x32_f16 v[14:17], v[200:203], v[236:239], v[14:17]
	v_mfma_f32_16x16x32_f16 v[22:25], v[200:203], v[244:247], v[22:25]
	v_mfma_f32_16x16x32_f16 v[34:37], v[212:215], v[236:239], v[34:37]
	v_mfma_f32_16x16x32_f16 v[46:49], v[212:215], v[244:247], v[46:49]
	v_mfma_f32_16x16x32_f16 v[58:61], v[220:223], v[236:239], v[58:61]
	v_mfma_f32_16x16x32_f16 v[70:73], v[220:223], v[244:247], v[70:73]
	v_mfma_f32_16x16x32_f16 v[78:81], v[228:231], v[236:239], v[78:81]
	v_mfma_f32_16x16x32_f16 v[86:89], v[228:231], v[244:247], v[86:89]
	v_lshl_add_u64 v[192:193], v[192:193], 0, s[40:41]
	s_mov_b32 m0, s84
	s_barrier
	ds_read_b128 v[196:199], v173 offset:49152
	ds_read_b128 v[200:203], v173 offset:50176
	ds_read_b128 v[204:207], v173 offset:51200
	ds_read_b128 v[212:215], v173 offset:52224
	ds_read_b128 v[216:219], v173 offset:53248
	ds_read_b128 v[220:223], v173 offset:54272
	ds_read_b128 v[224:227], v173 offset:55296
	ds_read_b128 v[228:231], v173 offset:56320
	global_load_lds_dwordx4 v[192:193], off
	v_lshl_add_u64 v[192:193], v[248:249], 0, s[40:41]
	s_mov_b32 m0, s85
	s_nop 0
	global_load_lds_dwordx4 v[192:193], off
	s_barrier
	s_waitcnt lgkmcnt(0)
	v_mfma_f32_16x16x32_f16 v[26:29], v[196:199], v[176:179], v[26:29]
	v_mfma_f32_16x16x32_f16 v[38:41], v[196:199], v[184:187], v[38:41]
	v_mfma_f32_16x16x32_f16 v[50:53], v[204:207], v[176:179], v[50:53]
	v_mfma_f32_16x16x32_f16 v[62:65], v[204:207], v[184:187], v[62:65]
	v_mfma_f32_16x16x32_f16 v[74:77], v[216:219], v[176:179], v[74:77]
	v_mfma_f32_16x16x32_f16 v[82:85], v[216:219], v[184:187], v[82:85]
	v_mfma_f32_16x16x32_f16 v[90:93], v[224:227], v[176:179], v[90:93]
	v_mfma_f32_16x16x32_f16 v[94:97], v[224:227], v[184:187], v[94:97]
	v_mfma_f32_16x16x32_f16 v[26:29], v[200:203], v[180:183], v[26:29]
	v_mfma_f32_16x16x32_f16 v[38:41], v[200:203], v[188:191], v[38:41]
	v_mfma_f32_16x16x32_f16 v[50:53], v[212:215], v[180:183], v[50:53]
	v_mfma_f32_16x16x32_f16 v[62:65], v[212:215], v[188:191], v[62:65]
	v_mfma_f32_16x16x32_f16 v[74:77], v[220:223], v[180:183], v[74:77]
	v_mfma_f32_16x16x32_f16 v[82:85], v[220:223], v[188:191], v[82:85]
	v_mfma_f32_16x16x32_f16 v[90:93], v[228:231], v[180:183], v[90:93]
	v_mfma_f32_16x16x32_f16 v[94:97], v[228:231], v[188:191], v[94:97]
	s_barrier
	v_lshl_add_u64 v[176:177], v[250:251], 0, s[42:43]
	s_mov_b32 m0, s86
	global_load_lds_dwordx4 v[176:177], off
	v_lshl_add_u64 v[176:177], v[252:253], 0, s[42:43]
	s_mov_b32 m0, s87
	s_nop 0
	global_load_lds_dwordx4 v[176:177], off
	s_waitcnt vmcnt(6)
	s_barrier
	v_mfma_f32_16x16x32_f16 v[98:101], v[196:199], v[232:235], v[98:101]
	v_mfma_f32_16x16x32_f16 v[102:105], v[196:199], v[240:243], v[102:105]
	v_mfma_f32_16x16x32_f16 v[106:109], v[204:207], v[232:235], v[106:109]
	v_mfma_f32_16x16x32_f16 v[110:113], v[204:207], v[240:243], v[110:113]
	v_mfma_f32_16x16x32_f16 v[114:117], v[216:219], v[232:235], v[114:117]
	v_mfma_f32_16x16x32_f16 v[118:121], v[216:219], v[240:243], v[118:121]
	v_mfma_f32_16x16x32_f16 v[122:125], v[224:227], v[232:235], v[122:125]
	v_mfma_f32_16x16x32_f16 v[126:129], v[224:227], v[240:243], v[126:129]
	v_mfma_f32_16x16x32_f16 v[98:101], v[200:203], v[236:239], v[98:101]
	v_mfma_f32_16x16x32_f16 v[102:105], v[200:203], v[244:247], v[102:105]
	v_mfma_f32_16x16x32_f16 v[106:109], v[212:215], v[236:239], v[106:109]
	v_mfma_f32_16x16x32_f16 v[110:113], v[212:215], v[244:247], v[110:113]
	v_mfma_f32_16x16x32_f16 v[114:117], v[220:223], v[236:239], v[114:117]
	v_mfma_f32_16x16x32_f16 v[118:121], v[220:223], v[244:247], v[118:121]
	v_mfma_f32_16x16x32_f16 v[122:125], v[228:231], v[236:239], v[122:125]
	v_mfma_f32_16x16x32_f16 v[126:129], v[228:231], v[244:247], v[126:129]
	s_add_i32 s48, s48, 2
	s_add_u32 s46, s46, 0x100
	s_addc_u32 s47, s47, 0
	s_cmp_lt_u32 s48, 4
	s_barrier
	s_cbranch_scc1 .LBB7_239
	s_add_u32 s0, s0, 0x20380
	s_addc_u32 s1, s1, 0
	v_readfirstlane_b32 s5, v174
	v_lshl_add_u64 v[130:131], v[130:131], 1, s[0:1]
	s_mov_b32 m0, s5
	ds_read_b128 v[134:137], v169
	ds_read_b128 v[138:141], v170
	ds_read_b128 v[152:155], v171
	ds_read_b128 v[156:159], v172
	ds_read_b128 v[166:169], v173
	ds_read_b128 v[176:179], v173 offset:1024
	ds_read_b128 v[180:183], v173 offset:2048
	ds_read_b128 v[184:187], v173 offset:3072
	ds_read_b128 v[188:191], v173 offset:4096
	ds_read_b128 v[196:199], v173 offset:5120
	ds_read_b128 v[200:203], v173 offset:6144
	ds_read_b128 v[204:207], v173 offset:7168
	global_load_lds_dwordx4 v[130:131], off
	v_lshl_add_u64 v[130:131], v[132:133], 1, s[0:1]
	v_readfirstlane_b32 s0, v175
	s_mov_b32 m0, s0
	s_nop 0
	global_load_lds_dwordx4 v[130:131], off
	s_barrier
	s_waitcnt lgkmcnt(0)
	v_mfma_f32_16x16x32_f16 v[2:5], v[166:169], v[134:137], v[2:5]
	v_mfma_f32_16x16x32_f16 v[42:45], v[188:191], v[152:155], v[42:45]
	v_mfma_f32_16x16x32_f16 v[54:57], v[200:203], v[134:137], v[54:57]
	v_mfma_f32_16x16x32_f16 v[66:69], v[200:203], v[152:155], v[66:69]
	v_mfma_f32_16x16x32_f16 v[2:5], v[176:179], v[138:141], v[2:5]
	v_mfma_f32_16x16x32_f16 v[6:9], v[166:169], v[152:155], v[6:9]
	v_mfma_f32_16x16x32_f16 v[10:13], v[180:183], v[134:137], v[10:13]
	v_mfma_f32_16x16x32_f16 v[18:21], v[180:183], v[152:155], v[18:21]
	v_mfma_f32_16x16x32_f16 v[30:33], v[188:191], v[134:137], v[30:33]
	v_mfma_f32_16x16x32_f16 v[42:45], v[196:199], v[156:159], v[42:45]
	v_mfma_f32_16x16x32_f16 v[54:57], v[204:207], v[138:141], v[54:57]
	v_mfma_f32_16x16x32_f16 v[66:69], v[204:207], v[156:159], v[66:69]
	v_mfma_f32_16x16x32_f16 v[6:9], v[176:179], v[156:159], v[6:9]
	v_mfma_f32_16x16x32_f16 v[10:13], v[184:187], v[138:141], v[10:13]
	v_mfma_f32_16x16x32_f16 v[18:21], v[184:187], v[156:159], v[18:21]
	v_mfma_f32_16x16x32_f16 v[30:33], v[196:199], v[138:141], v[30:33]
	s_barrier
	ds_read_b128 v[130:133], v161
	ds_read_b128 v[212:215], v162
	ds_read_b128 v[160:163], v163
	ds_read_b128 v[216:219], v164
	s_barrier
	s_waitcnt lgkmcnt(0)
	v_mfma_f32_16x16x32_f16 v[14:17], v[166:169], v[130:133], v[14:17]
	v_mfma_f32_16x16x32_f16 v[78:81], v[200:203], v[130:133], v[78:81]
	v_mfma_f32_16x16x32_f16 v[14:17], v[176:179], v[212:215], v[14:17]
	v_mfma_f32_16x16x32_f16 v[22:25], v[166:169], v[160:163], v[22:25]
	v_mfma_f32_16x16x32_f16 v[34:37], v[180:183], v[130:133], v[34:37]
	v_mfma_f32_16x16x32_f16 v[46:49], v[180:183], v[160:163], v[46:49]
	v_mfma_f32_16x16x32_f16 v[58:61], v[188:191], v[130:133], v[58:61]
	v_mfma_f32_16x16x32_f16 v[70:73], v[188:191], v[160:163], v[70:73]
	v_mfma_f32_16x16x32_f16 v[164:167], v[204:207], v[212:215], v[78:81]
	v_mfma_f32_16x16x32_f16 v[78:81], v[200:203], v[160:163], v[86:89]
	v_mfma_f32_16x16x32_f16 v[22:25], v[176:179], v[216:219], v[22:25]
	v_mfma_f32_16x16x32_f16 v[34:37], v[184:187], v[212:215], v[34:37]
	v_mfma_f32_16x16x32_f16 v[46:49], v[184:187], v[216:219], v[46:49]
	v_mfma_f32_16x16x32_f16 v[58:61], v[196:199], v[212:215], v[58:61]
	v_mfma_f32_16x16x32_f16 v[70:73], v[196:199], v[216:219], v[70:73]
	v_mfma_f32_16x16x32_f16 v[86:89], v[204:207], v[216:219], v[78:81]
	s_barrier
	s_nop 0
	ds_read_b128 v[78:81], v173 offset:16384
	ds_read_b128 v[168:171], v173 offset:17408
	ds_read_b128 v[174:177], v173 offset:18432
	ds_read_b128 v[178:181], v173 offset:19456
	ds_read_b128 v[182:185], v173 offset:20480
	ds_read_b128 v[186:189], v173 offset:21504
	ds_read_b128 v[190:193], v173 offset:22528
	ds_read_b128 v[196:199], v173 offset:23552
	s_waitcnt vmcnt(4)
	s_barrier
	s_waitcnt lgkmcnt(0)
	v_mfma_f32_16x16x32_f16 v[26:29], v[78:81], v[134:137], v[26:29]
	v_mfma_f32_16x16x32_f16 v[38:41], v[78:81], v[152:155], v[38:41]
	v_mfma_f32_16x16x32_f16 v[26:29], v[168:171], v[138:141], v[26:29]
	v_mfma_f32_16x16x32_f16 v[38:41], v[168:171], v[156:159], v[38:41]
	v_mfma_f32_16x16x32_f16 v[50:53], v[174:177], v[134:137], v[50:53]
	v_mfma_f32_16x16x32_f16 v[62:65], v[174:177], v[152:155], v[62:65]
	v_mfma_f32_16x16x32_f16 v[74:77], v[182:185], v[134:137], v[74:77]
	v_mfma_f32_16x16x32_f16 v[82:85], v[182:185], v[152:155], v[82:85]
	v_mfma_f32_16x16x32_f16 v[90:93], v[190:193], v[134:137], v[90:93]
	v_mfma_f32_16x16x32_f16 v[94:97], v[190:193], v[152:155], v[94:97]
	v_mfma_f32_16x16x32_f16 v[50:53], v[178:181], v[138:141], v[50:53]
	v_mfma_f32_16x16x32_f16 v[62:65], v[178:181], v[156:159], v[62:65]
	v_mfma_f32_16x16x32_f16 v[74:77], v[186:189], v[138:141], v[74:77]
	v_mfma_f32_16x16x32_f16 v[82:85], v[186:189], v[156:159], v[82:85]
	v_mfma_f32_16x16x32_f16 v[90:93], v[196:199], v[138:141], v[90:93]
	v_mfma_f32_16x16x32_f16 v[94:97], v[196:199], v[156:159], v[94:97]
	v_mfma_f32_16x16x32_f16 v[98:101], v[78:81], v[130:133], v[98:101]
	v_mfma_f32_16x16x32_f16 v[78:81], v[78:81], v[160:163], v[102:105]
	v_mfma_f32_16x16x32_f16 v[102:105], v[168:171], v[216:219], v[78:81]
	v_mfma_f32_16x16x32_f16 v[78:81], v[174:177], v[130:133], v[106:109]
	v_mfma_f32_16x16x32_f16 v[106:109], v[178:181], v[212:215], v[78:81]
	v_mfma_f32_16x16x32_f16 v[78:81], v[174:177], v[160:163], v[110:113]
	v_mfma_f32_16x16x32_f16 v[200:203], v[178:181], v[216:219], v[78:81]
	v_mfma_f32_16x16x32_f16 v[78:81], v[182:185], v[130:133], v[114:117]
	v_mfma_f32_16x16x32_f16 v[204:207], v[186:189], v[212:215], v[78:81]
	v_mfma_f32_16x16x32_f16 v[78:81], v[182:185], v[160:163], v[118:121]
	v_mfma_f32_16x16x32_f16 v[220:223], v[186:189], v[216:219], v[78:81]
	v_mfma_f32_16x16x32_f16 v[78:81], v[190:193], v[130:133], v[122:125]
	v_mfma_f32_16x16x32_f16 v[98:101], v[168:171], v[212:215], v[98:101]
	v_mfma_f32_16x16x32_f16 v[212:215], v[196:199], v[212:215], v[78:81]
	v_mfma_f32_16x16x32_f16 v[78:81], v[190:193], v[160:163], v[126:129]
	v_mfma_f32_16x16x32_f16 v[196:199], v[196:199], v[216:219], v[78:81]
	s_barrier
	ds_read_b128 v[110:113], v148
	ds_read_b128 v[130:133], v149
	ds_read_b128 v[216:219], v150
	ds_read_b128 v[224:227], v151
	s_nop 0
	ds_read_b128 v[78:81], v173 offset:32768
	ds_read_b128 v[114:117], v173 offset:33792
	ds_read_b128 v[118:121], v173 offset:34816
	ds_read_b128 v[134:137], v173 offset:35840
	ds_read_b128 v[138:141], v173 offset:36864
	ds_read_b128 v[168:171], v173 offset:37888
	ds_read_b128 v[174:177], v173 offset:38912
	ds_read_b128 v[228:231], v173 offset:39936
	s_waitcnt vmcnt(2)
	s_barrier
	s_waitcnt lgkmcnt(0)
	v_mfma_f32_16x16x32_f16 v[2:5], v[78:81], v[110:113], v[2:5]
	v_mfma_f32_16x16x32_f16 v[190:193], v[114:117], v[130:133], v[2:5]
	v_mfma_f32_16x16x32_f16 v[2:5], v[78:81], v[216:219], v[6:9]
	v_mfma_f32_16x16x32_f16 v[158:161], v[114:117], v[224:227], v[2:5]
	v_mfma_f32_16x16x32_f16 v[2:5], v[118:121], v[110:113], v[10:13]
	v_mfma_f32_16x16x32_f16 v[186:189], v[134:137], v[130:133], v[2:5]
	v_mfma_f32_16x16x32_f16 v[2:5], v[118:121], v[216:219], v[18:21]
	v_mfma_f32_16x16x32_f16 v[154:157], v[134:137], v[224:227], v[2:5]
	v_mfma_f32_16x16x32_f16 v[2:5], v[138:141], v[110:113], v[30:33]
	v_mfma_f32_16x16x32_f16 v[182:185], v[168:171], v[130:133], v[2:5]
	v_mfma_f32_16x16x32_f16 v[2:5], v[138:141], v[216:219], v[42:45]
	v_mfma_f32_16x16x32_f16 v[150:153], v[168:171], v[224:227], v[2:5]
	v_mfma_f32_16x16x32_f16 v[2:5], v[174:177], v[110:113], v[54:57]
	v_mfma_f32_16x16x32_f16 v[178:181], v[228:231], v[130:133], v[2:5]
	v_mfma_f32_16x16x32_f16 v[2:5], v[174:177], v[216:219], v[66:69]
	v_mfma_f32_16x16x32_f16 v[146:149], v[228:231], v[224:227], v[2:5]
	s_barrier
	s_nop 4
	ds_read_b128 v[2:5], v142
	ds_read_b128 v[6:9], v143
	ds_read_b128 v[10:13], v144
	ds_read_b128 v[18:21], v145
	s_waitcnt vmcnt(0)
	s_barrier
	s_waitcnt lgkmcnt(0)
	v_mfma_f32_16x16x32_f16 v[14:17], v[78:81], v[2:5], v[14:17]
	v_mfma_f32_16x16x32_f16 v[126:129], v[114:117], v[6:9], v[14:17]
	v_mfma_f32_16x16x32_f16 v[14:17], v[78:81], v[10:13], v[22:25]
	v_mfma_f32_16x16x32_f16 v[78:81], v[114:117], v[18:21], v[14:17]
	v_mfma_f32_16x16x32_f16 v[14:17], v[118:121], v[2:5], v[34:37]
	v_mfma_f32_16x16x32_f16 v[122:125], v[134:137], v[6:9], v[14:17]
	v_mfma_f32_16x16x32_f16 v[14:17], v[118:121], v[10:13], v[46:49]
	v_mfma_f32_16x16x32_f16 v[66:69], v[134:137], v[18:21], v[14:17]
	v_mfma_f32_16x16x32_f16 v[14:17], v[138:141], v[2:5], v[58:61]
	v_mfma_f32_16x16x32_f16 v[118:121], v[168:171], v[6:9], v[14:17]
	v_mfma_f32_16x16x32_f16 v[14:17], v[138:141], v[10:13], v[70:73]
	v_mfma_f32_16x16x32_f16 v[54:57], v[168:171], v[18:21], v[14:17]
	v_mfma_f32_16x16x32_f16 v[14:17], v[174:177], v[2:5], v[164:167]
	v_mfma_f32_16x16x32_f16 v[114:117], v[228:231], v[6:9], v[14:17]
	v_mfma_f32_16x16x32_f16 v[14:17], v[174:177], v[10:13], v[86:89]
	v_mfma_f32_16x16x32_f16 v[42:45], v[228:231], v[18:21], v[14:17]
	s_barrier
	s_nop 4
	ds_read_b128 v[14:17], v173 offset:49152
	ds_read_b128 v[22:25], v173 offset:50176
	ds_read_b128 v[30:33], v173 offset:51200
	ds_read_b128 v[34:37], v173 offset:52224
	ds_read_b128 v[46:49], v173 offset:53248
	ds_read_b128 v[58:61], v173 offset:54272
	ds_read_b128 v[70:73], v173 offset:55296
	ds_read_b128 v[86:89], v173 offset:56320
	s_barrier
	s_waitcnt lgkmcnt(0)
	v_mfma_f32_16x16x32_f16 v[26:29], v[14:17], v[110:113], v[26:29]
	v_mfma_f32_16x16x32_f16 v[174:177], v[22:25], v[130:133], v[26:29]
	v_mfma_f32_16x16x32_f16 v[26:29], v[14:17], v[216:219], v[38:41]
	v_mfma_f32_16x16x32_f16 v[142:145], v[22:25], v[224:227], v[26:29]
	v_mfma_f32_16x16x32_f16 v[26:29], v[30:33], v[110:113], v[50:53]
	v_mfma_f32_16x16x32_f16 v[170:173], v[34:37], v[130:133], v[26:29]
	v_mfma_f32_16x16x32_f16 v[26:29], v[30:33], v[216:219], v[62:65]
	v_mfma_f32_16x16x32_f16 v[138:141], v[34:37], v[224:227], v[26:29]
	v_mfma_f32_16x16x32_f16 v[26:29], v[46:49], v[110:113], v[74:77]
	v_mfma_f32_16x16x32_f16 v[166:169], v[58:61], v[130:133], v[26:29]
	v_mfma_f32_16x16x32_f16 v[26:29], v[46:49], v[216:219], v[82:85]
	v_mfma_f32_16x16x32_f16 v[134:137], v[58:61], v[224:227], v[26:29]
	v_mfma_f32_16x16x32_f16 v[26:29], v[70:73], v[110:113], v[90:93]
	v_mfma_f32_16x16x32_f16 v[162:165], v[86:89], v[130:133], v[26:29]
	v_mfma_f32_16x16x32_f16 v[26:29], v[70:73], v[216:219], v[94:97]
	v_mfma_f32_16x16x32_f16 v[130:133], v[86:89], v[224:227], v[26:29]
	v_mfma_f32_16x16x32_f16 v[26:29], v[14:17], v[2:5], v[98:101]
	v_mfma_f32_16x16x32_f16 v[14:17], v[14:17], v[10:13], v[102:105]
	v_mfma_f32_16x16x32_f16 v[38:41], v[22:25], v[18:21], v[14:17]
	v_mfma_f32_16x16x32_f16 v[14:17], v[30:33], v[2:5], v[106:109]
	v_mfma_f32_16x16x32_f16 v[106:109], v[34:37], v[6:9], v[14:17]
	v_mfma_f32_16x16x32_f16 v[14:17], v[30:33], v[10:13], v[200:203]
	v_mfma_f32_16x16x32_f16 v[110:113], v[22:25], v[6:9], v[26:29]
	v_mfma_f32_16x16x32_f16 v[26:29], v[34:37], v[18:21], v[14:17]
	v_mfma_f32_16x16x32_f16 v[14:17], v[46:49], v[2:5], v[204:207]
	v_mfma_f32_16x16x32_f16 v[2:5], v[70:73], v[2:5], v[212:215]
	v_mfma_f32_16x16x32_f16 v[102:105], v[58:61], v[6:9], v[14:17]
	v_mfma_f32_16x16x32_f16 v[14:17], v[46:49], v[10:13], v[220:223]
	v_mfma_f32_16x16x32_f16 v[98:101], v[86:89], v[6:9], v[2:5]
	v_mfma_f32_16x16x32_f16 v[2:5], v[70:73], v[10:13], v[196:199]
	v_mfma_f32_16x16x32_f16 v[14:17], v[58:61], v[18:21], v[14:17]
	v_mfma_f32_16x16x32_f16 v[2:5], v[86:89], v[18:21], v[2:5]
	s_cmpk_gt_u32 s65, 0xff
	s_barrier
	s_cbranch_scc1 .LBB7_242
	s_barrier

	.amdhsa_kernel _Z14gemm256_kernelILi0ELi512ELi1024EEv8GemmArgs
		.amdhsa_group_segment_fixed_size 0
		.amdhsa_private_segment_fixed_size 0
		.amdhsa_kernarg_size 592
		.amdhsa_user_sgpr_count 2
		.amdhsa_user_sgpr_dispatch_ptr 0
		.amdhsa_user_sgpr_queue_ptr 0
		.amdhsa_user_sgpr_kernarg_segment_ptr 1
		.amdhsa_user_sgpr_dispatch_id 0
		.amdhsa_user_sgpr_kernarg_preload_length 0
		.amdhsa_user_sgpr_kernarg_preload_offset 0
		.amdhsa_user_sgpr_private_segment_size 0
		.amdhsa_uses_dynamic_stack 0
		.amdhsa_enable_private_segment 0
		.amdhsa_system_sgpr_workgroup_id_x 1
		.amdhsa_system_sgpr_workgroup_id_y 0
		.amdhsa_system_sgpr_workgroup_id_z 0
		.amdhsa_system_sgpr_workgroup_info 0
		.amdhsa_system_vgpr_workitem_id 0
		.amdhsa_next_free_vgpr 256
		.amdhsa_next_free_sgpr 88
		.amdhsa_accum_offset 256
		.amdhsa_reserve_vcc 1
		.amdhsa_float_round_mode_32 0
		.amdhsa_float_round_mode_16_64 0
		.amdhsa_float_denorm_mode_32 3
		.amdhsa_float_denorm_mode_16_64 3
		.amdhsa_dx10_clamp 1
		.amdhsa_ieee_mode 1
		.amdhsa_fp16_overflow 0
		.amdhsa_tg_split 0
		.amdhsa_exception_fp_ieee_invalid_op 0
		.amdhsa_exception_fp_denorm_src 0
		.amdhsa_exception_fp_ieee_div_zero 0
		.amdhsa_exception_fp_ieee_overflow 0
		.amdhsa_exception_fp_ieee_underflow 0
		.amdhsa_exception_fp_ieee_inexact 0
		.amdhsa_exception_int_div_zero 0
	.end_amdhsa_kernel

.LBB8_40:
	v_lshlrev_b32_e32 v2, 12, v2
	s_lshl_b32 s49, s62, 6
	v_and_b32_e32 v2, 0xffffe000, v2
	v_lshlrev_b32_e32 v4, 12, v4
	s_lshl_b32 s48, s64, 13
	s_and_b32 s49, s49, 0x3000
	v_lshl_add_u32 v2, v3, 9, v2
	v_and_b32_e32 v4, 0xffffe000, v4
	v_and_b32_e32 v10, 48, v172
	v_lshlrev_b32_e32 v11, 6, v172
	v_or_b32_e32 v2, v2, v5
	s_add_u32 s46, s24, s46
	v_lshl_add_u32 v4, v7, 9, v4
	v_and_or_b32 v10, v11, s57, v10
	v_lshlrev_b32_e32 v11, 2, v172
	v_add_u32_sdwa v2, v2, sext(v6) dst_sel:DWORD dst_unused:UNUSED_PAD src0_sel:DWORD src1_sel:WORD_0
	s_addc_u32 s47, s25, s47
	v_or_b32_e32 v4, v4, v8
	v_and_b32_e32 v11, 32, v11
	v_ashrrev_i32_e32 v3, 31, v2
	v_add_u32_sdwa v4, v4, sext(v9) dst_sel:DWORD dst_unused:UNUSED_PAD src0_sel:DWORD src1_sel:WORD_0
	s_add_u32 s44, s22, s44
	v_xad_u32 v170, v10, v11, 0
	s_waitcnt vmcnt(6)
	v_lshlrev_b64 v[2:3], 1, v[2:3]
	v_ashrrev_i32_e32 v5, 31, v4
	s_addc_u32 s45, s23, s45
	v_add_u32_e32 v10, s49, v170
	v_lshl_add_u64 v[134:135], s[46:47], 0, v[2:3]
	v_lshlrev_b64 v[4:5], 1, v[4:5]
	v_lshl_add_u64 v[138:139], s[44:45], 0, v[2:3]
	v_mov_b32_e32 v2, 0
	v_add_u32_e32 v171, 0x10000, v10
	v_add_u32_e32 v173, 0x10400, v10
	v_add_u32_e32 v174, 0x10800, v10
	v_add_u32_e32 v175, 0x10c00, v10
	v_add_u32_e32 v162, 0x14000, v10
	v_add_u32_e32 v163, 0x14400, v10
	v_add_u32_e32 v164, 0x14800, v10
	v_add_u32_e32 v165, 0x14c00, v10
	v_add_u32_e32 v144, 0x18000, v10
	v_add_u32_e32 v145, 0x18400, v10
	v_add_u32_e32 v146, 0x18800, v10
	v_add_u32_e32 v147, 0x18c00, v10
	v_add_u32_e32 v150, 0x1c000, v10
	v_add_u32_e32 v151, 0x1c400, v10
	v_add_u32_e32 v152, 0x1c800, v10
	v_add_u32_e32 v153, 0x1cc00, v10
	v_lshl_add_u64 v[136:137], s[46:47], 0, v[4:5]
	v_lshl_add_u64 v[140:141], s[44:45], 0, v[4:5]
	s_mov_b32 s46, -2
	s_mov_b64 s[44:45], 0
	v_mov_b32_e32 v3, v2
	v_mov_b32_e32 v4, v2
	v_mov_b32_e32 v5, v2
	v_mov_b32_e32 v6, v2
	v_mov_b32_e32 v7, v2
	v_mov_b32_e32 v8, v2
	v_mov_b32_e32 v9, v2
	v_mov_b32_e32 v10, v2
	v_mov_b32_e32 v11, v2
	v_mov_b32_e32 v12, v2
	v_mov_b32_e32 v13, v2
	v_mov_b32_e32 v14, v2
	v_mov_b32_e32 v15, v2
	v_mov_b32_e32 v16, v2
	v_mov_b32_e32 v17, v2
	v_mov_b32_e32 v18, v2
	v_mov_b32_e32 v19, v2
	v_mov_b32_e32 v20, v2
	v_mov_b32_e32 v21, v2
	v_mov_b32_e32 v22, v2
	v_mov_b32_e32 v23, v2
	v_mov_b32_e32 v24, v2
	v_mov_b32_e32 v25, v2
	v_mov_b32_e32 v26, v2
	v_mov_b32_e32 v27, v2
	v_mov_b32_e32 v28, v2
	v_mov_b32_e32 v29, v2
	v_mov_b32_e32 v30, v2
	v_mov_b32_e32 v31, v2
	v_mov_b32_e32 v32, v2
	v_mov_b32_e32 v33, v2
	v_mov_b32_e32 v34, v2
	v_mov_b32_e32 v35, v2
	v_mov_b32_e32 v36, v2
	v_mov_b32_e32 v37, v2
	v_mov_b32_e32 v38, v2
	v_mov_b32_e32 v39, v2
	v_mov_b32_e32 v40, v2
	v_mov_b32_e32 v41, v2
	v_mov_b32_e32 v42, v2
	v_mov_b32_e32 v43, v2
	v_mov_b32_e32 v44, v2
	v_mov_b32_e32 v45, v2
	v_mov_b32_e32 v46, v2
	v_mov_b32_e32 v47, v2
	v_mov_b32_e32 v48, v2
	v_mov_b32_e32 v49, v2
	v_mov_b32_e32 v50, v2
	v_mov_b32_e32 v51, v2
	v_mov_b32_e32 v52, v2
	v_mov_b32_e32 v53, v2
	v_mov_b32_e32 v54, v2
	v_mov_b32_e32 v55, v2
	v_mov_b32_e32 v56, v2
	v_mov_b32_e32 v57, v2
	v_mov_b32_e32 v58, v2
	v_mov_b32_e32 v59, v2
	v_mov_b32_e32 v60, v2
	v_mov_b32_e32 v61, v2
	v_mov_b32_e32 v62, v2
	v_mov_b32_e32 v63, v2
	v_mov_b32_e32 v64, v2
	v_mov_b32_e32 v65, v2
	v_mov_b32_e32 v66, v2
	v_mov_b32_e32 v67, v2
	v_mov_b32_e32 v68, v2
	v_mov_b32_e32 v69, v2
	v_mov_b32_e32 v70, v2
	v_mov_b32_e32 v71, v2
	v_mov_b32_e32 v72, v2
	v_mov_b32_e32 v73, v2
	v_mov_b32_e32 v74, v2
	v_mov_b32_e32 v75, v2
	v_mov_b32_e32 v76, v2
	v_mov_b32_e32 v77, v2
	v_mov_b32_e32 v78, v2
	v_mov_b32_e32 v79, v2
	v_mov_b32_e32 v80, v2
	v_mov_b32_e32 v81, v2
	v_mov_b32_e32 v82, v2
	v_mov_b32_e32 v83, v2
	v_mov_b32_e32 v84, v2
	v_mov_b32_e32 v85, v2
	v_mov_b32_e32 v86, v2
	v_mov_b32_e32 v87, v2
	v_mov_b32_e32 v88, v2
	v_mov_b32_e32 v89, v2
	v_mov_b32_e32 v90, v2
	v_mov_b32_e32 v91, v2
	v_mov_b32_e32 v92, v2
	v_mov_b32_e32 v93, v2
	v_mov_b32_e32 v94, v2
	v_mov_b32_e32 v95, v2
	v_mov_b32_e32 v96, v2
	v_mov_b32_e32 v97, v2
	v_mov_b32_e32 v98, v2
	v_mov_b32_e32 v99, v2
	v_mov_b32_e32 v100, v2
	v_mov_b32_e32 v101, v2
	v_mov_b32_e32 v102, v2
	v_mov_b32_e32 v103, v2
	v_mov_b32_e32 v104, v2
	v_mov_b32_e32 v105, v2
	v_mov_b32_e32 v106, v2
	v_mov_b32_e32 v107, v2
	v_mov_b32_e32 v108, v2
	v_mov_b32_e32 v109, v2
	v_mov_b32_e32 v110, v2
	v_mov_b32_e32 v111, v2
	v_mov_b32_e32 v112, v2
	v_mov_b32_e32 v113, v2
	v_mov_b32_e32 v114, v2
	v_mov_b32_e32 v115, v2
	v_mov_b32_e32 v116, v2
	v_mov_b32_e32 v117, v2
	v_mov_b32_e32 v118, v2
	v_mov_b32_e32 v119, v2
	v_mov_b32_e32 v120, v2
	v_mov_b32_e32 v121, v2
	v_mov_b32_e32 v122, v2
	v_mov_b32_e32 v123, v2
	v_mov_b32_e32 v124, v2
	v_mov_b32_e32 v125, v2
	v_mov_b32_e32 v126, v2
	v_mov_b32_e32 v127, v2
	v_mov_b32_e32 v128, v2
	v_mov_b32_e32 v129, v2
	v_add_u32_e32 v177, 0xc000, v148
	v_add_u32_e32 v178, 0xe000, v148
	s_nop 0
	v_readfirstlane_b32 s75, v177
	v_readfirstlane_b32 s76, v178
	v_readfirstlane_b32 s77, v142
	v_readfirstlane_b32 s78, v143
	v_readfirstlane_b32 s79, v148
	v_readfirstlane_b32 s80, v149
	v_readfirstlane_b32 s81, v154
	v_readfirstlane_b32 s82, v155
	v_readfirstlane_b32 s83, v156
	v_readfirstlane_b32 s84, v157
	v_readfirstlane_b32 s85, v158
	v_readfirstlane_b32 s86, v160
	v_readfirstlane_b32 s87, v161
	v_readfirstlane_b32 s88, v166
	v_readfirstlane_b32 s89, v168
	v_readfirstlane_b32 s90, v169
	s_barrier
	s_barrier
.LBB8_41:
	ds_read_b128 v[182:185], v171
	ds_read_b128 v[186:189], v173
	ds_read_b128 v[190:193], v174
	ds_read_b128 v[194:197], v175
	v_add_u32_e32 v177, 0xc000, v148
	v_lshl_add_u64 v[246:247], v[134:135], 0, s[44:45]
	v_add_u32_e32 v176, s48, v170
	v_lshl_add_u64 v[178:179], v[246:247], 0, s[28:29]
	s_mov_b32 m0, s75
	ds_read_b128 v[198:201], v176
	ds_read_b128 v[202:205], v176 offset:1024
	ds_read_b128 v[206:209], v176 offset:2048
	ds_read_b128 v[210:213], v176 offset:3072
	ds_read_b128 v[214:217], v176 offset:4096
	ds_read_b128 v[218:221], v176 offset:5120
	ds_read_b128 v[222:225], v176 offset:6144
	ds_read_b128 v[226:229], v176 offset:7168
	global_load_lds_dwordx4 v[178:179], off
	v_add_u32_e32 v178, 0xe000, v148
	v_lshl_add_u64 v[248:249], v[136:137], 0, s[44:45]
	v_lshl_add_u64 v[230:231], v[248:249], 0, s[28:29]
	s_mov_b32 m0, s76
	s_nop 0
	global_load_lds_dwordx4 v[230:231], off
	s_waitcnt lgkmcnt(8)
	s_barrier
	s_waitcnt lgkmcnt(0)
	v_mfma_f32_16x16x32_f16 v[126:129], v[198:201], v[182:185], v[126:129]
	v_mfma_f32_16x16x32_f16 v[122:125], v[198:201], v[190:193], v[122:125]
	v_mfma_f32_16x16x32_f16 v[118:121], v[206:209], v[182:185], v[118:121]
	v_mfma_f32_16x16x32_f16 v[114:117], v[206:209], v[190:193], v[114:117]
	v_mfma_f32_16x16x32_f16 v[110:113], v[214:217], v[182:185], v[110:113]
	v_mfma_f32_16x16x32_f16 v[106:109], v[214:217], v[190:193], v[106:109]
	v_mfma_f32_16x16x32_f16 v[102:105], v[222:225], v[182:185], v[102:105]
	v_mfma_f32_16x16x32_f16 v[98:101], v[222:225], v[190:193], v[98:101]
	v_mfma_f32_16x16x32_f16 v[126:129], v[202:205], v[186:189], v[126:129]
	v_mfma_f32_16x16x32_f16 v[122:125], v[202:205], v[194:197], v[122:125]
	v_mfma_f32_16x16x32_f16 v[118:121], v[210:213], v[186:189], v[118:121]
	v_mfma_f32_16x16x32_f16 v[114:117], v[210:213], v[194:197], v[114:117]
	v_mfma_f32_16x16x32_f16 v[110:113], v[218:221], v[186:189], v[110:113]
	v_mfma_f32_16x16x32_f16 v[106:109], v[218:221], v[194:197], v[106:109]
	v_mfma_f32_16x16x32_f16 v[102:105], v[226:229], v[186:189], v[102:105]
	v_mfma_f32_16x16x32_f16 v[98:101], v[226:229], v[194:197], v[98:101]
	s_barrier
	v_lshl_add_u64 v[250:251], v[138:139], 0, s[44:45]
	v_lshl_add_u64 v[252:253], v[250:251], 0, s[30:31]
	s_mov_b32 m0, s77
	ds_read_b128 v[230:233], v162
	ds_read_b128 v[234:237], v163
	ds_read_b128 v[238:241], v164
	ds_read_b128 v[242:245], v165
	global_load_lds_dwordx4 v[252:253], off
	v_lshl_add_u64 v[252:253], v[140:141], 0, s[44:45]
	v_lshl_add_u64 v[254:255], v[252:253], 0, s[30:31]
	s_mov_b32 m0, s78
	s_nop 0
	global_load_lds_dwordx4 v[254:255], off
	s_barrier
	s_waitcnt lgkmcnt(0)
	v_mfma_f32_16x16x32_f16 v[94:97], v[198:201], v[230:233], v[94:97]
	v_mfma_f32_16x16x32_f16 v[90:93], v[198:201], v[238:241], v[90:93]
	v_mfma_f32_16x16x32_f16 v[86:89], v[206:209], v[230:233], v[86:89]
	v_mfma_f32_16x16x32_f16 v[82:85], v[206:209], v[238:241], v[82:85]
	v_mfma_f32_16x16x32_f16 v[78:81], v[214:217], v[230:233], v[78:81]
	v_mfma_f32_16x16x32_f16 v[74:77], v[214:217], v[238:241], v[74:77]
	v_mfma_f32_16x16x32_f16 v[70:73], v[222:225], v[230:233], v[70:73]
	v_mfma_f32_16x16x32_f16 v[66:69], v[222:225], v[238:241], v[66:69]
	v_mfma_f32_16x16x32_f16 v[94:97], v[202:205], v[234:237], v[94:97]
	v_mfma_f32_16x16x32_f16 v[90:93], v[202:205], v[242:245], v[90:93]
	v_mfma_f32_16x16x32_f16 v[86:89], v[210:213], v[234:237], v[86:89]
	v_mfma_f32_16x16x32_f16 v[82:85], v[210:213], v[242:245], v[82:85]
	v_mfma_f32_16x16x32_f16 v[78:81], v[218:221], v[234:237], v[78:81]
	v_mfma_f32_16x16x32_f16 v[74:77], v[218:221], v[242:245], v[74:77]
	v_mfma_f32_16x16x32_f16 v[70:73], v[226:229], v[234:237], v[70:73]
	v_mfma_f32_16x16x32_f16 v[66:69], v[226:229], v[242:245], v[66:69]
	v_lshl_add_u64 v[254:255], v[246:247], 0, s[30:31]
	s_mov_b32 m0, s79
	s_barrier
	ds_read_b128 v[198:201], v176 offset:16384
	ds_read_b128 v[202:205], v176 offset:17408
	ds_read_b128 v[206:209], v176 offset:18432
	ds_read_b128 v[210:213], v176 offset:19456
	ds_read_b128 v[214:217], v176 offset:20480
	ds_read_b128 v[218:221], v176 offset:21504
	ds_read_b128 v[222:225], v176 offset:22528
	ds_read_b128 v[226:229], v176 offset:23552
	global_load_lds_dwordx4 v[254:255], off
	v_lshl_add_u64 v[254:255], v[248:249], 0, s[30:31]
	s_mov_b32 m0, s80
	s_nop 0
	global_load_lds_dwordx4 v[254:255], off
	s_barrier
	s_waitcnt lgkmcnt(0)
	v_mfma_f32_16x16x32_f16 v[62:65], v[198:201], v[182:185], v[62:65]
	v_mfma_f32_16x16x32_f16 v[58:61], v[198:201], v[190:193], v[58:61]
	v_mfma_f32_16x16x32_f16 v[54:57], v[206:209], v[182:185], v[54:57]
	v_mfma_f32_16x16x32_f16 v[50:53], v[206:209], v[190:193], v[50:53]
	v_mfma_f32_16x16x32_f16 v[46:49], v[214:217], v[182:185], v[46:49]
	v_mfma_f32_16x16x32_f16 v[42:45], v[214:217], v[190:193], v[42:45]
	v_mfma_f32_16x16x32_f16 v[38:41], v[222:225], v[182:185], v[38:41]
	v_mfma_f32_16x16x32_f16 v[34:37], v[222:225], v[190:193], v[34:37]
	v_mfma_f32_16x16x32_f16 v[62:65], v[202:205], v[186:189], v[62:65]
	v_mfma_f32_16x16x32_f16 v[58:61], v[202:205], v[194:197], v[58:61]
	v_mfma_f32_16x16x32_f16 v[54:57], v[210:213], v[186:189], v[54:57]
	v_mfma_f32_16x16x32_f16 v[50:53], v[210:213], v[194:197], v[50:53]
	v_mfma_f32_16x16x32_f16 v[46:49], v[218:221], v[186:189], v[46:49]
	v_mfma_f32_16x16x32_f16 v[42:45], v[218:221], v[194:197], v[42:45]
	v_mfma_f32_16x16x32_f16 v[38:41], v[226:229], v[186:189], v[38:41]
	v_mfma_f32_16x16x32_f16 v[34:37], v[226:229], v[194:197], v[34:37]
	s_barrier
	v_lshl_add_u64 v[182:183], v[250:251], 0, s[34:35]
	s_mov_b32 m0, s81
	global_load_lds_dwordx4 v[182:183], off
	v_lshl_add_u64 v[182:183], v[252:253], 0, s[34:35]
	s_mov_b32 m0, s82
	s_nop 0
	global_load_lds_dwordx4 v[182:183], off
	s_waitcnt vmcnt(6)
	s_barrier
	v_mfma_f32_16x16x32_f16 v[30:33], v[198:201], v[230:233], v[30:33]
	v_mfma_f32_16x16x32_f16 v[26:29], v[198:201], v[238:241], v[26:29]
	v_mfma_f32_16x16x32_f16 v[22:25], v[206:209], v[230:233], v[22:25]
	v_mfma_f32_16x16x32_f16 v[18:21], v[206:209], v[238:241], v[18:21]
	v_mfma_f32_16x16x32_f16 v[14:17], v[214:217], v[230:233], v[14:17]
	v_mfma_f32_16x16x32_f16 v[10:13], v[214:217], v[238:241], v[10:13]
	v_mfma_f32_16x16x32_f16 v[6:9], v[222:225], v[230:233], v[6:9]
	v_mfma_f32_16x16x32_f16 v[2:5], v[222:225], v[238:241], v[2:5]
	v_mfma_f32_16x16x32_f16 v[30:33], v[202:205], v[234:237], v[30:33]
	v_mfma_f32_16x16x32_f16 v[26:29], v[202:205], v[242:245], v[26:29]
	v_mfma_f32_16x16x32_f16 v[22:25], v[210:213], v[234:237], v[22:25]
	v_mfma_f32_16x16x32_f16 v[18:21], v[210:213], v[242:245], v[18:21]
	v_mfma_f32_16x16x32_f16 v[14:17], v[218:221], v[234:237], v[14:17]
	v_mfma_f32_16x16x32_f16 v[10:13], v[218:221], v[242:245], v[10:13]
	v_mfma_f32_16x16x32_f16 v[6:9], v[226:229], v[234:237], v[6:9]
	v_mfma_f32_16x16x32_f16 v[2:5], v[226:229], v[242:245], v[2:5]
	s_barrier
	ds_read_b128 v[182:185], v144
	ds_read_b128 v[186:189], v145
	ds_read_b128 v[190:193], v146
	ds_read_b128 v[194:197], v147
	v_lshl_add_u64 v[230:231], v[246:247], 0, s[34:35]
	s_mov_b32 m0, s83
	ds_read_b128 v[198:201], v176 offset:32768
	ds_read_b128 v[202:205], v176 offset:33792
	ds_read_b128 v[206:209], v176 offset:34816
	ds_read_b128 v[210:213], v176 offset:35840
	ds_read_b128 v[214:217], v176 offset:36864
	ds_read_b128 v[218:221], v176 offset:37888
	ds_read_b128 v[222:225], v176 offset:38912
	ds_read_b128 v[226:229], v176 offset:39936
	global_load_lds_dwordx4 v[230:231], off
	v_lshl_add_u64 v[230:231], v[248:249], 0, s[34:35]
	s_mov_b32 m0, s84
	s_nop 0
	global_load_lds_dwordx4 v[230:231], off
	s_waitcnt lgkmcnt(8)
	s_barrier
	s_waitcnt lgkmcnt(0)
	v_mfma_f32_16x16x32_f16 v[126:129], v[198:201], v[182:185], v[126:129]
	v_mfma_f32_16x16x32_f16 v[122:125], v[198:201], v[190:193], v[122:125]
	v_mfma_f32_16x16x32_f16 v[118:121], v[206:209], v[182:185], v[118:121]
	v_mfma_f32_16x16x32_f16 v[114:117], v[206:209], v[190:193], v[114:117]
	v_mfma_f32_16x16x32_f16 v[110:113], v[214:217], v[182:185], v[110:113]
	v_mfma_f32_16x16x32_f16 v[106:109], v[214:217], v[190:193], v[106:109]
	v_mfma_f32_16x16x32_f16 v[102:105], v[222:225], v[182:185], v[102:105]
	v_mfma_f32_16x16x32_f16 v[98:101], v[222:225], v[190:193], v[98:101]
	v_mfma_f32_16x16x32_f16 v[126:129], v[202:205], v[186:189], v[126:129]
	v_mfma_f32_16x16x32_f16 v[122:125], v[202:205], v[194:197], v[122:125]
	v_mfma_f32_16x16x32_f16 v[118:121], v[210:213], v[186:189], v[118:121]
	v_mfma_f32_16x16x32_f16 v[114:117], v[210:213], v[194:197], v[114:117]
	v_mfma_f32_16x16x32_f16 v[110:113], v[218:221], v[186:189], v[110:113]
	v_mfma_f32_16x16x32_f16 v[106:109], v[218:221], v[194:197], v[106:109]
	v_mfma_f32_16x16x32_f16 v[102:105], v[226:229], v[186:189], v[102:105]
	v_mfma_f32_16x16x32_f16 v[98:101], v[226:229], v[194:197], v[98:101]
	s_barrier
	v_lshl_add_u64 v[254:255], v[250:251], 0, s[36:37]
	s_mov_b32 m0, s85
	ds_read_b128 v[230:233], v150
	ds_read_b128 v[234:237], v151
	ds_read_b128 v[238:241], v152
	ds_read_b128 v[242:245], v153
	global_load_lds_dwordx4 v[254:255], off
	v_lshl_add_u64 v[254:255], v[252:253], 0, s[36:37]
	s_mov_b32 m0, s86
	s_nop 0
	global_load_lds_dwordx4 v[254:255], off
	s_barrier
	s_waitcnt lgkmcnt(0)
	v_mfma_f32_16x16x32_f16 v[94:97], v[198:201], v[230:233], v[94:97]
	v_mfma_f32_16x16x32_f16 v[90:93], v[198:201], v[238:241], v[90:93]
	v_mfma_f32_16x16x32_f16 v[86:89], v[206:209], v[230:233], v[86:89]
	v_mfma_f32_16x16x32_f16 v[82:85], v[206:209], v[238:241], v[82:85]
	v_mfma_f32_16x16x32_f16 v[78:81], v[214:217], v[230:233], v[78:81]
	v_mfma_f32_16x16x32_f16 v[74:77], v[214:217], v[238:241], v[74:77]
	v_mfma_f32_16x16x32_f16 v[70:73], v[222:225], v[230:233], v[70:73]
	v_mfma_f32_16x16x32_f16 v[66:69], v[222:225], v[238:241], v[66:69]
	v_mfma_f32_16x16x32_f16 v[94:97], v[202:205], v[234:237], v[94:97]
	v_mfma_f32_16x16x32_f16 v[90:93], v[202:205], v[242:245], v[90:93]
	v_mfma_f32_16x16x32_f16 v[86:89], v[210:213], v[234:237], v[86:89]
	v_mfma_f32_16x16x32_f16 v[82:85], v[210:213], v[242:245], v[82:85]
	v_mfma_f32_16x16x32_f16 v[78:81], v[218:221], v[234:237], v[78:81]
	v_mfma_f32_16x16x32_f16 v[74:77], v[218:221], v[242:245], v[74:77]
	v_mfma_f32_16x16x32_f16 v[70:73], v[226:229], v[234:237], v[70:73]
	v_mfma_f32_16x16x32_f16 v[66:69], v[226:229], v[242:245], v[66:69]
	v_lshl_add_u64 v[246:247], v[246:247], 0, s[36:37]
	s_mov_b32 m0, s87
	s_barrier
	ds_read_b128 v[198:201], v176 offset:49152
	ds_read_b128 v[202:205], v176 offset:50176
	ds_read_b128 v[206:209], v176 offset:51200
	ds_read_b128 v[210:213], v176 offset:52224
	ds_read_b128 v[214:217], v176 offset:53248
	ds_read_b128 v[218:221], v176 offset:54272
	ds_read_b128 v[222:225], v176 offset:55296
	ds_read_b128 v[226:229], v176 offset:56320
	global_load_lds_dwordx4 v[246:247], off
	v_lshl_add_u64 v[246:247], v[248:249], 0, s[36:37]
	s_mov_b32 m0, s88
	s_nop 0
	global_load_lds_dwordx4 v[246:247], off
	s_barrier
	s_waitcnt lgkmcnt(0)
	v_mfma_f32_16x16x32_f16 v[62:65], v[198:201], v[182:185], v[62:65]
	v_mfma_f32_16x16x32_f16 v[58:61], v[198:201], v[190:193], v[58:61]
	v_mfma_f32_16x16x32_f16 v[54:57], v[206:209], v[182:185], v[54:57]
	v_mfma_f32_16x16x32_f16 v[50:53], v[206:209], v[190:193], v[50:53]
	v_mfma_f32_16x16x32_f16 v[46:49], v[214:217], v[182:185], v[46:49]
	v_mfma_f32_16x16x32_f16 v[42:45], v[214:217], v[190:193], v[42:45]
	v_mfma_f32_16x16x32_f16 v[38:41], v[222:225], v[182:185], v[38:41]
	v_mfma_f32_16x16x32_f16 v[34:37], v[222:225], v[190:193], v[34:37]
	v_mfma_f32_16x16x32_f16 v[62:65], v[202:205], v[186:189], v[62:65]
	v_mfma_f32_16x16x32_f16 v[58:61], v[202:205], v[194:197], v[58:61]
	v_mfma_f32_16x16x32_f16 v[54:57], v[210:213], v[186:189], v[54:57]
	v_mfma_f32_16x16x32_f16 v[50:53], v[210:213], v[194:197], v[50:53]
	v_mfma_f32_16x16x32_f16 v[46:49], v[218:221], v[186:189], v[46:49]
	v_mfma_f32_16x16x32_f16 v[42:45], v[218:221], v[194:197], v[42:45]
	v_mfma_f32_16x16x32_f16 v[38:41], v[226:229], v[186:189], v[38:41]
	v_mfma_f32_16x16x32_f16 v[34:37], v[226:229], v[194:197], v[34:37]
	s_barrier
	v_lshl_add_u64 v[182:183], v[250:251], 0, s[38:39]
	s_mov_b32 m0, s89
	global_load_lds_dwordx4 v[182:183], off
	v_lshl_add_u64 v[182:183], v[252:253], 0, s[38:39]
	s_mov_b32 m0, s90
	s_nop 0
	global_load_lds_dwordx4 v[182:183], off
	s_waitcnt vmcnt(6)
	s_barrier
	v_mfma_f32_16x16x32_f16 v[30:33], v[198:201], v[230:233], v[30:33]
	v_mfma_f32_16x16x32_f16 v[26:29], v[198:201], v[238:241], v[26:29]
	v_mfma_f32_16x16x32_f16 v[22:25], v[206:209], v[230:233], v[22:25]
	v_mfma_f32_16x16x32_f16 v[18:21], v[206:209], v[238:241], v[18:21]
	v_mfma_f32_16x16x32_f16 v[14:17], v[214:217], v[230:233], v[14:17]
	v_mfma_f32_16x16x32_f16 v[10:13], v[214:217], v[238:241], v[10:13]
	v_mfma_f32_16x16x32_f16 v[6:9], v[222:225], v[230:233], v[6:9]
	v_mfma_f32_16x16x32_f16 v[2:5], v[222:225], v[238:241], v[2:5]
	v_mfma_f32_16x16x32_f16 v[30:33], v[202:205], v[234:237], v[30:33]
	v_mfma_f32_16x16x32_f16 v[26:29], v[202:205], v[242:245], v[26:29]
	v_mfma_f32_16x16x32_f16 v[22:25], v[210:213], v[234:237], v[22:25]
	v_mfma_f32_16x16x32_f16 v[18:21], v[210:213], v[242:245], v[18:21]
	v_mfma_f32_16x16x32_f16 v[14:17], v[218:221], v[234:237], v[14:17]
	v_mfma_f32_16x16x32_f16 v[10:13], v[218:221], v[242:245], v[10:13]
	v_mfma_f32_16x16x32_f16 v[6:9], v[226:229], v[234:237], v[6:9]
	v_mfma_f32_16x16x32_f16 v[2:5], v[226:229], v[242:245], v[2:5]
	s_add_i32 s46, s46, 2
	s_add_u32 s44, s44, 0x100
	s_addc_u32 s45, s45, 0
	s_cmp_lt_u32 s46, 4
	s_barrier
	s_cbranch_scc1 .LBB8_41
	s_add_u32 s42, s42, 0x20380
	s_addc_u32 s43, s43, 0
	v_readfirstlane_b32 s44, v177
	v_lshl_add_u64 v[130:131], v[130:131], 1, s[42:43]
	s_mov_b32 m0, s44
	ds_read_b128 v[134:137], v171
	ds_read_b128 v[138:141], v173
	ds_read_b128 v[154:157], v174
	ds_read_b128 v[168:171], v175
	ds_read_b128 v[182:185], v176
	ds_read_b128 v[186:189], v176 offset:1024
	ds_read_b128 v[190:193], v176 offset:2048
	ds_read_b128 v[194:197], v176 offset:3072
	ds_read_b128 v[198:201], v176 offset:4096
	ds_read_b128 v[202:205], v176 offset:5120
	ds_read_b128 v[206:209], v176 offset:6144
	ds_read_b128 v[210:213], v176 offset:7168
	global_load_lds_dwordx4 v[130:131], off
	v_lshl_add_u64 v[130:131], v[132:133], 1, s[42:43]
	v_readfirstlane_b32 s42, v178
	s_mov_b32 m0, s42
	s_nop 0
	global_load_lds_dwordx4 v[130:131], off
	s_barrier
	s_waitcnt lgkmcnt(0)
	v_mfma_f32_16x16x32_f16 v[122:125], v[182:185], v[154:157], v[122:125]
	v_mfma_f32_16x16x32_f16 v[110:113], v[198:201], v[134:137], v[110:113]
	v_mfma_f32_16x16x32_f16 v[98:101], v[206:209], v[154:157], v[98:101]
	v_mfma_f32_16x16x32_f16 v[126:129], v[182:185], v[134:137], v[126:129]
	v_mfma_f32_16x16x32_f16 v[122:125], v[186:189], v[168:171], v[122:125]
	v_mfma_f32_16x16x32_f16 v[118:121], v[190:193], v[134:137], v[118:121]
	v_mfma_f32_16x16x32_f16 v[114:117], v[190:193], v[154:157], v[114:117]
	v_mfma_f32_16x16x32_f16 v[130:133], v[202:205], v[138:141], v[110:113]
	v_mfma_f32_16x16x32_f16 v[106:109], v[198:201], v[154:157], v[106:109]
	v_mfma_f32_16x16x32_f16 v[102:105], v[206:209], v[134:137], v[102:105]
	v_mfma_f32_16x16x32_f16 v[98:101], v[210:213], v[168:171], v[98:101]
	v_mfma_f32_16x16x32_f16 v[126:129], v[186:189], v[138:141], v[126:129]
	v_mfma_f32_16x16x32_f16 v[118:121], v[194:197], v[138:141], v[118:121]
	v_mfma_f32_16x16x32_f16 v[114:117], v[194:197], v[168:171], v[114:117]
	v_mfma_f32_16x16x32_f16 v[214:217], v[202:205], v[168:171], v[106:109]
	v_mfma_f32_16x16x32_f16 v[102:105], v[210:213], v[138:141], v[102:105]
	s_barrier
	ds_read_b128 v[106:109], v162
	ds_read_b128 v[110:113], v163
	ds_read_b128 v[160:163], v164
	ds_read_b128 v[218:221], v165
	s_barrier
	s_waitcnt lgkmcnt(0)
	v_mfma_f32_16x16x32_f16 v[82:85], v[190:193], v[160:163], v[82:85]
	v_mfma_f32_16x16x32_f16 v[78:81], v[198:201], v[106:109], v[78:81]
	v_mfma_f32_16x16x32_f16 v[74:77], v[198:201], v[160:163], v[74:77]
	v_mfma_f32_16x16x32_f16 v[70:73], v[206:209], v[106:109], v[70:73]
	v_mfma_f32_16x16x32_f16 v[66:69], v[206:209], v[160:163], v[66:69]
	v_mfma_f32_16x16x32_f16 v[94:97], v[182:185], v[106:109], v[94:97]
	v_mfma_f32_16x16x32_f16 v[90:93], v[182:185], v[160:163], v[90:93]
	v_mfma_f32_16x16x32_f16 v[86:89], v[190:193], v[106:109], v[86:89]
	v_mfma_f32_16x16x32_f16 v[82:85], v[194:197], v[218:221], v[82:85]
	v_mfma_f32_16x16x32_f16 v[78:81], v[202:205], v[110:113], v[78:81]
	v_mfma_f32_16x16x32_f16 v[74:77], v[202:205], v[218:221], v[74:77]
	v_mfma_f32_16x16x32_f16 v[70:73], v[210:213], v[110:113], v[70:73]
	v_mfma_f32_16x16x32_f16 v[66:69], v[210:213], v[218:221], v[66:69]
	v_mfma_f32_16x16x32_f16 v[222:225], v[186:189], v[110:113], v[94:97]
	v_mfma_f32_16x16x32_f16 v[182:185], v[186:189], v[218:221], v[90:93]
	v_mfma_f32_16x16x32_f16 v[86:89], v[194:197], v[110:113], v[86:89]
	s_barrier
	ds_read_b128 v[90:93], v176 offset:16384
	ds_read_b128 v[94:97], v176 offset:17408
	ds_read_b128 v[186:189], v176 offset:18432
	ds_read_b128 v[190:193], v176 offset:19456
	ds_read_b128 v[194:197], v176 offset:20480
	ds_read_b128 v[198:201], v176 offset:21504
	ds_read_b128 v[202:205], v176 offset:22528
	ds_read_b128 v[206:209], v176 offset:23552
	s_waitcnt vmcnt(4)
	s_barrier
	s_waitcnt lgkmcnt(0)
	v_mfma_f32_16x16x32_f16 v[46:49], v[194:197], v[134:137], v[46:49]
	v_mfma_f32_16x16x32_f16 v[42:45], v[194:197], v[154:157], v[42:45]
	v_mfma_f32_16x16x32_f16 v[38:41], v[202:205], v[134:137], v[38:41]
	v_mfma_f32_16x16x32_f16 v[34:37], v[202:205], v[154:157], v[34:37]
	v_mfma_f32_16x16x32_f16 v[62:65], v[90:93], v[134:137], v[62:65]
	v_mfma_f32_16x16x32_f16 v[58:61], v[90:93], v[154:157], v[58:61]
	v_mfma_f32_16x16x32_f16 v[54:57], v[186:189], v[134:137], v[54:57]
	v_mfma_f32_16x16x32_f16 v[50:53], v[186:189], v[154:157], v[50:53]
	v_mfma_f32_16x16x32_f16 v[46:49], v[198:201], v[138:141], v[46:49]
	v_mfma_f32_16x16x32_f16 v[42:45], v[198:201], v[168:171], v[42:45]
	v_mfma_f32_16x16x32_f16 v[38:41], v[206:209], v[138:141], v[38:41]
	v_mfma_f32_16x16x32_f16 v[34:37], v[206:209], v[168:171], v[34:37]
	v_mfma_f32_16x16x32_f16 v[210:213], v[94:97], v[138:141], v[62:65]
	v_mfma_f32_16x16x32_f16 v[226:229], v[94:97], v[168:171], v[58:61]
	v_mfma_f32_16x16x32_f16 v[230:233], v[190:193], v[138:141], v[54:57]
	v_mfma_f32_16x16x32_f16 v[234:237], v[190:193], v[168:171], v[50:53]
	v_mfma_f32_16x16x32_f16 v[2:5], v[202:205], v[160:163], v[2:5]
	v_mfma_f32_16x16x32_f16 v[30:33], v[90:93], v[106:109], v[30:33]
	v_mfma_f32_16x16x32_f16 v[26:29], v[90:93], v[160:163], v[26:29]
	v_mfma_f32_16x16x32_f16 v[22:25], v[186:189], v[106:109], v[22:25]
	v_mfma_f32_16x16x32_f16 v[18:21], v[186:189], v[160:163], v[18:21]
	v_mfma_f32_16x16x32_f16 v[14:17], v[194:197], v[106:109], v[14:17]
	v_mfma_f32_16x16x32_f16 v[10:13], v[194:197], v[160:163], v[10:13]
	v_mfma_f32_16x16x32_f16 v[6:9], v[202:205], v[106:109], v[6:9]
	v_mfma_f32_16x16x32_f16 v[2:5], v[206:209], v[218:221], v[2:5]
	v_mfma_f32_16x16x32_f16 v[138:141], v[94:97], v[110:113], v[30:33]
	v_mfma_f32_16x16x32_f16 v[168:171], v[94:97], v[218:221], v[26:29]
	v_mfma_f32_16x16x32_f16 v[238:241], v[190:193], v[110:113], v[22:25]
	v_mfma_f32_16x16x32_f16 v[186:189], v[190:193], v[218:221], v[18:21]
	v_mfma_f32_16x16x32_f16 v[190:193], v[198:201], v[110:113], v[14:17]
	v_mfma_f32_16x16x32_f16 v[194:197], v[198:201], v[218:221], v[10:13]
	v_mfma_f32_16x16x32_f16 v[198:201], v[206:209], v[110:113], v[6:9]
	s_barrier
	s_nop 0
	ds_read_b128 v[6:9], v144
	ds_read_b128 v[10:13], v145
	ds_read_b128 v[14:17], v146
	ds_read_b128 v[160:163], v147
	ds_read_b128 v[18:21], v176 offset:32768
	ds_read_b128 v[22:25], v176 offset:33792
	ds_read_b128 v[26:29], v176 offset:34816
	ds_read_b128 v[50:53], v176 offset:35840
	ds_read_b128 v[202:205], v176 offset:36864
	ds_read_b128 v[206:209], v176 offset:37888
	ds_read_b128 v[218:221], v176 offset:38912
	ds_read_b128 v[242:245], v176 offset:39936
	s_waitcnt vmcnt(2)
	s_barrier
	s_waitcnt lgkmcnt(0)
	v_mfma_f32_16x16x32_f16 v[30:33], v[18:21], v[6:9], v[126:129]
	v_mfma_f32_16x16x32_f16 v[154:157], v[22:25], v[10:13], v[30:33]
	v_mfma_f32_16x16x32_f16 v[30:33], v[18:21], v[14:17], v[122:125]
	v_mfma_f32_16x16x32_f16 v[110:113], v[22:25], v[160:163], v[30:33]
	v_mfma_f32_16x16x32_f16 v[30:33], v[26:29], v[6:9], v[118:121]
	v_mfma_f32_16x16x32_f16 v[146:149], v[50:53], v[10:13], v[30:33]
	v_mfma_f32_16x16x32_f16 v[30:33], v[26:29], v[14:17], v[114:117]
	v_mfma_f32_16x16x32_f16 v[106:109], v[50:53], v[160:163], v[30:33]
	v_mfma_f32_16x16x32_f16 v[30:33], v[202:205], v[6:9], v[130:133]
	v_mfma_f32_16x16x32_f16 v[142:145], v[206:209], v[10:13], v[30:33]
	v_mfma_f32_16x16x32_f16 v[30:33], v[202:205], v[14:17], v[214:217]
	v_mfma_f32_16x16x32_f16 v[94:97], v[206:209], v[160:163], v[30:33]
	v_mfma_f32_16x16x32_f16 v[30:33], v[218:221], v[6:9], v[102:105]
	v_mfma_f32_16x16x32_f16 v[134:137], v[242:245], v[10:13], v[30:33]
	v_mfma_f32_16x16x32_f16 v[30:33], v[218:221], v[14:17], v[98:101]
	v_mfma_f32_16x16x32_f16 v[90:93], v[242:245], v[160:163], v[30:33]
	s_barrier
	ds_read_b128 v[102:105], v150
	ds_read_b128 v[114:117], v151
	ds_read_b128 v[118:121], v152
	ds_read_b128 v[126:129], v153
	s_waitcnt vmcnt(0)
	s_barrier
	s_waitcnt lgkmcnt(0)
	v_mfma_f32_16x16x32_f16 v[30:33], v[18:21], v[102:105], v[222:225]
	v_mfma_f32_16x16x32_f16 v[18:21], v[18:21], v[118:121], v[182:185]
	v_mfma_f32_16x16x32_f16 v[62:65], v[22:25], v[114:117], v[30:33]
	v_mfma_f32_16x16x32_f16 v[30:33], v[22:25], v[126:129], v[18:21]
	v_mfma_f32_16x16x32_f16 v[18:21], v[26:29], v[102:105], v[86:89]
	v_mfma_f32_16x16x32_f16 v[58:61], v[50:53], v[114:117], v[18:21]
	v_mfma_f32_16x16x32_f16 v[18:21], v[26:29], v[118:121], v[82:85]
	v_mfma_f32_16x16x32_f16 v[26:29], v[50:53], v[126:129], v[18:21]
	v_mfma_f32_16x16x32_f16 v[18:21], v[202:205], v[102:105], v[78:81]
	v_mfma_f32_16x16x32_f16 v[54:57], v[206:209], v[114:117], v[18:21]
	v_mfma_f32_16x16x32_f16 v[18:21], v[202:205], v[118:121], v[74:77]
	v_mfma_f32_16x16x32_f16 v[22:25], v[206:209], v[126:129], v[18:21]
	v_mfma_f32_16x16x32_f16 v[18:21], v[218:221], v[102:105], v[70:73]
	v_mfma_f32_16x16x32_f16 v[50:53], v[242:245], v[114:117], v[18:21]
	v_mfma_f32_16x16x32_f16 v[18:21], v[218:221], v[118:121], v[66:69]
	v_mfma_f32_16x16x32_f16 v[18:21], v[242:245], v[126:129], v[18:21]
	s_barrier
	ds_read_b128 v[86:89], v176 offset:49152
	ds_read_b128 v[150:153], v176 offset:50176
	ds_read_b128 v[182:185], v176 offset:51200
	ds_read_b128 v[202:205], v176 offset:52224
	ds_read_b128 v[206:209], v176 offset:53248
	ds_read_b128 v[214:217], v176 offset:54272
	ds_read_b128 v[218:221], v176 offset:55296
	ds_read_b128 v[174:177], v176 offset:56320
	s_barrier
	s_waitcnt lgkmcnt(0)
	v_mfma_f32_16x16x32_f16 v[66:69], v[86:89], v[6:9], v[210:213]
	v_mfma_f32_16x16x32_f16 v[130:133], v[150:153], v[10:13], v[66:69]
	v_mfma_f32_16x16x32_f16 v[66:69], v[86:89], v[14:17], v[226:229]
	v_mfma_f32_16x16x32_f16 v[78:81], v[150:153], v[160:163], v[66:69]
	v_mfma_f32_16x16x32_f16 v[66:69], v[182:185], v[6:9], v[230:233]
	v_mfma_f32_16x16x32_f16 v[46:49], v[206:209], v[6:9], v[46:49]
	v_mfma_f32_16x16x32_f16 v[6:9], v[218:221], v[6:9], v[38:41]
	v_mfma_f32_16x16x32_f16 v[122:125], v[202:205], v[10:13], v[66:69]
	v_mfma_f32_16x16x32_f16 v[66:69], v[182:185], v[14:17], v[234:237]
	v_mfma_f32_16x16x32_f16 v[42:45], v[206:209], v[14:17], v[42:45]
	v_mfma_f32_16x16x32_f16 v[82:85], v[174:177], v[10:13], v[6:9]
	v_mfma_f32_16x16x32_f16 v[6:9], v[218:221], v[14:17], v[34:37]
	v_mfma_f32_16x16x32_f16 v[74:77], v[202:205], v[160:163], v[66:69]
	v_mfma_f32_16x16x32_f16 v[98:101], v[214:217], v[10:13], v[46:49]
	v_mfma_f32_16x16x32_f16 v[70:73], v[214:217], v[160:163], v[42:45]
	v_mfma_f32_16x16x32_f16 v[66:69], v[174:177], v[160:163], v[6:9]
	v_mfma_f32_16x16x32_f16 v[6:9], v[86:89], v[102:105], v[138:141]
	v_mfma_f32_16x16x32_f16 v[46:49], v[150:153], v[114:117], v[6:9]
	v_mfma_f32_16x16x32_f16 v[6:9], v[86:89], v[118:121], v[168:171]
	v_mfma_f32_16x16x32_f16 v[14:17], v[150:153], v[126:129], v[6:9]
	v_mfma_f32_16x16x32_f16 v[6:9], v[182:185], v[102:105], v[238:241]
	v_mfma_f32_16x16x32_f16 v[42:45], v[202:205], v[114:117], v[6:9]
	v_mfma_f32_16x16x32_f16 v[6:9], v[182:185], v[118:121], v[186:189]
	v_mfma_f32_16x16x32_f16 v[10:13], v[202:205], v[126:129], v[6:9]
	v_mfma_f32_16x16x32_f16 v[6:9], v[206:209], v[102:105], v[190:193]
	v_mfma_f32_16x16x32_f16 v[38:41], v[214:217], v[114:117], v[6:9]
	v_mfma_f32_16x16x32_f16 v[6:9], v[206:209], v[118:121], v[194:197]
	v_mfma_f32_16x16x32_f16 v[34:37], v[218:221], v[102:105], v[198:201]
	v_mfma_f32_16x16x32_f16 v[2:5], v[218:221], v[118:121], v[2:5]
	v_mfma_f32_16x16x32_f16 v[6:9], v[214:217], v[126:129], v[6:9]
	v_mfma_f32_16x16x32_f16 v[34:37], v[174:177], v[114:117], v[34:37]
	v_mfma_f32_16x16x32_f16 v[2:5], v[174:177], v[126:129], v[2:5]
	s_cmpk_gt_u32 s62, 0xff
	s_barrier
	s_cbranch_scc1 .LBB8_44
	s_barrier

	.amdhsa_kernel _Z14gemm256_kernelILi1ELi512ELi512EEv8GemmArgs
		.amdhsa_group_segment_fixed_size 0
		.amdhsa_private_segment_fixed_size 0
		.amdhsa_kernarg_size 592
		.amdhsa_user_sgpr_count 2
		.amdhsa_user_sgpr_dispatch_ptr 0
		.amdhsa_user_sgpr_queue_ptr 0
		.amdhsa_user_sgpr_kernarg_segment_ptr 1
		.amdhsa_user_sgpr_dispatch_id 0
		.amdhsa_user_sgpr_kernarg_preload_length 0
		.amdhsa_user_sgpr_kernarg_preload_offset 0
		.amdhsa_user_sgpr_private_segment_size 0
		.amdhsa_uses_dynamic_stack 0
		.amdhsa_enable_private_segment 0
		.amdhsa_system_sgpr_workgroup_id_x 1
		.amdhsa_system_sgpr_workgroup_id_y 0
		.amdhsa_system_sgpr_workgroup_id_z 0
		.amdhsa_system_sgpr_workgroup_info 0
		.amdhsa_system_vgpr_workitem_id 0
		.amdhsa_next_free_vgpr 256
		.amdhsa_next_free_sgpr 91
		.amdhsa_accum_offset 256
		.amdhsa_reserve_vcc 1
		.amdhsa_float_round_mode_32 0
		.amdhsa_float_round_mode_16_64 0
		.amdhsa_float_denorm_mode_32 3
		.amdhsa_float_denorm_mode_16_64 3
		.amdhsa_dx10_clamp 1
		.amdhsa_ieee_mode 1
		.amdhsa_fp16_overflow 0
		.amdhsa_tg_split 0
		.amdhsa_exception_fp_ieee_invalid_op 0
		.amdhsa_exception_fp_denorm_src 0
		.amdhsa_exception_fp_ieee_div_zero 0
		.amdhsa_exception_fp_ieee_overflow 0
		.amdhsa_exception_fp_ieee_underflow 0
		.amdhsa_exception_fp_ieee_inexact 0
		.amdhsa_exception_int_div_zero 0
	.end_amdhsa_kernel

.LBB9_37:
	v_and_b32_e32 v10, 48, v196
	v_lshlrev_b32_e32 v11, 6, v196
	v_and_or_b32 v10, v11, s49, v10
	v_lshlrev_b32_e32 v11, 2, v196
	v_and_b32_e32 v11, 32, v11
	s_lshl_b32 s39, s54, 6
	v_lshlrev_b32_e32 v2, 12, v2
	v_xad_u32 v168, v10, v11, 0
	s_and_b32 s39, s39, 0x3000
	v_lshlrev_b32_e32 v6, 12, v6
	v_and_b32_e32 v2, 0xffffe000, v2
	v_add_u32_e32 v10, s39, v168
	s_lshl_b32 s39, s55, 13
	v_and_b32_e32 v6, 0xffffe000, v6
	v_lshl_add_u32 v2, v3, 9, v2
	v_lshl_add_u32 v6, v7, 9, v6
	s_add_u32 s44, s24, s44
	v_or_b32_e32 v2, v2, v4
	v_or_b32_e32 v6, v6, v8
	s_addc_u32 s45, s25, s45
	v_add_u32_sdwa v2, v2, sext(v5) dst_sel:DWORD dst_unused:UNUSED_PAD src0_sel:DWORD src1_sel:WORD_0
	v_add_u32_sdwa v6, v6, sext(v9) dst_sel:DWORD dst_unused:UNUSED_PAD src0_sel:DWORD src1_sel:WORD_0
	v_ashrrev_i32_e32 v3, 31, v2
	s_add_u32 s42, s20, s42
	s_waitcnt vmcnt(6)
	v_ashrrev_i32_e32 v7, 31, v6
	v_lshlrev_b64 v[2:3], 1, v[2:3]
	s_addc_u32 s43, s21, s43
	v_lshlrev_b64 v[6:7], 1, v[6:7]
	v_lshl_add_u64 v[136:137], s[44:45], 0, v[2:3]
	v_lshl_add_u64 v[140:141], s[42:43], 0, v[2:3]
	v_mov_b32_e32 v2, 0
	v_add_u32_e32 v169, 0x10000, v10
	v_add_u32_e32 v170, 0x10400, v10
	v_add_u32_e32 v171, 0x10800, v10
	v_add_u32_e32 v172, 0x10c00, v10
	v_add_u32_e32 v161, 0x14000, v10
	v_add_u32_e32 v162, 0x14400, v10
	v_add_u32_e32 v163, 0x14800, v10
	v_add_u32_e32 v164, 0x14c00, v10
	v_add_u32_e32 v144, 0x18000, v10
	v_add_u32_e32 v145, 0x18400, v10
	v_add_u32_e32 v150, 0x18800, v10
	v_add_u32_e32 v151, 0x18c00, v10
	v_add_u32_e32 v146, 0x1c000, v10
	v_add_u32_e32 v147, 0x1c400, v10
	v_add_u32_e32 v148, 0x1c800, v10
	v_add_u32_e32 v149, 0x1cc00, v10
	v_lshl_add_u64 v[134:135], s[44:45], 0, v[6:7]
	v_lshl_add_u64 v[138:139], s[42:43], 0, v[6:7]
	s_mov_b32 s44, -2
	s_mov_b64 s[42:43], 0
	v_mov_b32_e32 v3, v2
	v_mov_b32_e32 v4, v2
	v_mov_b32_e32 v5, v2
	v_mov_b32_e32 v6, v2
	v_mov_b32_e32 v7, v2
	v_mov_b32_e32 v8, v2
	v_mov_b32_e32 v9, v2
	v_mov_b32_e32 v10, v2
	v_mov_b32_e32 v11, v2
	v_mov_b32_e32 v12, v2
	v_mov_b32_e32 v13, v2
	v_mov_b32_e32 v18, v2
	v_mov_b32_e32 v19, v2
	v_mov_b32_e32 v20, v2
	v_mov_b32_e32 v21, v2
	v_mov_b32_e32 v30, v2
	v_mov_b32_e32 v31, v2
	v_mov_b32_e32 v32, v2
	v_mov_b32_e32 v33, v2
	v_mov_b32_e32 v42, v2
	v_mov_b32_e32 v43, v2
	v_mov_b32_e32 v44, v2
	v_mov_b32_e32 v45, v2
	v_mov_b32_e32 v54, v2
	v_mov_b32_e32 v55, v2
	v_mov_b32_e32 v56, v2
	v_mov_b32_e32 v57, v2
	v_mov_b32_e32 v66, v2
	v_mov_b32_e32 v67, v2
	v_mov_b32_e32 v68, v2
	v_mov_b32_e32 v69, v2
	v_mov_b32_e32 v14, v2
	v_mov_b32_e32 v15, v2
	v_mov_b32_e32 v16, v2
	v_mov_b32_e32 v17, v2
	v_mov_b32_e32 v22, v2
	v_mov_b32_e32 v23, v2
	v_mov_b32_e32 v24, v2
	v_mov_b32_e32 v25, v2
	v_mov_b32_e32 v34, v2
	v_mov_b32_e32 v35, v2
	v_mov_b32_e32 v36, v2
	v_mov_b32_e32 v37, v2
	v_mov_b32_e32 v46, v2
	v_mov_b32_e32 v47, v2
	v_mov_b32_e32 v48, v2
	v_mov_b32_e32 v49, v2
	v_mov_b32_e32 v58, v2
	v_mov_b32_e32 v59, v2
	v_mov_b32_e32 v60, v2
	v_mov_b32_e32 v61, v2
	v_mov_b32_e32 v70, v2
	v_mov_b32_e32 v71, v2
	v_mov_b32_e32 v72, v2
	v_mov_b32_e32 v73, v2
	v_mov_b32_e32 v78, v2
	v_mov_b32_e32 v79, v2
	v_mov_b32_e32 v80, v2
	v_mov_b32_e32 v81, v2
	v_mov_b32_e32 v86, v2
	v_mov_b32_e32 v87, v2
	v_mov_b32_e32 v88, v2
	v_mov_b32_e32 v89, v2
	v_mov_b32_e32 v26, v2
	v_mov_b32_e32 v27, v2
	v_mov_b32_e32 v28, v2
	v_mov_b32_e32 v29, v2
	v_mov_b32_e32 v38, v2
	v_mov_b32_e32 v39, v2
	v_mov_b32_e32 v40, v2
	v_mov_b32_e32 v41, v2
	v_mov_b32_e32 v50, v2
	v_mov_b32_e32 v51, v2
	v_mov_b32_e32 v52, v2
	v_mov_b32_e32 v53, v2
	v_mov_b32_e32 v62, v2
	v_mov_b32_e32 v63, v2
	v_mov_b32_e32 v64, v2
	v_mov_b32_e32 v65, v2
	v_mov_b32_e32 v74, v2
	v_mov_b32_e32 v75, v2
	v_mov_b32_e32 v76, v2
	v_mov_b32_e32 v77, v2
	v_mov_b32_e32 v82, v2
	v_mov_b32_e32 v83, v2
	v_mov_b32_e32 v84, v2
	v_mov_b32_e32 v85, v2
	v_mov_b32_e32 v90, v2
	v_mov_b32_e32 v91, v2
	v_mov_b32_e32 v92, v2
	v_mov_b32_e32 v93, v2
	v_mov_b32_e32 v94, v2
	v_mov_b32_e32 v95, v2
	v_mov_b32_e32 v96, v2
	v_mov_b32_e32 v97, v2
	v_mov_b32_e32 v98, v2
	v_mov_b32_e32 v99, v2
	v_mov_b32_e32 v100, v2
	v_mov_b32_e32 v101, v2
	v_mov_b32_e32 v102, v2
	v_mov_b32_e32 v103, v2
	v_mov_b32_e32 v104, v2
	v_mov_b32_e32 v105, v2
	v_mov_b32_e32 v106, v2
	v_mov_b32_e32 v107, v2
	v_mov_b32_e32 v108, v2
	v_mov_b32_e32 v109, v2
	v_mov_b32_e32 v110, v2
	v_mov_b32_e32 v111, v2
	v_mov_b32_e32 v112, v2
	v_mov_b32_e32 v113, v2
	v_mov_b32_e32 v114, v2
	v_mov_b32_e32 v115, v2
	v_mov_b32_e32 v116, v2
	v_mov_b32_e32 v117, v2
	v_mov_b32_e32 v118, v2
	v_mov_b32_e32 v119, v2
	v_mov_b32_e32 v120, v2
	v_mov_b32_e32 v121, v2
	v_mov_b32_e32 v122, v2
	v_mov_b32_e32 v123, v2
	v_mov_b32_e32 v124, v2
	v_mov_b32_e32 v125, v2
	v_mov_b32_e32 v126, v2
	v_mov_b32_e32 v127, v2
	v_mov_b32_e32 v128, v2
	v_mov_b32_e32 v129, v2
	v_add_u32_e32 v174, 0xc000, v152
	v_add_u32_e32 v175, 0xe000, v152
	s_nop 0
	v_readfirstlane_b32 s65, v174
	v_readfirstlane_b32 s66, v175
	v_readfirstlane_b32 s67, v142
	v_readfirstlane_b32 s68, v143
	v_readfirstlane_b32 s69, v152
	v_readfirstlane_b32 s70, v153
	v_readfirstlane_b32 s71, v154
	v_readfirstlane_b32 s72, v155
	v_readfirstlane_b32 s73, v156
	v_readfirstlane_b32 s74, v157
	v_readfirstlane_b32 s75, v158
	v_readfirstlane_b32 s76, v159
	v_readfirstlane_b32 s77, v160
	v_readfirstlane_b32 s78, v165
	v_readfirstlane_b32 s79, v166
	v_readfirstlane_b32 s80, v167
	s_barrier
	s_barrier
.LBB9_38:
	ds_read_b128 v[176:179], v169
	ds_read_b128 v[180:183], v170
	ds_read_b128 v[184:187], v171
	ds_read_b128 v[188:191], v172
	v_add_u32_e32 v174, 0xc000, v152
	v_lshl_add_u64 v[192:193], v[136:137], 0, s[42:43]
	v_add_u32_e32 v175, 0xe000, v152
	v_add_u32_e32 v173, s39, v168
	v_lshl_add_u64 v[230:231], v[192:193], 0, s[10:11]
	s_mov_b32 m0, s65
	v_lshl_add_u64 v[246:247], v[134:135], 0, s[42:43]
	ds_read_b128 v[198:201], v173
	ds_read_b128 v[202:205], v173 offset:1024
	ds_read_b128 v[206:209], v173 offset:2048
	ds_read_b128 v[210:213], v173 offset:3072
	ds_read_b128 v[214:217], v173 offset:4096
	ds_read_b128 v[218:221], v173 offset:5120
	ds_read_b128 v[222:225], v173 offset:6144
	ds_read_b128 v[226:229], v173 offset:7168
	global_load_lds_dwordx4 v[230:231], off
	v_lshl_add_u64 v[230:231], v[246:247], 0, s[10:11]
	s_mov_b32 m0, s66
	s_nop 0
	global_load_lds_dwordx4 v[230:231], off
	s_waitcnt lgkmcnt(8)
	s_barrier
	s_waitcnt lgkmcnt(0)
	v_mfma_f32_16x16x32_f16 v[2:5], v[198:201], v[176:179], v[2:5]
	v_mfma_f32_16x16x32_f16 v[6:9], v[198:201], v[184:187], v[6:9]
	v_mfma_f32_16x16x32_f16 v[10:13], v[206:209], v[176:179], v[10:13]
	v_mfma_f32_16x16x32_f16 v[18:21], v[206:209], v[184:187], v[18:21]
	v_mfma_f32_16x16x32_f16 v[30:33], v[214:217], v[176:179], v[30:33]
	v_mfma_f32_16x16x32_f16 v[42:45], v[214:217], v[184:187], v[42:45]
	v_mfma_f32_16x16x32_f16 v[54:57], v[222:225], v[176:179], v[54:57]
	v_mfma_f32_16x16x32_f16 v[66:69], v[222:225], v[184:187], v[66:69]
	v_mfma_f32_16x16x32_f16 v[2:5], v[202:205], v[180:183], v[2:5]
	v_mfma_f32_16x16x32_f16 v[6:9], v[202:205], v[188:191], v[6:9]
	v_mfma_f32_16x16x32_f16 v[10:13], v[210:213], v[180:183], v[10:13]
	v_mfma_f32_16x16x32_f16 v[18:21], v[210:213], v[188:191], v[18:21]
	v_mfma_f32_16x16x32_f16 v[30:33], v[218:221], v[180:183], v[30:33]
	v_mfma_f32_16x16x32_f16 v[42:45], v[218:221], v[188:191], v[42:45]
	v_mfma_f32_16x16x32_f16 v[54:57], v[226:229], v[180:183], v[54:57]
	v_mfma_f32_16x16x32_f16 v[66:69], v[226:229], v[188:191], v[66:69]
	s_barrier
	v_lshl_add_u64 v[248:249], v[140:141], 0, s[42:43]
	v_lshl_add_u64 v[250:251], v[248:249], 0, s[26:27]
	s_mov_b32 m0, s67
	ds_read_b128 v[230:233], v161
	ds_read_b128 v[234:237], v162
	ds_read_b128 v[238:241], v163
	ds_read_b128 v[242:245], v164
	global_load_lds_dwordx4 v[250:251], off
	v_lshl_add_u64 v[250:251], v[138:139], 0, s[42:43]
	v_lshl_add_u64 v[252:253], v[250:251], 0, s[26:27]
	s_mov_b32 m0, s68
	s_nop 0
	global_load_lds_dwordx4 v[252:253], off
	s_barrier
	s_waitcnt lgkmcnt(0)
	v_mfma_f32_16x16x32_f16 v[14:17], v[198:201], v[230:233], v[14:17]
	v_mfma_f32_16x16x32_f16 v[22:25], v[198:201], v[238:241], v[22:25]
	v_mfma_f32_16x16x32_f16 v[34:37], v[206:209], v[230:233], v[34:37]
	v_mfma_f32_16x16x32_f16 v[46:49], v[206:209], v[238:241], v[46:49]
	v_mfma_f32_16x16x32_f16 v[58:61], v[214:217], v[230:233], v[58:61]
	v_mfma_f32_16x16x32_f16 v[70:73], v[214:217], v[238:241], v[70:73]
	v_mfma_f32_16x16x32_f16 v[78:81], v[222:225], v[230:233], v[78:81]
	v_mfma_f32_16x16x32_f16 v[86:89], v[222:225], v[238:241], v[86:89]
	v_mfma_f32_16x16x32_f16 v[14:17], v[202:205], v[234:237], v[14:17]
	v_mfma_f32_16x16x32_f16 v[22:25], v[202:205], v[242:245], v[22:25]
	v_mfma_f32_16x16x32_f16 v[34:37], v[210:213], v[234:237], v[34:37]
	v_mfma_f32_16x16x32_f16 v[46:49], v[210:213], v[242:245], v[46:49]
	v_mfma_f32_16x16x32_f16 v[58:61], v[218:221], v[234:237], v[58:61]
	v_mfma_f32_16x16x32_f16 v[70:73], v[218:221], v[242:245], v[70:73]
	v_mfma_f32_16x16x32_f16 v[78:81], v[226:229], v[234:237], v[78:81]
	v_mfma_f32_16x16x32_f16 v[86:89], v[226:229], v[242:245], v[86:89]
	v_lshl_add_u64 v[252:253], v[192:193], 0, s[26:27]
	s_mov_b32 m0, s69
	s_barrier
	ds_read_b128 v[198:201], v173 offset:16384
	ds_read_b128 v[202:205], v173 offset:17408
	ds_read_b128 v[206:209], v173 offset:18432
	ds_read_b128 v[210:213], v173 offset:19456
	ds_read_b128 v[214:217], v173 offset:20480
	ds_read_b128 v[218:221], v173 offset:21504
	ds_read_b128 v[222:225], v173 offset:22528
	ds_read_b128 v[226:229], v173 offset:23552
	global_load_lds_dwordx4 v[252:253], off
	v_lshl_add_u64 v[252:253], v[246:247], 0, s[26:27]
	s_mov_b32 m0, s70
	s_nop 0
	global_load_lds_dwordx4 v[252:253], off
	s_barrier
	s_waitcnt lgkmcnt(0)
	v_mfma_f32_16x16x32_f16 v[26:29], v[198:201], v[176:179], v[26:29]
	v_mfma_f32_16x16x32_f16 v[38:41], v[198:201], v[184:187], v[38:41]
	v_mfma_f32_16x16x32_f16 v[50:53], v[206:209], v[176:179], v[50:53]
	v_mfma_f32_16x16x32_f16 v[62:65], v[206:209], v[184:187], v[62:65]
	v_mfma_f32_16x16x32_f16 v[74:77], v[214:217], v[176:179], v[74:77]
	v_mfma_f32_16x16x32_f16 v[82:85], v[214:217], v[184:187], v[82:85]
	v_mfma_f32_16x16x32_f16 v[90:93], v[222:225], v[176:179], v[90:93]
	v_mfma_f32_16x16x32_f16 v[94:97], v[222:225], v[184:187], v[94:97]
	v_mfma_f32_16x16x32_f16 v[26:29], v[202:205], v[180:183], v[26:29]
	v_mfma_f32_16x16x32_f16 v[38:41], v[202:205], v[188:191], v[38:41]
	v_mfma_f32_16x16x32_f16 v[50:53], v[210:213], v[180:183], v[50:53]
	v_mfma_f32_16x16x32_f16 v[62:65], v[210:213], v[188:191], v[62:65]
	v_mfma_f32_16x16x32_f16 v[74:77], v[218:221], v[180:183], v[74:77]
	v_mfma_f32_16x16x32_f16 v[82:85], v[218:221], v[188:191], v[82:85]
	v_mfma_f32_16x16x32_f16 v[90:93], v[226:229], v[180:183], v[90:93]
	v_mfma_f32_16x16x32_f16 v[94:97], v[226:229], v[188:191], v[94:97]
	s_barrier
	v_lshl_add_u64 v[176:177], v[248:249], 0, s[28:29]
	s_mov_b32 m0, s71
	global_load_lds_dwordx4 v[176:177], off
	v_lshl_add_u64 v[176:177], v[250:251], 0, s[28:29]
	s_mov_b32 m0, s72
	s_nop 0
	global_load_lds_dwordx4 v[176:177], off
	s_waitcnt vmcnt(6)
	s_barrier
	v_mfma_f32_16x16x32_f16 v[98:101], v[198:201], v[230:233], v[98:101]
	v_mfma_f32_16x16x32_f16 v[102:105], v[198:201], v[238:241], v[102:105]
	v_mfma_f32_16x16x32_f16 v[106:109], v[206:209], v[230:233], v[106:109]
	v_mfma_f32_16x16x32_f16 v[110:113], v[206:209], v[238:241], v[110:113]
	v_mfma_f32_16x16x32_f16 v[114:117], v[214:217], v[230:233], v[114:117]
	v_mfma_f32_16x16x32_f16 v[118:121], v[214:217], v[238:241], v[118:121]
	v_mfma_f32_16x16x32_f16 v[122:125], v[222:225], v[230:233], v[122:125]
	v_mfma_f32_16x16x32_f16 v[126:129], v[222:225], v[238:241], v[126:129]
	v_mfma_f32_16x16x32_f16 v[98:101], v[202:205], v[234:237], v[98:101]
	v_mfma_f32_16x16x32_f16 v[102:105], v[202:205], v[242:245], v[102:105]
	v_mfma_f32_16x16x32_f16 v[106:109], v[210:213], v[234:237], v[106:109]
	v_mfma_f32_16x16x32_f16 v[110:113], v[210:213], v[242:245], v[110:113]
	v_mfma_f32_16x16x32_f16 v[114:117], v[218:221], v[234:237], v[114:117]
	v_mfma_f32_16x16x32_f16 v[118:121], v[218:221], v[242:245], v[118:121]
	v_mfma_f32_16x16x32_f16 v[122:125], v[226:229], v[234:237], v[122:125]
	v_mfma_f32_16x16x32_f16 v[126:129], v[226:229], v[242:245], v[126:129]
	s_barrier
	ds_read_b128 v[176:179], v144
	ds_read_b128 v[180:183], v145
	ds_read_b128 v[184:187], v150
	ds_read_b128 v[188:191], v151
	v_lshl_add_u64 v[230:231], v[192:193], 0, s[28:29]
	s_mov_b32 m0, s73
	ds_read_b128 v[198:201], v173 offset:32768
	ds_read_b128 v[202:205], v173 offset:33792
	ds_read_b128 v[206:209], v173 offset:34816
	ds_read_b128 v[210:213], v173 offset:35840
	ds_read_b128 v[214:217], v173 offset:36864
	ds_read_b128 v[218:221], v173 offset:37888
	ds_read_b128 v[222:225], v173 offset:38912
	ds_read_b128 v[226:229], v173 offset:39936
	global_load_lds_dwordx4 v[230:231], off
	v_lshl_add_u64 v[230:231], v[246:247], 0, s[28:29]
	s_mov_b32 m0, s74
	s_nop 0
	global_load_lds_dwordx4 v[230:231], off
	s_waitcnt lgkmcnt(8)
	s_barrier
	s_waitcnt lgkmcnt(0)
	v_mfma_f32_16x16x32_f16 v[2:5], v[198:201], v[176:179], v[2:5]
	v_mfma_f32_16x16x32_f16 v[6:9], v[198:201], v[184:187], v[6:9]
	v_mfma_f32_16x16x32_f16 v[10:13], v[206:209], v[176:179], v[10:13]
	v_mfma_f32_16x16x32_f16 v[18:21], v[206:209], v[184:187], v[18:21]
	v_mfma_f32_16x16x32_f16 v[30:33], v[214:217], v[176:179], v[30:33]
	v_mfma_f32_16x16x32_f16 v[42:45], v[214:217], v[184:187], v[42:45]
	v_mfma_f32_16x16x32_f16 v[54:57], v[222:225], v[176:179], v[54:57]
	v_mfma_f32_16x16x32_f16 v[66:69], v[222:225], v[184:187], v[66:69]
	v_mfma_f32_16x16x32_f16 v[2:5], v[202:205], v[180:183], v[2:5]
	v_mfma_f32_16x16x32_f16 v[6:9], v[202:205], v[188:191], v[6:9]
	v_mfma_f32_16x16x32_f16 v[10:13], v[210:213], v[180:183], v[10:13]
	v_mfma_f32_16x16x32_f16 v[18:21], v[210:213], v[188:191], v[18:21]
	v_mfma_f32_16x16x32_f16 v[30:33], v[218:221], v[180:183], v[30:33]
	v_mfma_f32_16x16x32_f16 v[42:45], v[218:221], v[188:191], v[42:45]
	v_mfma_f32_16x16x32_f16 v[54:57], v[226:229], v[180:183], v[54:57]
	v_mfma_f32_16x16x32_f16 v[66:69], v[226:229], v[188:191], v[66:69]
	s_barrier
	v_lshl_add_u64 v[252:253], v[248:249], 0, s[30:31]
	s_mov_b32 m0, s75
	ds_read_b128 v[230:233], v146
	ds_read_b128 v[234:237], v147
	ds_read_b128 v[238:241], v148
	ds_read_b128 v[242:245], v149
	global_load_lds_dwordx4 v[252:253], off
	v_lshl_add_u64 v[252:253], v[250:251], 0, s[30:31]
	s_mov_b32 m0, s76
	s_nop 0
	global_load_lds_dwordx4 v[252:253], off
	s_barrier
	s_waitcnt lgkmcnt(0)
	v_mfma_f32_16x16x32_f16 v[14:17], v[198:201], v[230:233], v[14:17]
	v_mfma_f32_16x16x32_f16 v[22:25], v[198:201], v[238:241], v[22:25]
	v_mfma_f32_16x16x32_f16 v[34:37], v[206:209], v[230:233], v[34:37]
	v_mfma_f32_16x16x32_f16 v[46:49], v[206:209], v[238:241], v[46:49]
	v_mfma_f32_16x16x32_f16 v[58:61], v[214:217], v[230:233], v[58:61]
	v_mfma_f32_16x16x32_f16 v[70:73], v[214:217], v[238:241], v[70:73]
	v_mfma_f32_16x16x32_f16 v[78:81], v[222:225], v[230:233], v[78:81]
	v_mfma_f32_16x16x32_f16 v[86:89], v[222:225], v[238:241], v[86:89]
	v_mfma_f32_16x16x32_f16 v[14:17], v[202:205], v[234:237], v[14:17]
	v_mfma_f32_16x16x32_f16 v[22:25], v[202:205], v[242:245], v[22:25]
	v_mfma_f32_16x16x32_f16 v[34:37], v[210:213], v[234:237], v[34:37]
	v_mfma_f32_16x16x32_f16 v[46:49], v[210:213], v[242:245], v[46:49]
	v_mfma_f32_16x16x32_f16 v[58:61], v[218:221], v[234:237], v[58:61]
	v_mfma_f32_16x16x32_f16 v[70:73], v[218:221], v[242:245], v[70:73]
	v_mfma_f32_16x16x32_f16 v[78:81], v[226:229], v[234:237], v[78:81]
	v_mfma_f32_16x16x32_f16 v[86:89], v[226:229], v[242:245], v[86:89]
	v_lshl_add_u64 v[192:193], v[192:193], 0, s[30:31]
	s_mov_b32 m0, s77
	s_barrier
	ds_read_b128 v[198:201], v173 offset:49152
	ds_read_b128 v[202:205], v173 offset:50176
	ds_read_b128 v[206:209], v173 offset:51200
	ds_read_b128 v[210:213], v173 offset:52224
	ds_read_b128 v[214:217], v173 offset:53248
	ds_read_b128 v[218:221], v173 offset:54272
	ds_read_b128 v[222:225], v173 offset:55296
	ds_read_b128 v[226:229], v173 offset:56320
	global_load_lds_dwordx4 v[192:193], off
	v_lshl_add_u64 v[192:193], v[246:247], 0, s[30:31]
	s_mov_b32 m0, s78
	s_nop 0
	global_load_lds_dwordx4 v[192:193], off
	s_barrier
	s_waitcnt lgkmcnt(0)
	v_mfma_f32_16x16x32_f16 v[26:29], v[198:201], v[176:179], v[26:29]
	v_mfma_f32_16x16x32_f16 v[38:41], v[198:201], v[184:187], v[38:41]
	v_mfma_f32_16x16x32_f16 v[50:53], v[206:209], v[176:179], v[50:53]
	v_mfma_f32_16x16x32_f16 v[62:65], v[206:209], v[184:187], v[62:65]
	v_mfma_f32_16x16x32_f16 v[74:77], v[214:217], v[176:179], v[74:77]
	v_mfma_f32_16x16x32_f16 v[82:85], v[214:217], v[184:187], v[82:85]
	v_mfma_f32_16x16x32_f16 v[90:93], v[222:225], v[176:179], v[90:93]
	v_mfma_f32_16x16x32_f16 v[94:97], v[222:225], v[184:187], v[94:97]
	v_mfma_f32_16x16x32_f16 v[26:29], v[202:205], v[180:183], v[26:29]
	v_mfma_f32_16x16x32_f16 v[38:41], v[202:205], v[188:191], v[38:41]
	v_mfma_f32_16x16x32_f16 v[50:53], v[210:213], v[180:183], v[50:53]
	v_mfma_f32_16x16x32_f16 v[62:65], v[210:213], v[188:191], v[62:65]
	v_mfma_f32_16x16x32_f16 v[74:77], v[218:221], v[180:183], v[74:77]
	v_mfma_f32_16x16x32_f16 v[82:85], v[218:221], v[188:191], v[82:85]
	v_mfma_f32_16x16x32_f16 v[90:93], v[226:229], v[180:183], v[90:93]
	v_mfma_f32_16x16x32_f16 v[94:97], v[226:229], v[188:191], v[94:97]
	s_barrier
	v_lshl_add_u64 v[176:177], v[248:249], 0, s[34:35]
	s_mov_b32 m0, s79
	global_load_lds_dwordx4 v[176:177], off
	v_lshl_add_u64 v[176:177], v[250:251], 0, s[34:35]
	s_mov_b32 m0, s80
	s_nop 0
	global_load_lds_dwordx4 v[176:177], off
	s_waitcnt vmcnt(6)
	s_barrier
	v_mfma_f32_16x16x32_f16 v[98:101], v[198:201], v[230:233], v[98:101]
	v_mfma_f32_16x16x32_f16 v[102:105], v[198:201], v[238:241], v[102:105]
	v_mfma_f32_16x16x32_f16 v[106:109], v[206:209], v[230:233], v[106:109]
	v_mfma_f32_16x16x32_f16 v[110:113], v[206:209], v[238:241], v[110:113]
	v_mfma_f32_16x16x32_f16 v[114:117], v[214:217], v[230:233], v[114:117]
	v_mfma_f32_16x16x32_f16 v[118:121], v[214:217], v[238:241], v[118:121]
	v_mfma_f32_16x16x32_f16 v[122:125], v[222:225], v[230:233], v[122:125]
	v_mfma_f32_16x16x32_f16 v[126:129], v[222:225], v[238:241], v[126:129]
	v_mfma_f32_16x16x32_f16 v[98:101], v[202:205], v[234:237], v[98:101]
	v_mfma_f32_16x16x32_f16 v[102:105], v[202:205], v[242:245], v[102:105]
	v_mfma_f32_16x16x32_f16 v[106:109], v[210:213], v[234:237], v[106:109]
	v_mfma_f32_16x16x32_f16 v[110:113], v[210:213], v[242:245], v[110:113]
	v_mfma_f32_16x16x32_f16 v[114:117], v[218:221], v[234:237], v[114:117]
	v_mfma_f32_16x16x32_f16 v[118:121], v[218:221], v[242:245], v[118:121]
	v_mfma_f32_16x16x32_f16 v[122:125], v[226:229], v[234:237], v[122:125]
	v_mfma_f32_16x16x32_f16 v[126:129], v[226:229], v[242:245], v[126:129]
	s_add_i32 s44, s44, 2
	s_add_u32 s42, s42, 0x100
	s_addc_u32 s43, s43, 0
	s_cmp_lt_u32 s44, 4
	s_barrier
	s_cbranch_scc1 .LBB9_38
	s_add_u32 s40, s40, 0x20380
	s_addc_u32 s41, s41, 0
	v_readfirstlane_b32 s39, v174
	v_lshl_add_u64 v[130:131], v[130:131], 1, s[40:41]
	s_mov_b32 m0, s39
	v_readfirstlane_b32 s39, v175
	ds_read_b128 v[134:137], v169
	ds_read_b128 v[138:141], v170
	ds_read_b128 v[152:155], v171
	ds_read_b128 v[156:159], v172
	ds_read_b128 v[166:169], v173
	ds_read_b128 v[176:179], v173 offset:1024
	ds_read_b128 v[180:183], v173 offset:2048
	ds_read_b128 v[184:187], v173 offset:3072
	ds_read_b128 v[188:191], v173 offset:4096
	ds_read_b128 v[198:201], v173 offset:5120
	ds_read_b128 v[202:205], v173 offset:6144
	ds_read_b128 v[206:209], v173 offset:7168
	global_load_lds_dwordx4 v[130:131], off
	v_lshl_add_u64 v[130:131], v[132:133], 1, s[40:41]
	s_mov_b32 m0, s39
	s_nop 0
	global_load_lds_dwordx4 v[130:131], off
	s_barrier
	s_waitcnt lgkmcnt(0)
	v_mfma_f32_16x16x32_f16 v[2:5], v[166:169], v[134:137], v[2:5]
	v_mfma_f32_16x16x32_f16 v[6:9], v[166:169], v[152:155], v[6:9]
	v_mfma_f32_16x16x32_f16 v[30:33], v[188:191], v[134:137], v[30:33]
	v_mfma_f32_16x16x32_f16 v[2:5], v[176:179], v[138:141], v[2:5]
	v_mfma_f32_16x16x32_f16 v[6:9], v[176:179], v[156:159], v[6:9]
	v_mfma_f32_16x16x32_f16 v[10:13], v[180:183], v[134:137], v[10:13]
	v_mfma_f32_16x16x32_f16 v[18:21], v[180:183], v[152:155], v[18:21]
	v_mfma_f32_16x16x32_f16 v[30:33], v[198:201], v[138:141], v[30:33]
	v_mfma_f32_16x16x32_f16 v[42:45], v[188:191], v[152:155], v[42:45]
	v_mfma_f32_16x16x32_f16 v[54:57], v[202:205], v[134:137], v[54:57]
	v_mfma_f32_16x16x32_f16 v[66:69], v[202:205], v[152:155], v[66:69]
	v_mfma_f32_16x16x32_f16 v[10:13], v[184:187], v[138:141], v[10:13]
	v_mfma_f32_16x16x32_f16 v[18:21], v[184:187], v[156:159], v[18:21]
	v_mfma_f32_16x16x32_f16 v[42:45], v[198:201], v[156:159], v[42:45]
	v_mfma_f32_16x16x32_f16 v[54:57], v[206:209], v[138:141], v[54:57]
	v_mfma_f32_16x16x32_f16 v[66:69], v[206:209], v[156:159], v[66:69]
	s_barrier
	ds_read_b128 v[130:133], v161
	ds_read_b128 v[210:213], v162
	ds_read_b128 v[160:163], v163
	ds_read_b128 v[214:217], v164
	s_barrier
	s_waitcnt lgkmcnt(0)
	v_mfma_f32_16x16x32_f16 v[58:61], v[188:191], v[130:133], v[58:61]
	v_mfma_f32_16x16x32_f16 v[14:17], v[166:169], v[130:133], v[14:17]
	v_mfma_f32_16x16x32_f16 v[22:25], v[166:169], v[160:163], v[22:25]
	v_mfma_f32_16x16x32_f16 v[164:167], v[198:201], v[210:213], v[58:61]
	v_mfma_f32_16x16x32_f16 v[58:61], v[188:191], v[160:163], v[70:73]
	v_mfma_f32_16x16x32_f16 v[46:49], v[180:183], v[160:163], v[46:49]
	v_mfma_f32_16x16x32_f16 v[168:171], v[198:201], v[214:217], v[58:61]
	v_mfma_f32_16x16x32_f16 v[58:61], v[202:205], v[130:133], v[78:81]
	v_mfma_f32_16x16x32_f16 v[14:17], v[176:179], v[210:213], v[14:17]
	v_mfma_f32_16x16x32_f16 v[34:37], v[180:183], v[130:133], v[34:37]
	v_mfma_f32_16x16x32_f16 v[46:49], v[184:187], v[214:217], v[46:49]
	v_mfma_f32_16x16x32_f16 v[78:81], v[206:209], v[210:213], v[58:61]
	v_mfma_f32_16x16x32_f16 v[58:61], v[202:205], v[160:163], v[86:89]
	v_mfma_f32_16x16x32_f16 v[22:25], v[176:179], v[214:217], v[22:25]
	v_mfma_f32_16x16x32_f16 v[34:37], v[184:187], v[210:213], v[34:37]
	v_mfma_f32_16x16x32_f16 v[86:89], v[206:209], v[214:217], v[58:61]
	s_barrier
	s_nop 2
	ds_read_b128 v[58:61], v173 offset:16384
	ds_read_b128 v[70:73], v173 offset:17408
	ds_read_b128 v[174:177], v173 offset:18432
	ds_read_b128 v[178:181], v173 offset:19456
	ds_read_b128 v[182:185], v173 offset:20480
	ds_read_b128 v[186:189], v173 offset:21504
	ds_read_b128 v[190:193], v173 offset:22528
	ds_read_b128 v[198:201], v173 offset:23552
	s_waitcnt vmcnt(4)
	s_barrier
	s_waitcnt lgkmcnt(0)
	v_mfma_f32_16x16x32_f16 v[26:29], v[58:61], v[134:137], v[26:29]
	v_mfma_f32_16x16x32_f16 v[26:29], v[70:73], v[138:141], v[26:29]
	v_mfma_f32_16x16x32_f16 v[38:41], v[58:61], v[152:155], v[38:41]
	v_mfma_f32_16x16x32_f16 v[50:53], v[174:177], v[134:137], v[50:53]
	v_mfma_f32_16x16x32_f16 v[62:65], v[174:177], v[152:155], v[62:65]
	v_mfma_f32_16x16x32_f16 v[74:77], v[182:185], v[134:137], v[74:77]
	v_mfma_f32_16x16x32_f16 v[82:85], v[182:185], v[152:155], v[82:85]
	v_mfma_f32_16x16x32_f16 v[90:93], v[190:193], v[134:137], v[90:93]
	v_mfma_f32_16x16x32_f16 v[94:97], v[190:193], v[152:155], v[94:97]
	v_mfma_f32_16x16x32_f16 v[38:41], v[70:73], v[156:159], v[38:41]
	v_mfma_f32_16x16x32_f16 v[50:53], v[178:181], v[138:141], v[50:53]
	v_mfma_f32_16x16x32_f16 v[62:65], v[178:181], v[156:159], v[62:65]
	v_mfma_f32_16x16x32_f16 v[74:77], v[186:189], v[138:141], v[74:77]
	v_mfma_f32_16x16x32_f16 v[82:85], v[186:189], v[156:159], v[82:85]
	v_mfma_f32_16x16x32_f16 v[90:93], v[198:201], v[138:141], v[90:93]
	v_mfma_f32_16x16x32_f16 v[94:97], v[198:201], v[156:159], v[94:97]
	v_mfma_f32_16x16x32_f16 v[98:101], v[58:61], v[130:133], v[98:101]
	v_mfma_f32_16x16x32_f16 v[58:61], v[58:61], v[160:163], v[102:105]
	v_mfma_f32_16x16x32_f16 v[102:105], v[70:73], v[214:217], v[58:61]
	v_mfma_f32_16x16x32_f16 v[58:61], v[174:177], v[130:133], v[106:109]
	v_mfma_f32_16x16x32_f16 v[106:109], v[178:181], v[210:213], v[58:61]
	v_mfma_f32_16x16x32_f16 v[58:61], v[174:177], v[160:163], v[110:113]
	v_mfma_f32_16x16x32_f16 v[202:205], v[178:181], v[214:217], v[58:61]
	v_mfma_f32_16x16x32_f16 v[58:61], v[182:185], v[130:133], v[114:117]
	v_mfma_f32_16x16x32_f16 v[206:209], v[186:189], v[210:213], v[58:61]
	v_mfma_f32_16x16x32_f16 v[58:61], v[182:185], v[160:163], v[118:121]
	v_mfma_f32_16x16x32_f16 v[218:221], v[186:189], v[214:217], v[58:61]
	v_mfma_f32_16x16x32_f16 v[58:61], v[190:193], v[130:133], v[122:125]
	v_mfma_f32_16x16x32_f16 v[98:101], v[70:73], v[210:213], v[98:101]
	v_mfma_f32_16x16x32_f16 v[210:213], v[198:201], v[210:213], v[58:61]
	v_mfma_f32_16x16x32_f16 v[58:61], v[190:193], v[160:163], v[126:129]
	v_mfma_f32_16x16x32_f16 v[198:201], v[198:201], v[214:217], v[58:61]
	s_barrier
	ds_read_b128 v[110:113], v144
	ds_read_b128 v[130:133], v145
	ds_read_b128 v[214:217], v150
	ds_read_b128 v[222:225], v151
	s_nop 0
	ds_read_b128 v[58:61], v173 offset:32768
	ds_read_b128 v[70:73], v173 offset:33792
	ds_read_b128 v[114:117], v173 offset:34816
	ds_read_b128 v[118:121], v173 offset:35840
	ds_read_b128 v[134:137], v173 offset:36864
	ds_read_b128 v[138:141], v173 offset:37888
	ds_read_b128 v[178:181], v173 offset:38912
	ds_read_b128 v[226:229], v173 offset:39936
	s_waitcnt vmcnt(2)
	s_barrier
	s_waitcnt lgkmcnt(0)
	v_mfma_f32_16x16x32_f16 v[2:5], v[58:61], v[110:113], v[2:5]
	v_mfma_f32_16x16x32_f16 v[190:193], v[70:73], v[130:133], v[2:5]
	v_mfma_f32_16x16x32_f16 v[2:5], v[58:61], v[214:217], v[6:9]
	v_mfma_f32_16x16x32_f16 v[158:161], v[70:73], v[222:225], v[2:5]
	v_mfma_f32_16x16x32_f16 v[2:5], v[114:117], v[110:113], v[10:13]
	v_mfma_f32_16x16x32_f16 v[186:189], v[118:121], v[130:133], v[2:5]
	v_mfma_f32_16x16x32_f16 v[2:5], v[114:117], v[214:217], v[18:21]
	v_mfma_f32_16x16x32_f16 v[154:157], v[118:121], v[222:225], v[2:5]
	v_mfma_f32_16x16x32_f16 v[2:5], v[134:137], v[110:113], v[30:33]
	v_mfma_f32_16x16x32_f16 v[182:185], v[138:141], v[130:133], v[2:5]
	v_mfma_f32_16x16x32_f16 v[2:5], v[134:137], v[214:217], v[42:45]
	v_mfma_f32_16x16x32_f16 v[150:153], v[138:141], v[222:225], v[2:5]
	v_mfma_f32_16x16x32_f16 v[2:5], v[178:181], v[110:113], v[54:57]
	v_mfma_f32_16x16x32_f16 v[174:177], v[226:229], v[130:133], v[2:5]
	v_mfma_f32_16x16x32_f16 v[2:5], v[178:181], v[214:217], v[66:69]
	v_mfma_f32_16x16x32_f16 v[142:145], v[226:229], v[222:225], v[2:5]
	s_barrier
	s_nop 4
	ds_read_b128 v[2:5], v146
	ds_read_b128 v[10:13], v147
	ds_read_b128 v[18:21], v148
	ds_read_b128 v[42:45], v149
	s_waitcnt vmcnt(0)
	s_barrier
	s_waitcnt lgkmcnt(0)
	v_mfma_f32_16x16x32_f16 v[6:9], v[58:61], v[2:5], v[14:17]
	v_mfma_f32_16x16x32_f16 v[126:129], v[70:73], v[10:13], v[6:9]
	v_mfma_f32_16x16x32_f16 v[6:9], v[58:61], v[18:21], v[22:25]
	v_mfma_f32_16x16x32_f16 v[70:73], v[70:73], v[42:45], v[6:9]
	v_mfma_f32_16x16x32_f16 v[6:9], v[114:117], v[2:5], v[34:37]
	v_mfma_f32_16x16x32_f16 v[122:125], v[118:121], v[10:13], v[6:9]
	v_mfma_f32_16x16x32_f16 v[6:9], v[114:117], v[18:21], v[46:49]
	v_mfma_f32_16x16x32_f16 v[58:61], v[118:121], v[42:45], v[6:9]
	v_mfma_f32_16x16x32_f16 v[6:9], v[134:137], v[2:5], v[164:167]
	v_mfma_f32_16x16x32_f16 v[118:121], v[138:141], v[10:13], v[6:9]
	v_mfma_f32_16x16x32_f16 v[6:9], v[134:137], v[18:21], v[168:171]
	v_mfma_f32_16x16x32_f16 v[46:49], v[138:141], v[42:45], v[6:9]
	v_mfma_f32_16x16x32_f16 v[6:9], v[178:181], v[2:5], v[78:81]
	v_mfma_f32_16x16x32_f16 v[114:117], v[226:229], v[10:13], v[6:9]
	v_mfma_f32_16x16x32_f16 v[6:9], v[178:181], v[18:21], v[86:89]
	v_mfma_f32_16x16x32_f16 v[30:33], v[226:229], v[42:45], v[6:9]
	s_barrier
	s_nop 4
	ds_read_b128 v[6:9], v173 offset:49152
	ds_read_b128 v[14:17], v173 offset:50176
	ds_read_b128 v[22:25], v173 offset:51200
	ds_read_b128 v[34:37], v173 offset:52224
	ds_read_b128 v[54:57], v173 offset:53248
	ds_read_b128 v[66:69], v173 offset:54272
	ds_read_b128 v[78:81], v173 offset:55296
	ds_read_b128 v[86:89], v173 offset:56320
	s_barrier
	s_waitcnt lgkmcnt(0)
	v_mfma_f32_16x16x32_f16 v[26:29], v[6:9], v[110:113], v[26:29]
	v_mfma_f32_16x16x32_f16 v[178:181], v[14:17], v[130:133], v[26:29]
	v_mfma_f32_16x16x32_f16 v[26:29], v[6:9], v[214:217], v[38:41]
	v_mfma_f32_16x16x32_f16 v[146:149], v[14:17], v[222:225], v[26:29]
	v_mfma_f32_16x16x32_f16 v[26:29], v[22:25], v[110:113], v[50:53]
	v_mfma_f32_16x16x32_f16 v[170:173], v[34:37], v[130:133], v[26:29]
	v_mfma_f32_16x16x32_f16 v[26:29], v[22:25], v[214:217], v[62:65]
	v_mfma_f32_16x16x32_f16 v[138:141], v[34:37], v[222:225], v[26:29]
	v_mfma_f32_16x16x32_f16 v[26:29], v[54:57], v[110:113], v[74:77]
	v_mfma_f32_16x16x32_f16 v[166:169], v[66:69], v[130:133], v[26:29]
	v_mfma_f32_16x16x32_f16 v[26:29], v[54:57], v[214:217], v[82:85]
	v_mfma_f32_16x16x32_f16 v[134:137], v[66:69], v[222:225], v[26:29]
	v_mfma_f32_16x16x32_f16 v[26:29], v[78:81], v[110:113], v[90:93]
	v_mfma_f32_16x16x32_f16 v[162:165], v[86:89], v[130:133], v[26:29]
	v_mfma_f32_16x16x32_f16 v[26:29], v[78:81], v[214:217], v[94:97]
	v_mfma_f32_16x16x32_f16 v[130:133], v[86:89], v[222:225], v[26:29]
	v_mfma_f32_16x16x32_f16 v[26:29], v[6:9], v[2:5], v[98:101]
	v_mfma_f32_16x16x32_f16 v[6:9], v[6:9], v[18:21], v[102:105]
	v_mfma_f32_16x16x32_f16 v[110:113], v[14:17], v[10:13], v[26:29]
	v_mfma_f32_16x16x32_f16 v[26:29], v[14:17], v[42:45], v[6:9]
	v_mfma_f32_16x16x32_f16 v[6:9], v[22:25], v[2:5], v[106:109]
	v_mfma_f32_16x16x32_f16 v[106:109], v[34:37], v[10:13], v[6:9]
	v_mfma_f32_16x16x32_f16 v[6:9], v[22:25], v[18:21], v[202:205]
	v_mfma_f32_16x16x32_f16 v[14:17], v[34:37], v[42:45], v[6:9]
	v_mfma_f32_16x16x32_f16 v[6:9], v[54:57], v[2:5], v[206:209]
	v_mfma_f32_16x16x32_f16 v[2:5], v[78:81], v[2:5], v[210:213]
	v_mfma_f32_16x16x32_f16 v[102:105], v[66:69], v[10:13], v[6:9]
	v_mfma_f32_16x16x32_f16 v[6:9], v[54:57], v[18:21], v[218:221]
	v_mfma_f32_16x16x32_f16 v[98:101], v[86:89], v[10:13], v[2:5]
	v_mfma_f32_16x16x32_f16 v[2:5], v[78:81], v[18:21], v[198:201]
	v_mfma_f32_16x16x32_f16 v[6:9], v[66:69], v[42:45], v[6:9]
	v_mfma_f32_16x16x32_f16 v[2:5], v[86:89], v[42:45], v[2:5]
	s_cmpk_gt_u32 s54, 0xff
	s_barrier
	s_cbranch_scc1 .LBB9_34
	s_barrier
	s_branch .LBB9_34

	.amdhsa_kernel _Z14gemm256_kernelILi2ELi512ELi2048EEv8GemmArgs
		.amdhsa_group_segment_fixed_size 0
		.amdhsa_private_segment_fixed_size 0
		.amdhsa_kernarg_size 592
		.amdhsa_user_sgpr_count 2
		.amdhsa_user_sgpr_dispatch_ptr 0
		.amdhsa_user_sgpr_queue_ptr 0
		.amdhsa_user_sgpr_kernarg_segment_ptr 1
		.amdhsa_user_sgpr_dispatch_id 0
		.amdhsa_user_sgpr_kernarg_preload_length 0
		.amdhsa_user_sgpr_kernarg_preload_offset 0
		.amdhsa_user_sgpr_private_segment_size 0
		.amdhsa_uses_dynamic_stack 0
		.amdhsa_enable_private_segment 0
		.amdhsa_system_sgpr_workgroup_id_x 1
		.amdhsa_system_sgpr_workgroup_id_y 0
		.amdhsa_system_sgpr_workgroup_id_z 0
		.amdhsa_system_sgpr_workgroup_info 0
		.amdhsa_system_vgpr_workitem_id 0
		.amdhsa_next_free_vgpr 254
		.amdhsa_next_free_sgpr 81
		.amdhsa_accum_offset 256
		.amdhsa_reserve_vcc 1
		.amdhsa_float_round_mode_32 0
		.amdhsa_float_round_mode_16_64 0
		.amdhsa_float_denorm_mode_32 3
		.amdhsa_float_denorm_mode_16_64 3
		.amdhsa_dx10_clamp 1
		.amdhsa_ieee_mode 1
		.amdhsa_fp16_overflow 0
		.amdhsa_tg_split 0
		.amdhsa_exception_fp_ieee_invalid_op 0
		.amdhsa_exception_fp_denorm_src 0
		.amdhsa_exception_fp_ieee_div_zero 0
		.amdhsa_exception_fp_ieee_overflow 0
		.amdhsa_exception_fp_ieee_underflow 0
		.amdhsa_exception_fp_ieee_inexact 0
		.amdhsa_exception_int_div_zero 0
	.end_amdhsa_kernel

.LBB10_11:
	v_lshlrev_b32_e32 v2, 14, v2
	s_lshl_b32 s64, s61, 6
	v_lshlrev_b32_e32 v6, 14, v6
	v_and_b32_e32 v2, 0xffff8000, v2
	s_lshl_b32 s63, s63, 13
	s_and_b32 s64, s64, 0x3000
	v_and_b32_e32 v6, 0xffff8000, v6
	v_lshl_add_u32 v2, v3, 11, v2
	v_and_b32_e32 v10, 48, v172
	v_lshlrev_b32_e32 v11, 6, v172
	v_lshl_add_u32 v6, v7, 11, v6
	s_add_u32 s46, s24, s46
	v_or_b32_e32 v2, v2, v4
	v_and_or_b32 v10, v11, s56, v10
	v_lshlrev_b32_e32 v11, 2, v172
	v_or_b32_e32 v6, v6, v8
	s_addc_u32 s47, s25, s47
	v_add_u32_sdwa v2, v2, sext(v5) dst_sel:DWORD dst_unused:UNUSED_PAD src0_sel:DWORD src1_sel:WORD_0
	v_and_b32_e32 v11, 32, v11
	v_add_u32_sdwa v6, v6, sext(v9) dst_sel:DWORD dst_unused:UNUSED_PAD src0_sel:DWORD src1_sel:WORD_0
	v_ashrrev_i32_e32 v3, 31, v2
	s_add_u32 s44, s22, s44
	v_xad_u32 v170, v10, v11, 0
	s_waitcnt vmcnt(6)
	v_ashrrev_i32_e32 v7, 31, v6
	v_lshlrev_b64 v[2:3], 1, v[2:3]
	s_addc_u32 s45, s23, s45
	v_add_u32_e32 v10, s64, v170
	v_lshlrev_b64 v[6:7], 1, v[6:7]
	v_lshl_add_u64 v[136:137], s[46:47], 0, v[2:3]
	v_lshl_add_u64 v[140:141], s[44:45], 0, v[2:3]
	v_mov_b32_e32 v2, 0
	v_add_u32_e32 v171, 0x10000, v10
	v_add_u32_e32 v173, 0x10400, v10
	v_add_u32_e32 v174, 0x10800, v10
	v_add_u32_e32 v175, 0x10c00, v10
	v_add_u32_e32 v162, 0x14000, v10
	v_add_u32_e32 v163, 0x14400, v10
	v_add_u32_e32 v164, 0x14800, v10
	v_add_u32_e32 v165, 0x14c00, v10
	v_add_u32_e32 v144, 0x18000, v10
	v_add_u32_e32 v145, 0x18400, v10
	v_add_u32_e32 v146, 0x18800, v10
	v_add_u32_e32 v147, 0x18c00, v10
	v_add_u32_e32 v150, 0x1c000, v10
	v_add_u32_e32 v151, 0x1c400, v10
	v_add_u32_e32 v152, 0x1c800, v10
	v_add_u32_e32 v153, 0x1cc00, v10
	v_lshl_add_u64 v[134:135], s[46:47], 0, v[6:7]
	v_lshl_add_u64 v[138:139], s[44:45], 0, v[6:7]
	s_mov_b32 s46, -2
	s_mov_b64 s[44:45], 0
	v_mov_b32_e32 v3, v2
	v_mov_b32_e32 v4, v2
	v_mov_b32_e32 v5, v2
	v_mov_b32_e32 v6, v2
	v_mov_b32_e32 v7, v2
	v_mov_b32_e32 v8, v2
	v_mov_b32_e32 v9, v2
	v_mov_b32_e32 v10, v2
	v_mov_b32_e32 v11, v2
	v_mov_b32_e32 v12, v2
	v_mov_b32_e32 v13, v2
	v_mov_b32_e32 v14, v2
	v_mov_b32_e32 v15, v2
	v_mov_b32_e32 v16, v2
	v_mov_b32_e32 v17, v2
	v_mov_b32_e32 v18, v2
	v_mov_b32_e32 v19, v2
	v_mov_b32_e32 v20, v2
	v_mov_b32_e32 v21, v2
	v_mov_b32_e32 v22, v2
	v_mov_b32_e32 v23, v2
	v_mov_b32_e32 v24, v2
	v_mov_b32_e32 v25, v2
	v_mov_b32_e32 v26, v2
	v_mov_b32_e32 v27, v2
	v_mov_b32_e32 v28, v2
	v_mov_b32_e32 v29, v2
	v_mov_b32_e32 v30, v2
	v_mov_b32_e32 v31, v2
	v_mov_b32_e32 v32, v2
	v_mov_b32_e32 v33, v2
	v_mov_b32_e32 v34, v2
	v_mov_b32_e32 v35, v2
	v_mov_b32_e32 v36, v2
	v_mov_b32_e32 v37, v2
	v_mov_b32_e32 v38, v2
	v_mov_b32_e32 v39, v2
	v_mov_b32_e32 v40, v2
	v_mov_b32_e32 v41, v2
	v_mov_b32_e32 v42, v2
	v_mov_b32_e32 v43, v2
	v_mov_b32_e32 v44, v2
	v_mov_b32_e32 v45, v2
	v_mov_b32_e32 v46, v2
	v_mov_b32_e32 v47, v2
	v_mov_b32_e32 v48, v2
	v_mov_b32_e32 v49, v2
	v_mov_b32_e32 v50, v2
	v_mov_b32_e32 v51, v2
	v_mov_b32_e32 v52, v2
	v_mov_b32_e32 v53, v2
	v_mov_b32_e32 v54, v2
	v_mov_b32_e32 v55, v2
	v_mov_b32_e32 v56, v2
	v_mov_b32_e32 v57, v2
	v_mov_b32_e32 v58, v2
	v_mov_b32_e32 v59, v2
	v_mov_b32_e32 v60, v2
	v_mov_b32_e32 v61, v2
	v_mov_b32_e32 v62, v2
	v_mov_b32_e32 v63, v2
	v_mov_b32_e32 v64, v2
	v_mov_b32_e32 v65, v2
	v_mov_b32_e32 v66, v2
	v_mov_b32_e32 v67, v2
	v_mov_b32_e32 v68, v2
	v_mov_b32_e32 v69, v2
	v_mov_b32_e32 v70, v2
	v_mov_b32_e32 v71, v2
	v_mov_b32_e32 v72, v2
	v_mov_b32_e32 v73, v2
	v_mov_b32_e32 v74, v2
	v_mov_b32_e32 v75, v2
	v_mov_b32_e32 v76, v2
	v_mov_b32_e32 v77, v2
	v_mov_b32_e32 v78, v2
	v_mov_b32_e32 v79, v2
	v_mov_b32_e32 v80, v2
	v_mov_b32_e32 v81, v2
	v_mov_b32_e32 v82, v2
	v_mov_b32_e32 v83, v2
	v_mov_b32_e32 v84, v2
	v_mov_b32_e32 v85, v2
	v_mov_b32_e32 v86, v2
	v_mov_b32_e32 v87, v2
	v_mov_b32_e32 v88, v2
	v_mov_b32_e32 v89, v2
	v_mov_b32_e32 v90, v2
	v_mov_b32_e32 v91, v2
	v_mov_b32_e32 v92, v2
	v_mov_b32_e32 v93, v2
	v_mov_b32_e32 v94, v2
	v_mov_b32_e32 v95, v2
	v_mov_b32_e32 v96, v2
	v_mov_b32_e32 v97, v2
	v_mov_b32_e32 v98, v2
	v_mov_b32_e32 v99, v2
	v_mov_b32_e32 v100, v2
	v_mov_b32_e32 v101, v2
	v_mov_b32_e32 v102, v2
	v_mov_b32_e32 v103, v2
	v_mov_b32_e32 v104, v2
	v_mov_b32_e32 v105, v2
	v_mov_b32_e32 v106, v2
	v_mov_b32_e32 v107, v2
	v_mov_b32_e32 v108, v2
	v_mov_b32_e32 v109, v2
	v_mov_b32_e32 v110, v2
	v_mov_b32_e32 v111, v2
	v_mov_b32_e32 v112, v2
	v_mov_b32_e32 v113, v2
	v_mov_b32_e32 v114, v2
	v_mov_b32_e32 v115, v2
	v_mov_b32_e32 v116, v2
	v_mov_b32_e32 v117, v2
	v_mov_b32_e32 v118, v2
	v_mov_b32_e32 v119, v2
	v_mov_b32_e32 v120, v2
	v_mov_b32_e32 v121, v2
	v_mov_b32_e32 v122, v2
	v_mov_b32_e32 v123, v2
	v_mov_b32_e32 v124, v2
	v_mov_b32_e32 v125, v2
	v_mov_b32_e32 v126, v2
	v_mov_b32_e32 v127, v2
	v_mov_b32_e32 v128, v2
	v_mov_b32_e32 v129, v2
	v_add_u32_e32 v177, 0xc000, v148
	v_add_u32_e32 v178, 0xe000, v148
	s_nop 0
	v_readfirstlane_b32 s70, v177
	v_readfirstlane_b32 s71, v178
	v_readfirstlane_b32 s72, v142
	v_readfirstlane_b32 s73, v143
	v_readfirstlane_b32 s74, v148
	v_readfirstlane_b32 s75, v149
	v_readfirstlane_b32 s76, v154
	v_readfirstlane_b32 s77, v155
	v_readfirstlane_b32 s78, v156
	v_readfirstlane_b32 s79, v157
	v_readfirstlane_b32 s80, v158
	v_readfirstlane_b32 s81, v160
	v_readfirstlane_b32 s82, v161
	v_readfirstlane_b32 s83, v166
	v_readfirstlane_b32 s84, v168
	v_readfirstlane_b32 s85, v169
	s_barrier
	s_barrier
.LBB10_12:
	ds_read_b128 v[182:185], v171
	ds_read_b128 v[186:189], v173
	ds_read_b128 v[190:193], v174
	ds_read_b128 v[194:197], v175
	v_add_u32_e32 v177, 0xc000, v148
	v_lshl_add_u64 v[246:247], v[136:137], 0, s[44:45]
	v_add_u32_e32 v176, s63, v170
	v_lshl_add_u64 v[178:179], v[246:247], 0, s[28:29]
	s_mov_b32 m0, s70
	ds_read_b128 v[198:201], v176
	ds_read_b128 v[202:205], v176 offset:1024
	ds_read_b128 v[206:209], v176 offset:2048
	ds_read_b128 v[210:213], v176 offset:3072
	ds_read_b128 v[214:217], v176 offset:4096
	ds_read_b128 v[218:221], v176 offset:5120
	ds_read_b128 v[222:225], v176 offset:6144
	ds_read_b128 v[226:229], v176 offset:7168
	global_load_lds_dwordx4 v[178:179], off
	v_add_u32_e32 v178, 0xe000, v148
	v_lshl_add_u64 v[248:249], v[134:135], 0, s[44:45]
	v_lshl_add_u64 v[230:231], v[248:249], 0, s[28:29]
	s_mov_b32 m0, s71
	s_nop 0
	global_load_lds_dwordx4 v[230:231], off
	s_waitcnt lgkmcnt(8)
	s_barrier
	s_waitcnt lgkmcnt(0)
	v_mfma_f32_16x16x32_f16 v[126:129], v[198:201], v[182:185], v[126:129]
	v_mfma_f32_16x16x32_f16 v[122:125], v[198:201], v[190:193], v[122:125]
	v_mfma_f32_16x16x32_f16 v[118:121], v[206:209], v[182:185], v[118:121]
	v_mfma_f32_16x16x32_f16 v[114:117], v[206:209], v[190:193], v[114:117]
	v_mfma_f32_16x16x32_f16 v[110:113], v[214:217], v[182:185], v[110:113]
	v_mfma_f32_16x16x32_f16 v[106:109], v[214:217], v[190:193], v[106:109]
	v_mfma_f32_16x16x32_f16 v[102:105], v[222:225], v[182:185], v[102:105]
	v_mfma_f32_16x16x32_f16 v[98:101], v[222:225], v[190:193], v[98:101]
	v_mfma_f32_16x16x32_f16 v[126:129], v[202:205], v[186:189], v[126:129]
	v_mfma_f32_16x16x32_f16 v[122:125], v[202:205], v[194:197], v[122:125]
	v_mfma_f32_16x16x32_f16 v[118:121], v[210:213], v[186:189], v[118:121]
	v_mfma_f32_16x16x32_f16 v[114:117], v[210:213], v[194:197], v[114:117]
	v_mfma_f32_16x16x32_f16 v[110:113], v[218:221], v[186:189], v[110:113]
	v_mfma_f32_16x16x32_f16 v[106:109], v[218:221], v[194:197], v[106:109]
	v_mfma_f32_16x16x32_f16 v[102:105], v[226:229], v[186:189], v[102:105]
	v_mfma_f32_16x16x32_f16 v[98:101], v[226:229], v[194:197], v[98:101]
	s_barrier
	v_lshl_add_u64 v[250:251], v[140:141], 0, s[44:45]
	v_lshl_add_u64 v[252:253], v[250:251], 0, s[30:31]
	s_mov_b32 m0, s72
	ds_read_b128 v[230:233], v162
	ds_read_b128 v[234:237], v163
	ds_read_b128 v[238:241], v164
	ds_read_b128 v[242:245], v165
	global_load_lds_dwordx4 v[252:253], off
	v_lshl_add_u64 v[252:253], v[138:139], 0, s[44:45]
	v_lshl_add_u64 v[254:255], v[252:253], 0, s[30:31]
	s_mov_b32 m0, s73
	s_nop 0
	global_load_lds_dwordx4 v[254:255], off
	s_barrier
	s_waitcnt lgkmcnt(0)
	v_mfma_f32_16x16x32_f16 v[94:97], v[198:201], v[230:233], v[94:97]
	v_mfma_f32_16x16x32_f16 v[90:93], v[198:201], v[238:241], v[90:93]
	v_mfma_f32_16x16x32_f16 v[86:89], v[206:209], v[230:233], v[86:89]
	v_mfma_f32_16x16x32_f16 v[82:85], v[206:209], v[238:241], v[82:85]
	v_mfma_f32_16x16x32_f16 v[78:81], v[214:217], v[230:233], v[78:81]
	v_mfma_f32_16x16x32_f16 v[74:77], v[214:217], v[238:241], v[74:77]
	v_mfma_f32_16x16x32_f16 v[70:73], v[222:225], v[230:233], v[70:73]
	v_mfma_f32_16x16x32_f16 v[66:69], v[222:225], v[238:241], v[66:69]
	v_mfma_f32_16x16x32_f16 v[94:97], v[202:205], v[234:237], v[94:97]
	v_mfma_f32_16x16x32_f16 v[90:93], v[202:205], v[242:245], v[90:93]
	v_mfma_f32_16x16x32_f16 v[86:89], v[210:213], v[234:237], v[86:89]
	v_mfma_f32_16x16x32_f16 v[82:85], v[210:213], v[242:245], v[82:85]
	v_mfma_f32_16x16x32_f16 v[78:81], v[218:221], v[234:237], v[78:81]
	v_mfma_f32_16x16x32_f16 v[74:77], v[218:221], v[242:245], v[74:77]
	v_mfma_f32_16x16x32_f16 v[70:73], v[226:229], v[234:237], v[70:73]
	v_mfma_f32_16x16x32_f16 v[66:69], v[226:229], v[242:245], v[66:69]
	v_lshl_add_u64 v[254:255], v[246:247], 0, s[30:31]
	s_mov_b32 m0, s74
	s_barrier
	ds_read_b128 v[198:201], v176 offset:16384
	ds_read_b128 v[202:205], v176 offset:17408
	ds_read_b128 v[206:209], v176 offset:18432
	ds_read_b128 v[210:213], v176 offset:19456
	ds_read_b128 v[214:217], v176 offset:20480
	ds_read_b128 v[218:221], v176 offset:21504
	ds_read_b128 v[222:225], v176 offset:22528
	ds_read_b128 v[226:229], v176 offset:23552
	global_load_lds_dwordx4 v[254:255], off
	v_lshl_add_u64 v[254:255], v[248:249], 0, s[30:31]
	s_mov_b32 m0, s75
	s_nop 0
	global_load_lds_dwordx4 v[254:255], off
	s_barrier
	s_waitcnt lgkmcnt(0)
	v_mfma_f32_16x16x32_f16 v[62:65], v[198:201], v[182:185], v[62:65]
	v_mfma_f32_16x16x32_f16 v[58:61], v[198:201], v[190:193], v[58:61]
	v_mfma_f32_16x16x32_f16 v[54:57], v[206:209], v[182:185], v[54:57]
	v_mfma_f32_16x16x32_f16 v[50:53], v[206:209], v[190:193], v[50:53]
	v_mfma_f32_16x16x32_f16 v[46:49], v[214:217], v[182:185], v[46:49]
	v_mfma_f32_16x16x32_f16 v[42:45], v[214:217], v[190:193], v[42:45]
	v_mfma_f32_16x16x32_f16 v[38:41], v[222:225], v[182:185], v[38:41]
	v_mfma_f32_16x16x32_f16 v[34:37], v[222:225], v[190:193], v[34:37]
	v_mfma_f32_16x16x32_f16 v[62:65], v[202:205], v[186:189], v[62:65]
	v_mfma_f32_16x16x32_f16 v[58:61], v[202:205], v[194:197], v[58:61]
	v_mfma_f32_16x16x32_f16 v[54:57], v[210:213], v[186:189], v[54:57]
	v_mfma_f32_16x16x32_f16 v[50:53], v[210:213], v[194:197], v[50:53]
	v_mfma_f32_16x16x32_f16 v[46:49], v[218:221], v[186:189], v[46:49]
	v_mfma_f32_16x16x32_f16 v[42:45], v[218:221], v[194:197], v[42:45]
	v_mfma_f32_16x16x32_f16 v[38:41], v[226:229], v[186:189], v[38:41]
	v_mfma_f32_16x16x32_f16 v[34:37], v[226:229], v[194:197], v[34:37]
	s_barrier
	v_lshl_add_u64 v[182:183], v[250:251], 0, s[34:35]
	s_mov_b32 m0, s76
	global_load_lds_dwordx4 v[182:183], off
	v_lshl_add_u64 v[182:183], v[252:253], 0, s[34:35]
	s_mov_b32 m0, s77
	s_nop 0
	global_load_lds_dwordx4 v[182:183], off
	s_waitcnt vmcnt(6)
	s_barrier
	v_mfma_f32_16x16x32_f16 v[30:33], v[198:201], v[230:233], v[30:33]
	v_mfma_f32_16x16x32_f16 v[26:29], v[198:201], v[238:241], v[26:29]
	v_mfma_f32_16x16x32_f16 v[22:25], v[206:209], v[230:233], v[22:25]
	v_mfma_f32_16x16x32_f16 v[18:21], v[206:209], v[238:241], v[18:21]
	v_mfma_f32_16x16x32_f16 v[14:17], v[214:217], v[230:233], v[14:17]
	v_mfma_f32_16x16x32_f16 v[10:13], v[214:217], v[238:241], v[10:13]
	v_mfma_f32_16x16x32_f16 v[6:9], v[222:225], v[230:233], v[6:9]
	v_mfma_f32_16x16x32_f16 v[2:5], v[222:225], v[238:241], v[2:5]
	v_mfma_f32_16x16x32_f16 v[30:33], v[202:205], v[234:237], v[30:33]
	v_mfma_f32_16x16x32_f16 v[26:29], v[202:205], v[242:245], v[26:29]
	v_mfma_f32_16x16x32_f16 v[22:25], v[210:213], v[234:237], v[22:25]
	v_mfma_f32_16x16x32_f16 v[18:21], v[210:213], v[242:245], v[18:21]
	v_mfma_f32_16x16x32_f16 v[14:17], v[218:221], v[234:237], v[14:17]
	v_mfma_f32_16x16x32_f16 v[10:13], v[218:221], v[242:245], v[10:13]
	v_mfma_f32_16x16x32_f16 v[6:9], v[226:229], v[234:237], v[6:9]
	v_mfma_f32_16x16x32_f16 v[2:5], v[226:229], v[242:245], v[2:5]
	s_barrier
	ds_read_b128 v[182:185], v144
	ds_read_b128 v[186:189], v145
	ds_read_b128 v[190:193], v146
	ds_read_b128 v[194:197], v147
	v_lshl_add_u64 v[230:231], v[246:247], 0, s[34:35]
	s_mov_b32 m0, s78
	ds_read_b128 v[198:201], v176 offset:32768
	ds_read_b128 v[202:205], v176 offset:33792
	ds_read_b128 v[206:209], v176 offset:34816
	ds_read_b128 v[210:213], v176 offset:35840
	ds_read_b128 v[214:217], v176 offset:36864
	ds_read_b128 v[218:221], v176 offset:37888
	ds_read_b128 v[222:225], v176 offset:38912
	ds_read_b128 v[226:229], v176 offset:39936
	global_load_lds_dwordx4 v[230:231], off
	v_lshl_add_u64 v[230:231], v[248:249], 0, s[34:35]
	s_mov_b32 m0, s79
	s_nop 0
	global_load_lds_dwordx4 v[230:231], off
	s_waitcnt lgkmcnt(8)
	s_barrier
	s_waitcnt lgkmcnt(0)
	v_mfma_f32_16x16x32_f16 v[126:129], v[198:201], v[182:185], v[126:129]
	v_mfma_f32_16x16x32_f16 v[122:125], v[198:201], v[190:193], v[122:125]
	v_mfma_f32_16x16x32_f16 v[118:121], v[206:209], v[182:185], v[118:121]
	v_mfma_f32_16x16x32_f16 v[114:117], v[206:209], v[190:193], v[114:117]
	v_mfma_f32_16x16x32_f16 v[110:113], v[214:217], v[182:185], v[110:113]
	v_mfma_f32_16x16x32_f16 v[106:109], v[214:217], v[190:193], v[106:109]
	v_mfma_f32_16x16x32_f16 v[102:105], v[222:225], v[182:185], v[102:105]
	v_mfma_f32_16x16x32_f16 v[98:101], v[222:225], v[190:193], v[98:101]
	v_mfma_f32_16x16x32_f16 v[126:129], v[202:205], v[186:189], v[126:129]
	v_mfma_f32_16x16x32_f16 v[122:125], v[202:205], v[194:197], v[122:125]
	v_mfma_f32_16x16x32_f16 v[118:121], v[210:213], v[186:189], v[118:121]
	v_mfma_f32_16x16x32_f16 v[114:117], v[210:213], v[194:197], v[114:117]
	v_mfma_f32_16x16x32_f16 v[110:113], v[218:221], v[186:189], v[110:113]
	v_mfma_f32_16x16x32_f16 v[106:109], v[218:221], v[194:197], v[106:109]
	v_mfma_f32_16x16x32_f16 v[102:105], v[226:229], v[186:189], v[102:105]
	v_mfma_f32_16x16x32_f16 v[98:101], v[226:229], v[194:197], v[98:101]
	s_barrier
	v_lshl_add_u64 v[254:255], v[250:251], 0, s[36:37]
	s_mov_b32 m0, s80
	ds_read_b128 v[230:233], v150
	ds_read_b128 v[234:237], v151
	ds_read_b128 v[238:241], v152
	ds_read_b128 v[242:245], v153
	global_load_lds_dwordx4 v[254:255], off
	v_lshl_add_u64 v[254:255], v[252:253], 0, s[36:37]
	s_mov_b32 m0, s81
	s_nop 0
	global_load_lds_dwordx4 v[254:255], off
	s_barrier
	s_waitcnt lgkmcnt(0)
	v_mfma_f32_16x16x32_f16 v[94:97], v[198:201], v[230:233], v[94:97]
	v_mfma_f32_16x16x32_f16 v[90:93], v[198:201], v[238:241], v[90:93]
	v_mfma_f32_16x16x32_f16 v[86:89], v[206:209], v[230:233], v[86:89]
	v_mfma_f32_16x16x32_f16 v[82:85], v[206:209], v[238:241], v[82:85]
	v_mfma_f32_16x16x32_f16 v[78:81], v[214:217], v[230:233], v[78:81]
	v_mfma_f32_16x16x32_f16 v[74:77], v[214:217], v[238:241], v[74:77]
	v_mfma_f32_16x16x32_f16 v[70:73], v[222:225], v[230:233], v[70:73]
	v_mfma_f32_16x16x32_f16 v[66:69], v[222:225], v[238:241], v[66:69]
	v_mfma_f32_16x16x32_f16 v[94:97], v[202:205], v[234:237], v[94:97]
	v_mfma_f32_16x16x32_f16 v[90:93], v[202:205], v[242:245], v[90:93]
	v_mfma_f32_16x16x32_f16 v[86:89], v[210:213], v[234:237], v[86:89]
	v_mfma_f32_16x16x32_f16 v[82:85], v[210:213], v[242:245], v[82:85]
	v_mfma_f32_16x16x32_f16 v[78:81], v[218:221], v[234:237], v[78:81]
	v_mfma_f32_16x16x32_f16 v[74:77], v[218:221], v[242:245], v[74:77]
	v_mfma_f32_16x16x32_f16 v[70:73], v[226:229], v[234:237], v[70:73]
	v_mfma_f32_16x16x32_f16 v[66:69], v[226:229], v[242:245], v[66:69]
	v_lshl_add_u64 v[246:247], v[246:247], 0, s[36:37]
	s_mov_b32 m0, s82
	s_barrier
	ds_read_b128 v[198:201], v176 offset:49152
	ds_read_b128 v[202:205], v176 offset:50176
	ds_read_b128 v[206:209], v176 offset:51200
	ds_read_b128 v[210:213], v176 offset:52224
	ds_read_b128 v[214:217], v176 offset:53248
	ds_read_b128 v[218:221], v176 offset:54272
	ds_read_b128 v[222:225], v176 offset:55296
	ds_read_b128 v[226:229], v176 offset:56320
	global_load_lds_dwordx4 v[246:247], off
	v_lshl_add_u64 v[246:247], v[248:249], 0, s[36:37]
	s_mov_b32 m0, s83
	s_nop 0
	global_load_lds_dwordx4 v[246:247], off
	s_barrier
	s_waitcnt lgkmcnt(0)
	v_mfma_f32_16x16x32_f16 v[62:65], v[198:201], v[182:185], v[62:65]
	v_mfma_f32_16x16x32_f16 v[58:61], v[198:201], v[190:193], v[58:61]
	v_mfma_f32_16x16x32_f16 v[54:57], v[206:209], v[182:185], v[54:57]
	v_mfma_f32_16x16x32_f16 v[50:53], v[206:209], v[190:193], v[50:53]
	v_mfma_f32_16x16x32_f16 v[46:49], v[214:217], v[182:185], v[46:49]
	v_mfma_f32_16x16x32_f16 v[42:45], v[214:217], v[190:193], v[42:45]
	v_mfma_f32_16x16x32_f16 v[38:41], v[222:225], v[182:185], v[38:41]
	v_mfma_f32_16x16x32_f16 v[34:37], v[222:225], v[190:193], v[34:37]
	v_mfma_f32_16x16x32_f16 v[62:65], v[202:205], v[186:189], v[62:65]
	v_mfma_f32_16x16x32_f16 v[58:61], v[202:205], v[194:197], v[58:61]
	v_mfma_f32_16x16x32_f16 v[54:57], v[210:213], v[186:189], v[54:57]
	v_mfma_f32_16x16x32_f16 v[50:53], v[210:213], v[194:197], v[50:53]
	v_mfma_f32_16x16x32_f16 v[46:49], v[218:221], v[186:189], v[46:49]
	v_mfma_f32_16x16x32_f16 v[42:45], v[218:221], v[194:197], v[42:45]
	v_mfma_f32_16x16x32_f16 v[38:41], v[226:229], v[186:189], v[38:41]
	v_mfma_f32_16x16x32_f16 v[34:37], v[226:229], v[194:197], v[34:37]
	s_barrier
	v_lshl_add_u64 v[182:183], v[250:251], 0, s[38:39]
	s_mov_b32 m0, s84
	global_load_lds_dwordx4 v[182:183], off
	v_lshl_add_u64 v[182:183], v[252:253], 0, s[38:39]
	s_mov_b32 m0, s85
	s_nop 0
	global_load_lds_dwordx4 v[182:183], off
	s_waitcnt vmcnt(6)
	s_barrier
	v_mfma_f32_16x16x32_f16 v[30:33], v[198:201], v[230:233], v[30:33]
	v_mfma_f32_16x16x32_f16 v[26:29], v[198:201], v[238:241], v[26:29]
	v_mfma_f32_16x16x32_f16 v[22:25], v[206:209], v[230:233], v[22:25]
	v_mfma_f32_16x16x32_f16 v[18:21], v[206:209], v[238:241], v[18:21]
	v_mfma_f32_16x16x32_f16 v[14:17], v[214:217], v[230:233], v[14:17]
	v_mfma_f32_16x16x32_f16 v[10:13], v[214:217], v[238:241], v[10:13]
	v_mfma_f32_16x16x32_f16 v[6:9], v[222:225], v[230:233], v[6:9]
	v_mfma_f32_16x16x32_f16 v[2:5], v[222:225], v[238:241], v[2:5]
	v_mfma_f32_16x16x32_f16 v[30:33], v[202:205], v[234:237], v[30:33]
	v_mfma_f32_16x16x32_f16 v[26:29], v[202:205], v[242:245], v[26:29]
	v_mfma_f32_16x16x32_f16 v[22:25], v[210:213], v[234:237], v[22:25]
	v_mfma_f32_16x16x32_f16 v[18:21], v[210:213], v[242:245], v[18:21]
	v_mfma_f32_16x16x32_f16 v[14:17], v[218:221], v[234:237], v[14:17]
	v_mfma_f32_16x16x32_f16 v[10:13], v[218:221], v[242:245], v[10:13]
	v_mfma_f32_16x16x32_f16 v[6:9], v[226:229], v[234:237], v[6:9]
	v_mfma_f32_16x16x32_f16 v[2:5], v[226:229], v[242:245], v[2:5]
	s_add_i32 s46, s46, 2
	s_add_u32 s44, s44, 0x100
	s_addc_u32 s45, s45, 0
	s_cmp_lt_u32 s46, 28
	s_barrier
	s_cbranch_scc1 .LBB10_12
	s_add_u32 s42, s42, 0x80f80
	s_addc_u32 s43, s43, 0
	v_readfirstlane_b32 s44, v177
	v_lshl_add_u64 v[130:131], v[130:131], 1, s[42:43]
	s_mov_b32 m0, s44
	ds_read_b128 v[134:137], v171
	ds_read_b128 v[138:141], v173
	ds_read_b128 v[154:157], v174
	ds_read_b128 v[168:171], v175
	ds_read_b128 v[182:185], v176
	ds_read_b128 v[186:189], v176 offset:1024
	ds_read_b128 v[190:193], v176 offset:2048
	ds_read_b128 v[194:197], v176 offset:3072
	ds_read_b128 v[198:201], v176 offset:4096
	ds_read_b128 v[202:205], v176 offset:5120
	ds_read_b128 v[206:209], v176 offset:6144
	ds_read_b128 v[210:213], v176 offset:7168
	global_load_lds_dwordx4 v[130:131], off
	v_lshl_add_u64 v[130:131], v[132:133], 1, s[42:43]
	v_readfirstlane_b32 s42, v178
	s_mov_b32 m0, s42
	s_nop 0
	global_load_lds_dwordx4 v[130:131], off
	s_barrier
	s_waitcnt lgkmcnt(0)
	v_mfma_f32_16x16x32_f16 v[122:125], v[182:185], v[154:157], v[122:125]
	v_mfma_f32_16x16x32_f16 v[110:113], v[198:201], v[134:137], v[110:113]
	v_mfma_f32_16x16x32_f16 v[98:101], v[206:209], v[154:157], v[98:101]
	v_mfma_f32_16x16x32_f16 v[126:129], v[182:185], v[134:137], v[126:129]
	v_mfma_f32_16x16x32_f16 v[122:125], v[186:189], v[168:171], v[122:125]
	v_mfma_f32_16x16x32_f16 v[118:121], v[190:193], v[134:137], v[118:121]
	v_mfma_f32_16x16x32_f16 v[114:117], v[190:193], v[154:157], v[114:117]
	v_mfma_f32_16x16x32_f16 v[130:133], v[202:205], v[138:141], v[110:113]
	v_mfma_f32_16x16x32_f16 v[106:109], v[198:201], v[154:157], v[106:109]
	v_mfma_f32_16x16x32_f16 v[102:105], v[206:209], v[134:137], v[102:105]
	v_mfma_f32_16x16x32_f16 v[98:101], v[210:213], v[168:171], v[98:101]
	v_mfma_f32_16x16x32_f16 v[126:129], v[186:189], v[138:141], v[126:129]
	v_mfma_f32_16x16x32_f16 v[118:121], v[194:197], v[138:141], v[118:121]
	v_mfma_f32_16x16x32_f16 v[114:117], v[194:197], v[168:171], v[114:117]
	v_mfma_f32_16x16x32_f16 v[214:217], v[202:205], v[168:171], v[106:109]
	v_mfma_f32_16x16x32_f16 v[102:105], v[210:213], v[138:141], v[102:105]
	s_barrier
	ds_read_b128 v[106:109], v162
	ds_read_b128 v[110:113], v163
	ds_read_b128 v[160:163], v164
	ds_read_b128 v[218:221], v165
	s_barrier
	s_waitcnt lgkmcnt(0)
	v_mfma_f32_16x16x32_f16 v[82:85], v[190:193], v[160:163], v[82:85]
	v_mfma_f32_16x16x32_f16 v[78:81], v[198:201], v[106:109], v[78:81]
	v_mfma_f32_16x16x32_f16 v[74:77], v[198:201], v[160:163], v[74:77]
	v_mfma_f32_16x16x32_f16 v[70:73], v[206:209], v[106:109], v[70:73]
	v_mfma_f32_16x16x32_f16 v[66:69], v[206:209], v[160:163], v[66:69]
	v_mfma_f32_16x16x32_f16 v[94:97], v[182:185], v[106:109], v[94:97]
	v_mfma_f32_16x16x32_f16 v[90:93], v[182:185], v[160:163], v[90:93]
	v_mfma_f32_16x16x32_f16 v[86:89], v[190:193], v[106:109], v[86:89]
	v_mfma_f32_16x16x32_f16 v[82:85], v[194:197], v[218:221], v[82:85]
	v_mfma_f32_16x16x32_f16 v[78:81], v[202:205], v[110:113], v[78:81]
	v_mfma_f32_16x16x32_f16 v[74:77], v[202:205], v[218:221], v[74:77]
	v_mfma_f32_16x16x32_f16 v[70:73], v[210:213], v[110:113], v[70:73]
	v_mfma_f32_16x16x32_f16 v[66:69], v[210:213], v[218:221], v[66:69]
	v_mfma_f32_16x16x32_f16 v[222:225], v[186:189], v[110:113], v[94:97]
	v_mfma_f32_16x16x32_f16 v[182:185], v[186:189], v[218:221], v[90:93]
	v_mfma_f32_16x16x32_f16 v[86:89], v[194:197], v[110:113], v[86:89]
	s_barrier
	ds_read_b128 v[90:93], v176 offset:16384
	ds_read_b128 v[94:97], v176 offset:17408
	ds_read_b128 v[186:189], v176 offset:18432
	ds_read_b128 v[190:193], v176 offset:19456
	ds_read_b128 v[194:197], v176 offset:20480
	ds_read_b128 v[198:201], v176 offset:21504
	ds_read_b128 v[202:205], v176 offset:22528
	ds_read_b128 v[206:209], v176 offset:23552
	s_waitcnt vmcnt(4)
	s_barrier
	s_waitcnt lgkmcnt(0)
	v_mfma_f32_16x16x32_f16 v[46:49], v[194:197], v[134:137], v[46:49]
	v_mfma_f32_16x16x32_f16 v[42:45], v[194:197], v[154:157], v[42:45]
	v_mfma_f32_16x16x32_f16 v[38:41], v[202:205], v[134:137], v[38:41]
	v_mfma_f32_16x16x32_f16 v[34:37], v[202:205], v[154:157], v[34:37]
	v_mfma_f32_16x16x32_f16 v[62:65], v[90:93], v[134:137], v[62:65]
	v_mfma_f32_16x16x32_f16 v[58:61], v[90:93], v[154:157], v[58:61]
	v_mfma_f32_16x16x32_f16 v[54:57], v[186:189], v[134:137], v[54:57]
	v_mfma_f32_16x16x32_f16 v[50:53], v[186:189], v[154:157], v[50:53]
	v_mfma_f32_16x16x32_f16 v[46:49], v[198:201], v[138:141], v[46:49]
	v_mfma_f32_16x16x32_f16 v[42:45], v[198:201], v[168:171], v[42:45]
	v_mfma_f32_16x16x32_f16 v[38:41], v[206:209], v[138:141], v[38:41]
	v_mfma_f32_16x16x32_f16 v[34:37], v[206:209], v[168:171], v[34:37]
	v_mfma_f32_16x16x32_f16 v[210:213], v[94:97], v[138:141], v[62:65]
	v_mfma_f32_16x16x32_f16 v[226:229], v[94:97], v[168:171], v[58:61]
	v_mfma_f32_16x16x32_f16 v[230:233], v[190:193], v[138:141], v[54:57]
	v_mfma_f32_16x16x32_f16 v[234:237], v[190:193], v[168:171], v[50:53]
	v_mfma_f32_16x16x32_f16 v[2:5], v[202:205], v[160:163], v[2:5]
	v_mfma_f32_16x16x32_f16 v[30:33], v[90:93], v[106:109], v[30:33]
	v_mfma_f32_16x16x32_f16 v[26:29], v[90:93], v[160:163], v[26:29]
	v_mfma_f32_16x16x32_f16 v[22:25], v[186:189], v[106:109], v[22:25]
	v_mfma_f32_16x16x32_f16 v[18:21], v[186:189], v[160:163], v[18:21]
	v_mfma_f32_16x16x32_f16 v[14:17], v[194:197], v[106:109], v[14:17]
	v_mfma_f32_16x16x32_f16 v[10:13], v[194:197], v[160:163], v[10:13]
	v_mfma_f32_16x16x32_f16 v[6:9], v[202:205], v[106:109], v[6:9]
	v_mfma_f32_16x16x32_f16 v[2:5], v[206:209], v[218:221], v[2:5]
	v_mfma_f32_16x16x32_f16 v[138:141], v[94:97], v[110:113], v[30:33]
	v_mfma_f32_16x16x32_f16 v[168:171], v[94:97], v[218:221], v[26:29]
	v_mfma_f32_16x16x32_f16 v[238:241], v[190:193], v[110:113], v[22:25]
	v_mfma_f32_16x16x32_f16 v[186:189], v[190:193], v[218:221], v[18:21]
	v_mfma_f32_16x16x32_f16 v[190:193], v[198:201], v[110:113], v[14:17]
	v_mfma_f32_16x16x32_f16 v[194:197], v[198:201], v[218:221], v[10:13]
	v_mfma_f32_16x16x32_f16 v[198:201], v[206:209], v[110:113], v[6:9]
	s_barrier
	s_nop 0
	ds_read_b128 v[6:9], v144
	ds_read_b128 v[10:13], v145
	ds_read_b128 v[14:17], v146
	ds_read_b128 v[160:163], v147
	ds_read_b128 v[18:21], v176 offset:32768
	ds_read_b128 v[22:25], v176 offset:33792
	ds_read_b128 v[26:29], v176 offset:34816
	ds_read_b128 v[50:53], v176 offset:35840
	ds_read_b128 v[202:205], v176 offset:36864
	ds_read_b128 v[206:209], v176 offset:37888
	ds_read_b128 v[218:221], v176 offset:38912
	ds_read_b128 v[242:245], v176 offset:39936
	s_waitcnt vmcnt(2)
	s_barrier
	s_waitcnt lgkmcnt(0)
	v_mfma_f32_16x16x32_f16 v[30:33], v[18:21], v[6:9], v[126:129]
	v_mfma_f32_16x16x32_f16 v[154:157], v[22:25], v[10:13], v[30:33]
	v_mfma_f32_16x16x32_f16 v[30:33], v[18:21], v[14:17], v[122:125]
	v_mfma_f32_16x16x32_f16 v[110:113], v[22:25], v[160:163], v[30:33]
	v_mfma_f32_16x16x32_f16 v[30:33], v[26:29], v[6:9], v[118:121]
	v_mfma_f32_16x16x32_f16 v[146:149], v[50:53], v[10:13], v[30:33]
	v_mfma_f32_16x16x32_f16 v[30:33], v[26:29], v[14:17], v[114:117]
	v_mfma_f32_16x16x32_f16 v[106:109], v[50:53], v[160:163], v[30:33]
	v_mfma_f32_16x16x32_f16 v[30:33], v[202:205], v[6:9], v[130:133]
	v_mfma_f32_16x16x32_f16 v[142:145], v[206:209], v[10:13], v[30:33]
	v_mfma_f32_16x16x32_f16 v[30:33], v[202:205], v[14:17], v[214:217]
	v_mfma_f32_16x16x32_f16 v[94:97], v[206:209], v[160:163], v[30:33]
	v_mfma_f32_16x16x32_f16 v[30:33], v[218:221], v[6:9], v[102:105]
	v_mfma_f32_16x16x32_f16 v[134:137], v[242:245], v[10:13], v[30:33]
	v_mfma_f32_16x16x32_f16 v[30:33], v[218:221], v[14:17], v[98:101]
	v_mfma_f32_16x16x32_f16 v[90:93], v[242:245], v[160:163], v[30:33]
	s_barrier
	ds_read_b128 v[102:105], v150
	ds_read_b128 v[114:117], v151
	ds_read_b128 v[118:121], v152
	ds_read_b128 v[126:129], v153
	s_waitcnt vmcnt(0)
	s_barrier
	s_waitcnt lgkmcnt(0)
	v_mfma_f32_16x16x32_f16 v[30:33], v[18:21], v[102:105], v[222:225]
	v_mfma_f32_16x16x32_f16 v[18:21], v[18:21], v[118:121], v[182:185]
	v_mfma_f32_16x16x32_f16 v[62:65], v[22:25], v[114:117], v[30:33]
	v_mfma_f32_16x16x32_f16 v[30:33], v[22:25], v[126:129], v[18:21]
	v_mfma_f32_16x16x32_f16 v[18:21], v[26:29], v[102:105], v[86:89]
	v_mfma_f32_16x16x32_f16 v[58:61], v[50:53], v[114:117], v[18:21]
	v_mfma_f32_16x16x32_f16 v[18:21], v[26:29], v[118:121], v[82:85]
	v_mfma_f32_16x16x32_f16 v[26:29], v[50:53], v[126:129], v[18:21]
	v_mfma_f32_16x16x32_f16 v[18:21], v[202:205], v[102:105], v[78:81]
	v_mfma_f32_16x16x32_f16 v[54:57], v[206:209], v[114:117], v[18:21]
	v_mfma_f32_16x16x32_f16 v[18:21], v[202:205], v[118:121], v[74:77]
	v_mfma_f32_16x16x32_f16 v[22:25], v[206:209], v[126:129], v[18:21]
	v_mfma_f32_16x16x32_f16 v[18:21], v[218:221], v[102:105], v[70:73]
	v_mfma_f32_16x16x32_f16 v[50:53], v[242:245], v[114:117], v[18:21]
	v_mfma_f32_16x16x32_f16 v[18:21], v[218:221], v[118:121], v[66:69]
	v_mfma_f32_16x16x32_f16 v[18:21], v[242:245], v[126:129], v[18:21]
	s_barrier
	ds_read_b128 v[86:89], v176 offset:49152
	ds_read_b128 v[150:153], v176 offset:50176
	ds_read_b128 v[182:185], v176 offset:51200
	ds_read_b128 v[202:205], v176 offset:52224
	ds_read_b128 v[206:209], v176 offset:53248
	ds_read_b128 v[214:217], v176 offset:54272
	ds_read_b128 v[218:221], v176 offset:55296
	ds_read_b128 v[174:177], v176 offset:56320
	s_barrier
	s_waitcnt lgkmcnt(0)
	v_mfma_f32_16x16x32_f16 v[66:69], v[86:89], v[6:9], v[210:213]
	v_mfma_f32_16x16x32_f16 v[130:133], v[150:153], v[10:13], v[66:69]
	v_mfma_f32_16x16x32_f16 v[66:69], v[86:89], v[14:17], v[226:229]
	v_mfma_f32_16x16x32_f16 v[78:81], v[150:153], v[160:163], v[66:69]
	v_mfma_f32_16x16x32_f16 v[66:69], v[182:185], v[6:9], v[230:233]
	v_mfma_f32_16x16x32_f16 v[46:49], v[206:209], v[6:9], v[46:49]
	v_mfma_f32_16x16x32_f16 v[6:9], v[218:221], v[6:9], v[38:41]
	v_mfma_f32_16x16x32_f16 v[122:125], v[202:205], v[10:13], v[66:69]
	v_mfma_f32_16x16x32_f16 v[66:69], v[182:185], v[14:17], v[234:237]
	v_mfma_f32_16x16x32_f16 v[42:45], v[206:209], v[14:17], v[42:45]
	v_mfma_f32_16x16x32_f16 v[82:85], v[174:177], v[10:13], v[6:9]
	v_mfma_f32_16x16x32_f16 v[6:9], v[218:221], v[14:17], v[34:37]
	v_mfma_f32_16x16x32_f16 v[74:77], v[202:205], v[160:163], v[66:69]
	v_mfma_f32_16x16x32_f16 v[98:101], v[214:217], v[10:13], v[46:49]
	v_mfma_f32_16x16x32_f16 v[70:73], v[214:217], v[160:163], v[42:45]
	v_mfma_f32_16x16x32_f16 v[66:69], v[174:177], v[160:163], v[6:9]
	v_mfma_f32_16x16x32_f16 v[6:9], v[86:89], v[102:105], v[138:141]
	v_mfma_f32_16x16x32_f16 v[46:49], v[150:153], v[114:117], v[6:9]
	v_mfma_f32_16x16x32_f16 v[6:9], v[86:89], v[118:121], v[168:171]
	v_mfma_f32_16x16x32_f16 v[14:17], v[150:153], v[126:129], v[6:9]
	v_mfma_f32_16x16x32_f16 v[6:9], v[182:185], v[102:105], v[238:241]
	v_mfma_f32_16x16x32_f16 v[42:45], v[202:205], v[114:117], v[6:9]
	v_mfma_f32_16x16x32_f16 v[6:9], v[182:185], v[118:121], v[186:189]
	v_mfma_f32_16x16x32_f16 v[10:13], v[202:205], v[126:129], v[6:9]
	v_mfma_f32_16x16x32_f16 v[6:9], v[206:209], v[102:105], v[190:193]
	v_mfma_f32_16x16x32_f16 v[38:41], v[214:217], v[114:117], v[6:9]
	v_mfma_f32_16x16x32_f16 v[6:9], v[206:209], v[118:121], v[194:197]
	v_mfma_f32_16x16x32_f16 v[34:37], v[218:221], v[102:105], v[198:201]
	v_mfma_f32_16x16x32_f16 v[2:5], v[218:221], v[118:121], v[2:5]
	v_mfma_f32_16x16x32_f16 v[6:9], v[214:217], v[126:129], v[6:9]
	v_mfma_f32_16x16x32_f16 v[34:37], v[174:177], v[114:117], v[34:37]
	v_mfma_f32_16x16x32_f16 v[2:5], v[174:177], v[126:129], v[2:5]
	s_cmpk_gt_u32 s61, 0xff
	s_barrier
	s_cbranch_scc1 .LBB10_15
	s_barrier

	.amdhsa_kernel _Z14gemm256_kernelILi1ELi2048ELi512EEv8GemmArgs
		.amdhsa_group_segment_fixed_size 0
		.amdhsa_private_segment_fixed_size 0
		.amdhsa_kernarg_size 592
		.amdhsa_user_sgpr_count 2
		.amdhsa_user_sgpr_dispatch_ptr 0
		.amdhsa_user_sgpr_queue_ptr 0
		.amdhsa_user_sgpr_kernarg_segment_ptr 1
		.amdhsa_user_sgpr_dispatch_id 0
		.amdhsa_user_sgpr_kernarg_preload_length 0
		.amdhsa_user_sgpr_kernarg_preload_offset 0
		.amdhsa_user_sgpr_private_segment_size 0
		.amdhsa_uses_dynamic_stack 0
		.amdhsa_enable_private_segment 0
		.amdhsa_system_sgpr_workgroup_id_x 1
		.amdhsa_system_sgpr_workgroup_id_y 0
		.amdhsa_system_sgpr_workgroup_id_z 0
		.amdhsa_system_sgpr_workgroup_info 0
		.amdhsa_system_vgpr_workitem_id 0
		.amdhsa_next_free_vgpr 256
		.amdhsa_next_free_sgpr 86
		.amdhsa_accum_offset 256
		.amdhsa_reserve_vcc 1
		.amdhsa_float_round_mode_32 0
		.amdhsa_float_round_mode_16_64 0
		.amdhsa_float_denorm_mode_32 3
		.amdhsa_float_denorm_mode_16_64 3
		.amdhsa_dx10_clamp 1
		.amdhsa_ieee_mode 1
		.amdhsa_fp16_overflow 0
		.amdhsa_tg_split 0
		.amdhsa_exception_fp_ieee_invalid_op 0
		.amdhsa_exception_fp_denorm_src 0
		.amdhsa_exception_fp_ieee_div_zero 0
		.amdhsa_exception_fp_ieee_overflow 0
		.amdhsa_exception_fp_ieee_underflow 0
		.amdhsa_exception_fp_ieee_inexact 0
		.amdhsa_exception_int_div_zero 0
	.end_amdhsa_kernel

amdhsa.kernels:
  - .agpr_count:     0
    .args:
      - .offset:         0
        .size:           136
        .value_kind:     by_value
      - .actual_access:  read_only
        .address_space:  global
        .offset:         136
        .size:           8
        .value_kind:     global_buffer
      - .actual_access:  read_only
        .address_space:  global
        .offset:         144
        .size:           8
        .value_kind:     global_buffer
      - .actual_access:  read_only
        .address_space:  global
        .offset:         152
        .size:           8
        .value_kind:     global_buffer
      - .actual_access:  read_only
        .address_space:  global
        .offset:         160
        .size:           8
        .value_kind:     global_buffer
      - .actual_access:  write_only
        .address_space:  global
        .offset:         168
        .size:           8
        .value_kind:     global_buffer
      - .actual_access:  write_only
        .address_space:  global
        .offset:         176
        .size:           8
        .value_kind:     global_buffer
    .group_segment_fixed_size: 0
    .kernarg_segment_align: 8
    .kernarg_segment_size: 184
    .language:       OpenCL C
    .language_version:
      - 2
      - 0
    .max_flat_workgroup_size: 256
    .name:           _Z15prologue_kernel8PrepArgsPKfS1_PKiS1_PDF16_Pf
    .private_segment_fixed_size: 0
    .sgpr_count:     36
    .sgpr_spill_count: 0
    .symbol:         _Z15prologue_kernel8PrepArgsPKfS1_PKiS1_PDF16_Pf.kd
    .uniform_work_group_size: 1
    .uses_dynamic_stack: false
    .vgpr_count:     44
    .vgpr_spill_count: 0
    .wavefront_size: 64
  - .agpr_count:     0
    .args:
      - .actual_access:  read_only
        .address_space:  global
        .offset:         0
        .size:           8
        .value_kind:     global_buffer
      - .offset:         8
        .size:           4
        .value_kind:     by_value
      - .offset:         12
        .size:           4
        .value_kind:     by_value
      - .actual_access:  read_only
        .address_space:  global
        .offset:         16
        .size:           8
        .value_kind:     global_buffer
      - .actual_access:  read_only
        .address_space:  global
        .offset:         24
        .size:           8
        .value_kind:     global_buffer
      - .actual_access:  read_only
        .address_space:  global
        .offset:         32
        .size:           8
        .value_kind:     global_buffer
      - .actual_access:  read_only
        .address_space:  global
        .offset:         40
        .size:           8
        .value_kind:     global_buffer
      - .address_space:  global
        .offset:         48
        .size:           8
        .value_kind:     global_buffer
      - .actual_access:  write_only
        .address_space:  global
        .offset:         56
        .size:           8
        .value_kind:     global_buffer
    .group_segment_fixed_size: 0
    .kernarg_segment_align: 8
    .kernarg_segment_size: 64
    .language:       OpenCL C
    .language_version:
      - 2
      - 0
    .max_flat_workgroup_size: 256
    .name:           _Z18ffn2_finish_kernelPKfiiS0_PK15HIP_vector_typeIfLj2EES0_S0_PDF16_PS2_
    .private_segment_fixed_size: 0
    .sgpr_count:     20
    .sgpr_spill_count: 0
    .symbol:         _Z18ffn2_finish_kernelPKfiiS0_PK15HIP_vector_typeIfLj2EES0_S0_PDF16_PS2_.kd
    .uniform_work_group_size: 1
    .uses_dynamic_stack: false
    .vgpr_count:     52
    .vgpr_spill_count: 0
    .wavefront_size: 64
  - .agpr_count:     0
    .args:
      - .actual_access:  read_only
        .address_space:  global
        .offset:         0
        .size:           8
        .value_kind:     global_buffer
      - .actual_access:  read_only
        .address_space:  global
        .offset:         8
        .size:           8
        .value_kind:     global_buffer
      - .actual_access:  read_only
        .address_space:  global
        .offset:         16
        .size:           8
        .value_kind:     global_buffer
      - .actual_access:  write_only
        .address_space:  global
        .offset:         24
        .size:           8
        .value_kind:     global_buffer
      - .offset:         32
        .size:           4
        .value_kind:     by_value
    .group_segment_fixed_size: 0
    .kernarg_segment_align: 8
    .kernarg_segment_size: 36
    .language:       OpenCL C
    .language_version:
      - 2
      - 0
    .max_flat_workgroup_size: 1024
    .name:           _Z14attn_bh_kernelPKDF16_S0_S0_PDF16_i
    .private_segment_fixed_size: 0
    .sgpr_count:     38
    .sgpr_spill_count: 0
    .symbol:         _Z14attn_bh_kernelPKDF16_S0_S0_PDF16_i.kd
    .uniform_work_group_size: 1
    .uses_dynamic_stack: false
    .vgpr_count:     120
    .vgpr_spill_count: 0
    .wavefront_size: 64
  - .agpr_count:     0
    .args:
      - .offset:         0
        .size:           336
        .value_kind:     by_value
    .group_segment_fixed_size: 0
    .kernarg_segment_align: 8
    .kernarg_segment_size: 336
    .language:       OpenCL C
    .language_version:
      - 2
      - 0
    .max_flat_workgroup_size: 256
    .name:           _Z11gemm_kernelILi0EEv8GemmArgs
    .private_segment_fixed_size: 0
    .sgpr_count:     47
    .sgpr_spill_count: 0
    .symbol:         _Z11gemm_kernelILi0EEv8GemmArgs.kd
    .uniform_work_group_size: 1
    .uses_dynamic_stack: false
    .vgpr_count:     198
    .vgpr_spill_count: 0
    .wavefront_size: 64
  - .agpr_count:     0
    .args:
      - .offset:         0
        .size:           336
        .value_kind:     by_value
    .group_segment_fixed_size: 0
    .kernarg_segment_align: 8
    .kernarg_segment_size: 336
    .language:       OpenCL C
    .language_version:
      - 2
      - 0
    .max_flat_workgroup_size: 256
    .name:           _Z11gemm_kernelILi1EEv8GemmArgs
    .private_segment_fixed_size: 0
    .sgpr_count:     43
    .sgpr_spill_count: 0
    .symbol:         _Z11gemm_kernelILi1EEv8GemmArgs.kd
    .uniform_work_group_size: 1
    .uses_dynamic_stack: false
    .vgpr_count:     202
    .vgpr_spill_count: 0
    .wavefront_size: 64
  - .agpr_count:     0
    .args:
      - .offset:         0
        .size:           336
        .value_kind:     by_value
    .group_segment_fixed_size: 0
    .kernarg_segment_align: 8
    .kernarg_segment_size: 336
    .language:       OpenCL C
    .language_version:
      - 2
      - 0
    .max_flat_workgroup_size: 256
    .name:           _Z11gemm_kernelILi2EEv8GemmArgs
    .private_segment_fixed_size: 0
    .sgpr_count:     41
    .sgpr_spill_count: 0
    .symbol:         _Z11gemm_kernelILi2EEv8GemmArgs.kd
    .uniform_work_group_size: 1
    .uses_dynamic_stack: false
    .vgpr_count:     198
    .vgpr_spill_count: 0
    .wavefront_size: 64
  - .agpr_count:     0
    .args:
      - .offset:         0
        .size:           336
        .value_kind:     by_value
      - .offset:         336
        .size:           4
        .value_kind:     hidden_block_count_x
      - .offset:         340
        .size:           4
        .value_kind:     hidden_block_count_y
      - .offset:         344
        .size:           4
        .value_kind:     hidden_block_count_z
      - .offset:         348
        .size:           2
        .value_kind:     hidden_group_size_x
      - .offset:         350
        .size:           2
        .value_kind:     hidden_group_size_y
      - .offset:         352
        .size:           2
        .value_kind:     hidden_group_size_z
      - .offset:         354
        .size:           2
        .value_kind:     hidden_remainder_x
      - .offset:         356
        .size:           2
        .value_kind:     hidden_remainder_y
      - .offset:         358
        .size:           2
        .value_kind:     hidden_remainder_z
      - .offset:         376
        .size:           8
        .value_kind:     hidden_global_offset_x
      - .offset:         384
        .size:           8
        .value_kind:     hidden_global_offset_y
      - .offset:         392
        .size:           8
        .value_kind:     hidden_global_offset_z
      - .offset:         400
        .size:           2
        .value_kind:     hidden_grid_dims
      - .offset:         456
        .size:           4
        .value_kind:     hidden_dynamic_lds_size
    .group_segment_fixed_size: 0
    .kernarg_segment_align: 8
    .kernarg_segment_size: 592
    .language:       OpenCL C
    .language_version:
      - 2
      - 0
    .max_flat_workgroup_size: 512
    .name:           _Z14gemm256_kernelILi0ELi512ELi1536EEv8GemmArgs
    .private_segment_fixed_size: 0
    .sgpr_count:     94
    .sgpr_spill_count: 0
    .symbol:         _Z14gemm256_kernelILi0ELi512ELi1536EEv8GemmArgs.kd
    .uniform_work_group_size: 1
    .uses_dynamic_stack: false
    .vgpr_count:     256
    .vgpr_spill_count: 0
    .wavefront_size: 64
  - .agpr_count:     0
    .args:
      - .offset:         0
        .size:           336
        .value_kind:     by_value
      - .offset:         336
        .size:           4
        .value_kind:     hidden_block_count_x
      - .offset:         340
        .size:           4
        .value_kind:     hidden_block_count_y
      - .offset:         344
        .size:           4
        .value_kind:     hidden_block_count_z
      - .offset:         348
        .size:           2
        .value_kind:     hidden_group_size_x
      - .offset:         350
        .size:           2
        .value_kind:     hidden_group_size_y
      - .offset:         352
        .size:           2
        .value_kind:     hidden_group_size_z
      - .offset:         354
        .size:           2
        .value_kind:     hidden_remainder_x
      - .offset:         356
        .size:           2
        .value_kind:     hidden_remainder_y
      - .offset:         358
        .size:           2
        .value_kind:     hidden_remainder_z
      - .offset:         376
        .size:           8
        .value_kind:     hidden_global_offset_x
      - .offset:         384
        .size:           8
        .value_kind:     hidden_global_offset_y
      - .offset:         392
        .size:           8
        .value_kind:     hidden_global_offset_z
      - .offset:         400
        .size:           2
        .value_kind:     hidden_grid_dims
      - .offset:         456
        .size:           4
        .value_kind:     hidden_dynamic_lds_size
    .group_segment_fixed_size: 0
    .kernarg_segment_align: 8
    .kernarg_segment_size: 592
    .language:       OpenCL C
    .language_version:
      - 2
      - 0
    .max_flat_workgroup_size: 512
    .name:           _Z14gemm256_kernelILi0ELi512ELi1024EEv8GemmArgs
    .private_segment_fixed_size: 0
    .sgpr_count:     94
    .sgpr_spill_count: 0
    .symbol:         _Z14gemm256_kernelILi0ELi512ELi1024EEv8GemmArgs.kd
    .uniform_work_group_size: 1
    .uses_dynamic_stack: false
    .vgpr_count:     256
    .vgpr_spill_count: 0
    .wavefront_size: 64
  - .agpr_count:     0
    .args:
      - .offset:         0
        .size:           336
        .value_kind:     by_value
      - .offset:         336
        .size:           4
        .value_kind:     hidden_block_count_x
      - .offset:         340
        .size:           4
        .value_kind:     hidden_block_count_y
      - .offset:         344
        .size:           4
        .value_kind:     hidden_block_count_z
      - .offset:         348
        .size:           2
        .value_kind:     hidden_group_size_x
      - .offset:         350
        .size:           2
        .value_kind:     hidden_group_size_y
      - .offset:         352
        .size:           2
        .value_kind:     hidden_group_size_z
      - .offset:         354
        .size:           2
        .value_kind:     hidden_remainder_x
      - .offset:         356
        .size:           2
        .value_kind:     hidden_remainder_y
      - .offset:         358
        .size:           2
        .value_kind:     hidden_remainder_z
      - .offset:         376
        .size:           8
        .value_kind:     hidden_global_offset_x
      - .offset:         384
        .size:           8
        .value_kind:     hidden_global_offset_y
      - .offset:         392
        .size:           8
        .value_kind:     hidden_global_offset_z
      - .offset:         400
        .size:           2
        .value_kind:     hidden_grid_dims
      - .offset:         456
        .size:           4
        .value_kind:     hidden_dynamic_lds_size
    .group_segment_fixed_size: 0
    .kernarg_segment_align: 8
    .kernarg_segment_size: 592
    .language:       OpenCL C
    .language_version:
      - 2
      - 0
    .max_flat_workgroup_size: 512
    .name:           _Z14gemm256_kernelILi1ELi512ELi512EEv8GemmArgs
    .private_segment_fixed_size: 0
    .sgpr_count:     97
    .sgpr_spill_count: 0
    .symbol:         _Z14gemm256_kernelILi1ELi512ELi512EEv8GemmArgs.kd
    .uniform_work_group_size: 1
    .uses_dynamic_stack: false
    .vgpr_count:     256
    .vgpr_spill_count: 0
    .wavefront_size: 64
  - .agpr_count:     0
    .args:
      - .offset:         0
        .size:           336
        .value_kind:     by_value
      - .offset:         336
        .size:           4
        .value_kind:     hidden_block_count_x
      - .offset:         340
        .size:           4
        .value_kind:     hidden_block_count_y
      - .offset:         344
        .size:           4
        .value_kind:     hidden_block_count_z
      - .offset:         348
        .size:           2
        .value_kind:     hidden_group_size_x
      - .offset:         350
        .size:           2
        .value_kind:     hidden_group_size_y
      - .offset:         352
        .size:           2
        .value_kind:     hidden_group_size_z
      - .offset:         354
        .size:           2
        .value_kind:     hidden_remainder_x
      - .offset:         356
        .size:           2
        .value_kind:     hidden_remainder_y
      - .offset:         358
        .size:           2
        .value_kind:     hidden_remainder_z
      - .offset:         376
        .size:           8
        .value_kind:     hidden_global_offset_x
      - .offset:         384
        .size:           8
        .value_kind:     hidden_global_offset_y
      - .offset:         392
        .size:           8
        .value_kind:     hidden_global_offset_z
      - .offset:         400
        .size:           2
        .value_kind:     hidden_grid_dims
      - .offset:         456
        .size:           4
        .value_kind:     hidden_dynamic_lds_size
    .group_segment_fixed_size: 0
    .kernarg_segment_align: 8
    .kernarg_segment_size: 592
    .language:       OpenCL C
    .language_version:
      - 2
      - 0
    .max_flat_workgroup_size: 512
    .name:           _Z14gemm256_kernelILi2ELi512ELi2048EEv8GemmArgs
    .private_segment_fixed_size: 0
    .sgpr_count:     87
    .sgpr_spill_count: 0
    .symbol:         _Z14gemm256_kernelILi2ELi512ELi2048EEv8GemmArgs.kd
    .uniform_work_group_size: 1
    .uses_dynamic_stack: false
    .vgpr_count:     254
    .vgpr_spill_count: 0
    .wavefront_size: 64
  - .agpr_count:     0
    .args:
      - .offset:         0
        .size:           336
        .value_kind:     by_value
      - .offset:         336
        .size:           4
        .value_kind:     hidden_block_count_x
      - .offset:         340
        .size:           4
        .value_kind:     hidden_block_count_y
      - .offset:         344
        .size:           4
        .value_kind:     hidden_block_count_z
      - .offset:         348
        .size:           2
        .value_kind:     hidden_group_size_x
      - .offset:         350
        .size:           2
        .value_kind:     hidden_group_size_y
      - .offset:         352
        .size:           2
        .value_kind:     hidden_group_size_z
      - .offset:         354
        .size:           2
        .value_kind:     hidden_remainder_x
      - .offset:         356
        .size:           2
        .value_kind:     hidden_remainder_y
      - .offset:         358
        .size:           2
        .value_kind:     hidden_remainder_z
      - .offset:         376
        .size:           8
        .value_kind:     hidden_global_offset_x
      - .offset:         384
        .size:           8
        .value_kind:     hidden_global_offset_y
      - .offset:         392
        .size:           8
        .value_kind:     hidden_global_offset_z
      - .offset:         400
        .size:           2
        .value_kind:     hidden_grid_dims
      - .offset:         456
        .size:           4
        .value_kind:     hidden_dynamic_lds_size
    .group_segment_fixed_size: 0
    .kernarg_segment_align: 8
    .kernarg_segment_size: 592
    .language:       OpenCL C
    .language_version:
      - 2
      - 0
    .max_flat_workgroup_size: 512
    .name:           _Z14gemm256_kernelILi1ELi2048ELi512EEv8GemmArgs
    .private_segment_fixed_size: 0
    .sgpr_count:     92
    .sgpr_spill_count: 0
    .symbol:         _Z14gemm256_kernelILi1ELi2048ELi512EEv8GemmArgs.kd
    .uniform_work_group_size: 1
    .uses_dynamic_stack: false
    .vgpr_count:     256
    .vgpr_spill_count: 0
    .wavefront_size: 64
  - .agpr_count:     0
    .args:
      - .offset:         0
        .size:           336
        .value_kind:     by_value
    .group_segment_fixed_size: 0
    .kernarg_segment_align: 8
    .kernarg_segment_size: 336
    .language:       OpenCL C
    .language_version:
      - 2
      - 0
    .max_flat_workgroup_size: 256
    .name:           _Z11gemm_kernelILi4EEv8GemmArgs
    .private_segment_fixed_size: 0
    .sgpr_count:     42
    .sgpr_spill_count: 0
    .symbol:         _Z11gemm_kernelILi4EEv8GemmArgs.kd
    .uniform_work_group_size: 1
    .uses_dynamic_stack: false
    .vgpr_count:     196
    .vgpr_spill_count: 0
    .wavefront_size: 64
  - .agpr_count:     0
    .args:
      - .offset:         0
        .size:           336
        .value_kind:     by_value
    .group_segment_fixed_size: 0
    .kernarg_segment_align: 8
    .kernarg_segment_size: 336
    .language:       OpenCL C
    .language_version:
      - 2
      - 0
    .max_flat_workgroup_size: 256
    .name:           _Z11gemm_kernelILi3EEv8GemmArgs
    .private_segment_fixed_size: 0
    .sgpr_count:     38
    .sgpr_spill_count: 0
    .symbol:         _Z11gemm_kernelILi3EEv8GemmArgs.kd
    .uniform_work_group_size: 1
    .uses_dynamic_stack: false
    .vgpr_count:     200
    .vgpr_spill_count: 0
    .wavefront_size: 64
